# v68 + load segments at s_setprio 2 (above compute's 1)
# baseline (speedup 1.0000x reference)
.LBB0_286:
	s_lshl_b32 s10, s51, 19
	s_add_u32 s10, s20, s10
	s_addc_u32 s11, s21, 0
	s_and_b64 s[16:17], s[4:5], exec
	s_cselect_b32 s54, s11, s31
	s_cselect_b32 s55, s10, s30
	s_lshl_b32 s14, s50, 19
	s_add_u32 s16, s15, s14
	s_addc_u32 s17, s26, 0
	s_and_b64 s[36:37], s[4:5], exec
	s_cselect_b32 s56, s17, s23
	s_cselect_b32 s57, s16, s22
	s_add_i32 s60, 0, 0x10000
	v_add_u32_e32 v198, s60, v196
	s_add_i32 s62, 0, 0x14000
	v_add_u32_e32 v199, s62, v196
	ds_read_b128 v[160:163], v198
	ds_read_b128 v[152:155], v198 offset:1024
	ds_read_b128 v[156:159], v198 offset:2048
	ds_read_b128 v[148:151], v198 offset:3072
	ds_read_b128 v[144:147], v199
	ds_read_b128 v[136:139], v199 offset:1024
	ds_read_b128 v[140:143], v199 offset:2048
	ds_read_b128 v[132:135], v199 offset:3072
	s_add_u32 s36, s30, 0x40080
	s_addc_u32 s37, s31, 0
	s_add_i32 s58, s41, 0xc000
	v_lshl_add_u64 v[174:175], s[36:37], 0, v[168:169]
	s_mov_b32 m0, s58
	s_add_i32 s59, s41, 0xe000
	ds_read_b128 v[178:181], v197
	ds_read_b128 v[182:185], v197 offset:1024
	ds_read_b128 v[190:193], v197 offset:2048
	ds_read_b128 v[200:203], v197 offset:3072
	ds_read_b128 v[204:207], v197 offset:4096
	ds_read_b128 v[208:211], v197 offset:5120
	ds_read_b128 v[212:215], v197 offset:6144
	ds_read_b128 v[216:219], v197 offset:7168
	global_load_lds_dwordx4 v[174:175], off
	v_lshl_add_u64 v[174:175], s[36:37], 0, v[166:167]
	s_mov_b32 m0, s59
	s_nop 0
	global_load_lds_dwordx4 v[174:175], off
	s_waitcnt vmcnt(8)
	s_waitcnt lgkmcnt(0)
	s_barrier
	v_mfma_f32_16x16x32_bf16 v[128:131], v[160:163], v[178:181], 0
	s_setprio 1
	v_mfma_f32_16x16x32_bf16 v[124:127], v[156:159], v[178:181], 0
	v_mfma_f32_16x16x32_bf16 v[116:119], v[156:159], v[190:193], 0
	v_mfma_f32_16x16x32_bf16 v[120:123], v[160:163], v[190:193], 0
	v_mfma_f32_16x16x32_bf16 v[112:115], v[160:163], v[204:207], 0
	v_mfma_f32_16x16x32_bf16 v[108:111], v[156:159], v[204:207], 0
	v_mfma_f32_16x16x32_bf16 v[100:103], v[156:159], v[212:215], 0
	v_mfma_f32_16x16x32_bf16 v[104:107], v[160:163], v[212:215], 0
	s_nop 0
	v_mfma_f32_16x16x32_bf16 v[128:131], v[152:155], v[182:185], v[128:131]
	v_mfma_f32_16x16x32_bf16 v[124:127], v[148:151], v[182:185], v[124:127]
	v_mfma_f32_16x16x32_bf16 v[116:119], v[148:151], v[200:203], v[116:119]
	v_mfma_f32_16x16x32_bf16 v[120:123], v[152:155], v[200:203], v[120:123]
	v_mfma_f32_16x16x32_bf16 v[112:115], v[152:155], v[208:211], v[112:115]
	v_mfma_f32_16x16x32_bf16 v[108:111], v[148:151], v[208:211], v[108:111]
	v_mfma_f32_16x16x32_bf16 v[100:103], v[148:151], v[216:219], v[100:103]
	v_mfma_f32_16x16x32_bf16 v[104:107], v[152:155], v[216:219], v[104:107]
	s_setprio 2
	s_setprio 1
	v_mfma_f32_16x16x32_bf16 v[96:99], v[144:147], v[178:181], 0
	v_mfma_f32_16x16x32_bf16 v[92:95], v[140:143], v[178:181], 0
	v_mfma_f32_16x16x32_bf16 v[84:87], v[140:143], v[190:193], 0
	v_mfma_f32_16x16x32_bf16 v[88:91], v[144:147], v[190:193], 0
	v_mfma_f32_16x16x32_bf16 v[80:83], v[144:147], v[204:207], 0
	v_mfma_f32_16x16x32_bf16 v[76:79], v[140:143], v[204:207], 0
	v_mfma_f32_16x16x32_bf16 v[68:71], v[140:143], v[212:215], 0
	v_mfma_f32_16x16x32_bf16 v[72:75], v[144:147], v[212:215], 0
	s_nop 0
	v_mfma_f32_16x16x32_bf16 v[96:99], v[136:139], v[182:185], v[96:99]
	v_mfma_f32_16x16x32_bf16 v[92:95], v[132:135], v[182:185], v[92:95]
	v_mfma_f32_16x16x32_bf16 v[84:87], v[132:135], v[200:203], v[84:87]
	v_mfma_f32_16x16x32_bf16 v[88:91], v[136:139], v[200:203], v[88:91]
	v_mfma_f32_16x16x32_bf16 v[80:83], v[136:139], v[208:211], v[80:83]
	v_mfma_f32_16x16x32_bf16 v[76:79], v[132:135], v[208:211], v[76:79]
	v_mfma_f32_16x16x32_bf16 v[68:71], v[132:135], v[216:219], v[68:71]
	v_mfma_f32_16x16x32_bf16 v[72:75], v[136:139], v[216:219], v[72:75]
	s_barrier
	s_setprio 2
	v_lshl_add_u64 v[174:175], s[22:23], 0, v[34:35]
	s_add_i32 s60, s60, s40
	v_lshl_add_u64 v[190:191], v[174:175], 0, s[28:29]
	s_mov_b32 m0, s60
	s_add_i32 s61, s60, 0x2000
	ds_read_b128 v[178:181], v197 offset:16384
	ds_read_b128 v[182:185], v197 offset:17408
	ds_read_b128 v[200:203], v197 offset:18432
	ds_read_b128 v[204:207], v197 offset:19456
	ds_read_b128 v[208:211], v197 offset:20480
	ds_read_b128 v[212:215], v197 offset:21504
	ds_read_b128 v[216:219], v197 offset:22528
	ds_read_b128 v[222:225], v197 offset:23552
	global_load_lds_dwordx4 v[190:191], off
	v_lshl_add_u64 v[190:191], s[22:23], 0, v[164:165]
	s_add_u32 s36, s22, 0x40100
	v_lshl_add_u64 v[192:193], v[190:191], 0, s[28:29]
	s_mov_b32 m0, s61
	s_addc_u32 s37, s23, 0
	s_add_i32 s62, s62, s40
	global_load_lds_dwordx4 v[192:193], off
	v_lshl_add_u64 v[192:193], s[36:37], 0, v[34:35]
	s_mov_b32 m0, s62
	s_add_i32 s63, s62, 0x2000
	global_load_lds_dwordx4 v[192:193], off
	v_lshl_add_u64 v[192:193], s[36:37], 0, v[164:165]
	s_mov_b32 m0, s63
	s_nop 0
	global_load_lds_dwordx4 v[192:193], off
	v_lshl_add_u64 v[192:193], s[30:31], 0, v[168:169]
	v_lshl_add_u64 v[194:195], v[192:193], 0, s[28:29]
	s_mov_b32 m0, s41
	s_nop 0
	global_load_lds_dwordx4 v[194:195], off
	v_lshl_add_u64 v[194:195], s[30:31], 0, v[166:167]
	v_lshl_add_u64 v[226:227], v[194:195], 0, s[28:29]
	s_mov_b32 m0, s42
	s_nop 0
	global_load_lds_dwordx4 v[226:227], off
	s_waitcnt vmcnt(8)
	s_waitcnt lgkmcnt(0)
	s_barrier
	v_mfma_f32_16x16x32_bf16 v[64:67], v[160:163], v[178:181], 0
	s_setprio 1
	v_mfma_f32_16x16x32_bf16 v[60:63], v[156:159], v[178:181], 0
	v_mfma_f32_16x16x32_bf16 v[52:55], v[156:159], v[200:203], 0
	v_mfma_f32_16x16x32_bf16 v[56:59], v[160:163], v[200:203], 0
	v_mfma_f32_16x16x32_bf16 v[48:51], v[160:163], v[208:211], 0
	v_mfma_f32_16x16x32_bf16 v[44:47], v[156:159], v[208:211], 0
	v_mfma_f32_16x16x32_bf16 v[36:39], v[156:159], v[216:219], 0
	v_mfma_f32_16x16x32_bf16 v[40:43], v[160:163], v[216:219], 0
	s_nop 0
	v_mfma_f32_16x16x32_bf16 v[64:67], v[152:155], v[182:185], v[64:67]
	v_mfma_f32_16x16x32_bf16 v[60:63], v[148:151], v[182:185], v[60:63]
	v_mfma_f32_16x16x32_bf16 v[52:55], v[148:151], v[204:207], v[52:55]
	v_mfma_f32_16x16x32_bf16 v[56:59], v[152:155], v[204:207], v[56:59]
	v_mfma_f32_16x16x32_bf16 v[48:51], v[152:155], v[212:215], v[48:51]
	v_mfma_f32_16x16x32_bf16 v[44:47], v[148:151], v[212:215], v[44:47]
	v_mfma_f32_16x16x32_bf16 v[36:39], v[148:151], v[222:225], v[36:39]
	v_mfma_f32_16x16x32_bf16 v[40:43], v[152:155], v[222:225], v[40:43]
	s_setprio 2
	s_setprio 1
	v_mfma_f32_16x16x32_bf16 v[30:33], v[144:147], v[178:181], 0
	v_mfma_f32_16x16x32_bf16 v[26:29], v[140:143], v[178:181], 0
	v_mfma_f32_16x16x32_bf16 v[18:21], v[140:143], v[200:203], 0
	v_mfma_f32_16x16x32_bf16 v[22:25], v[144:147], v[200:203], 0
	v_mfma_f32_16x16x32_bf16 v[14:17], v[144:147], v[208:211], 0
	v_mfma_f32_16x16x32_bf16 v[10:13], v[140:143], v[208:211], 0
	v_mfma_f32_16x16x32_bf16 v[2:5], v[140:143], v[216:219], 0
	v_mfma_f32_16x16x32_bf16 v[6:9], v[144:147], v[216:219], 0
	s_nop 0
	v_mfma_f32_16x16x32_bf16 v[30:33], v[136:139], v[182:185], v[30:33]
	v_mfma_f32_16x16x32_bf16 v[26:29], v[132:135], v[182:185], v[26:29]
	v_mfma_f32_16x16x32_bf16 v[18:21], v[132:135], v[204:207], v[18:21]
	v_mfma_f32_16x16x32_bf16 v[22:25], v[136:139], v[204:207], v[22:25]
	v_mfma_f32_16x16x32_bf16 v[14:17], v[136:139], v[212:215], v[14:17]
	v_mfma_f32_16x16x32_bf16 v[10:13], v[132:135], v[212:215], v[10:13]
	v_mfma_f32_16x16x32_bf16 v[2:5], v[132:135], v[222:225], v[2:5]
	v_mfma_f32_16x16x32_bf16 v[6:9], v[136:139], v[222:225], v[6:9]
	s_barrier
	s_setprio 2
	s_add_i32 s64, 0, 0x18000
	s_add_i32 s66, 0, 0x1c000
	v_add_u32_e32 v132, s64, v196
	v_add_u32_e32 v133, s66, v196
	ds_read_b128 v[134:137], v132
	ds_read_b128 v[138:141], v132 offset:1024
	ds_read_b128 v[142:145], v132 offset:2048
	ds_read_b128 v[146:149], v132 offset:3072
	ds_read_b128 v[150:153], v133
	ds_read_b128 v[154:157], v133 offset:1024
	ds_read_b128 v[158:161], v133 offset:2048
	ds_read_b128 v[178:181], v133 offset:3072
	s_add_u32 s36, s30, 0x40100
	s_addc_u32 s37, s31, 0
	s_mov_b32 m0, s43
	v_lshl_add_u64 v[162:163], s[36:37], 0, v[168:169]
	ds_read_b128 v[182:185], v197 offset:32768
	ds_read_b128 v[200:203], v197 offset:33792
	ds_read_b128 v[204:207], v197 offset:34816
	ds_read_b128 v[208:211], v197 offset:35840
	ds_read_b128 v[212:215], v197 offset:36864
	ds_read_b128 v[216:219], v197 offset:37888
	ds_read_b128 v[222:225], v197 offset:38912
	ds_read_b128 v[226:229], v197 offset:39936
	global_load_lds_dwordx4 v[162:163], off
	v_lshl_add_u64 v[162:163], s[36:37], 0, v[166:167]
	s_mov_b32 m0, s44
	s_nop 0
	global_load_lds_dwordx4 v[162:163], off
	s_waitcnt vmcnt(8)
	s_waitcnt lgkmcnt(0)
	s_barrier
	v_mfma_f32_16x16x32_bf16 v[128:131], v[134:137], v[182:185], v[128:131]
	s_setprio 1
	v_mfma_f32_16x16x32_bf16 v[124:127], v[142:145], v[182:185], v[124:127]
	v_mfma_f32_16x16x32_bf16 v[116:119], v[142:145], v[204:207], v[116:119]
	v_mfma_f32_16x16x32_bf16 v[120:123], v[134:137], v[204:207], v[120:123]
	v_mfma_f32_16x16x32_bf16 v[112:115], v[134:137], v[212:215], v[112:115]
	v_mfma_f32_16x16x32_bf16 v[108:111], v[142:145], v[212:215], v[108:111]
	v_mfma_f32_16x16x32_bf16 v[100:103], v[142:145], v[222:225], v[100:103]
	v_mfma_f32_16x16x32_bf16 v[104:107], v[134:137], v[222:225], v[104:107]
	v_mfma_f32_16x16x32_bf16 v[128:131], v[138:141], v[200:203], v[128:131]
	v_mfma_f32_16x16x32_bf16 v[124:127], v[146:149], v[200:203], v[124:127]
	v_mfma_f32_16x16x32_bf16 v[116:119], v[146:149], v[208:211], v[116:119]
	v_mfma_f32_16x16x32_bf16 v[120:123], v[138:141], v[208:211], v[120:123]
	v_mfma_f32_16x16x32_bf16 v[112:115], v[138:141], v[216:219], v[112:115]
	v_mfma_f32_16x16x32_bf16 v[108:111], v[146:149], v[216:219], v[108:111]
	v_mfma_f32_16x16x32_bf16 v[100:103], v[146:149], v[226:229], v[100:103]
	v_mfma_f32_16x16x32_bf16 v[104:107], v[138:141], v[226:229], v[104:107]
	s_setprio 2
	s_setprio 1
	v_mfma_f32_16x16x32_bf16 v[96:99], v[150:153], v[182:185], v[96:99]
	v_mfma_f32_16x16x32_bf16 v[92:95], v[158:161], v[182:185], v[92:95]
	v_mfma_f32_16x16x32_bf16 v[84:87], v[158:161], v[204:207], v[84:87]
	v_mfma_f32_16x16x32_bf16 v[88:91], v[150:153], v[204:207], v[88:91]
	v_mfma_f32_16x16x32_bf16 v[80:83], v[150:153], v[212:215], v[80:83]
	v_mfma_f32_16x16x32_bf16 v[76:79], v[158:161], v[212:215], v[76:79]
	v_mfma_f32_16x16x32_bf16 v[68:71], v[158:161], v[222:225], v[68:71]
	v_mfma_f32_16x16x32_bf16 v[72:75], v[150:153], v[222:225], v[72:75]
	v_mfma_f32_16x16x32_bf16 v[96:99], v[154:157], v[200:203], v[96:99]
	v_mfma_f32_16x16x32_bf16 v[92:95], v[178:181], v[200:203], v[92:95]
	v_mfma_f32_16x16x32_bf16 v[84:87], v[178:181], v[208:211], v[84:87]
	v_mfma_f32_16x16x32_bf16 v[88:91], v[154:157], v[208:211], v[88:91]
	v_mfma_f32_16x16x32_bf16 v[80:83], v[154:157], v[216:219], v[80:83]
	v_mfma_f32_16x16x32_bf16 v[76:79], v[178:181], v[216:219], v[76:79]
	v_mfma_f32_16x16x32_bf16 v[68:71], v[178:181], v[226:229], v[68:71]
	v_mfma_f32_16x16x32_bf16 v[72:75], v[154:157], v[226:229], v[72:75]
	s_barrier
	s_setprio 2
	s_add_i32 s64, s64, s40
	s_mov_b64 s[24:25], 0x180
	s_add_i32 s65, s64, 0x2000
	v_lshl_add_u64 v[162:163], v[174:175], 0, s[24:25]
	s_mov_b32 m0, s64
	s_add_u32 s36, s22, 0x40180
	ds_read_b128 v[182:185], v197 offset:49152
	ds_read_b128 v[200:203], v197 offset:50176
	ds_read_b128 v[204:207], v197 offset:51200
	ds_read_b128 v[208:211], v197 offset:52224
	ds_read_b128 v[212:215], v197 offset:53248
	ds_read_b128 v[216:219], v197 offset:54272
	ds_read_b128 v[222:225], v197 offset:55296
	ds_read_b128 v[226:229], v197 offset:56320
	global_load_lds_dwordx4 v[162:163], off
	v_lshl_add_u64 v[162:163], v[190:191], 0, s[24:25]
	s_mov_b32 m0, s65
	s_addc_u32 s37, s23, 0
	s_add_i32 s66, s66, s40
	global_load_lds_dwordx4 v[162:163], off
	v_lshl_add_u64 v[162:163], s[36:37], 0, v[34:35]
	s_mov_b32 m0, s66
	s_add_i32 s67, s66, 0x2000
	global_load_lds_dwordx4 v[162:163], off
	v_lshl_add_u64 v[162:163], s[36:37], 0, v[164:165]
	s_mov_b32 m0, s67
	s_nop 0
	global_load_lds_dwordx4 v[162:163], off
	v_lshl_add_u64 v[162:163], v[192:193], 0, s[24:25]
	s_mov_b32 m0, s47
	s_nop 0
	global_load_lds_dwordx4 v[162:163], off
	v_lshl_add_u64 v[162:163], v[194:195], 0, s[24:25]
	s_mov_b32 m0, s48
	s_nop 0
	global_load_lds_dwordx4 v[162:163], off
	s_waitcnt vmcnt(8)
	s_waitcnt lgkmcnt(0)
	s_barrier
	v_mfma_f32_16x16x32_bf16 v[64:67], v[134:137], v[182:185], v[64:67]
	s_setprio 1
	v_mfma_f32_16x16x32_bf16 v[60:63], v[142:145], v[182:185], v[60:63]
	v_mfma_f32_16x16x32_bf16 v[52:55], v[142:145], v[204:207], v[52:55]
	v_mfma_f32_16x16x32_bf16 v[56:59], v[134:137], v[204:207], v[56:59]
	v_mfma_f32_16x16x32_bf16 v[48:51], v[134:137], v[212:215], v[48:51]
	v_mfma_f32_16x16x32_bf16 v[44:47], v[142:145], v[212:215], v[44:47]
	v_mfma_f32_16x16x32_bf16 v[36:39], v[142:145], v[222:225], v[36:39]
	v_mfma_f32_16x16x32_bf16 v[40:43], v[134:137], v[222:225], v[40:43]
	v_mfma_f32_16x16x32_bf16 v[64:67], v[138:141], v[200:203], v[64:67]
	v_mfma_f32_16x16x32_bf16 v[60:63], v[146:149], v[200:203], v[60:63]
	v_mfma_f32_16x16x32_bf16 v[52:55], v[146:149], v[208:211], v[52:55]
	v_mfma_f32_16x16x32_bf16 v[56:59], v[138:141], v[208:211], v[56:59]
	v_mfma_f32_16x16x32_bf16 v[48:51], v[138:141], v[216:219], v[48:51]
	v_mfma_f32_16x16x32_bf16 v[44:47], v[146:149], v[216:219], v[44:47]
	v_mfma_f32_16x16x32_bf16 v[36:39], v[146:149], v[226:229], v[36:39]
	v_mfma_f32_16x16x32_bf16 v[40:43], v[138:141], v[226:229], v[40:43]
	s_setprio 2
	s_setprio 1
	v_mfma_f32_16x16x32_bf16 v[30:33], v[150:153], v[182:185], v[30:33]
	v_mfma_f32_16x16x32_bf16 v[26:29], v[158:161], v[182:185], v[26:29]
	v_mfma_f32_16x16x32_bf16 v[18:21], v[158:161], v[204:207], v[18:21]
	v_mfma_f32_16x16x32_bf16 v[22:25], v[150:153], v[204:207], v[22:25]
	v_mfma_f32_16x16x32_bf16 v[14:17], v[150:153], v[212:215], v[14:17]
	v_mfma_f32_16x16x32_bf16 v[10:13], v[158:161], v[212:215], v[10:13]
	v_mfma_f32_16x16x32_bf16 v[2:5], v[158:161], v[222:225], v[2:5]
	v_mfma_f32_16x16x32_bf16 v[6:9], v[150:153], v[222:225], v[6:9]
	v_mfma_f32_16x16x32_bf16 v[30:33], v[154:157], v[200:203], v[30:33]
	v_mfma_f32_16x16x32_bf16 v[26:29], v[178:181], v[200:203], v[26:29]
	v_mfma_f32_16x16x32_bf16 v[18:21], v[178:181], v[208:211], v[18:21]
	v_mfma_f32_16x16x32_bf16 v[22:25], v[154:157], v[208:211], v[22:25]
	v_mfma_f32_16x16x32_bf16 v[14:17], v[154:157], v[216:219], v[14:17]
	v_mfma_f32_16x16x32_bf16 v[10:13], v[178:181], v[216:219], v[10:13]
	v_mfma_f32_16x16x32_bf16 v[2:5], v[178:181], v[226:229], v[2:5]
	v_mfma_f32_16x16x32_bf16 v[6:9], v[154:157], v[226:229], v[6:9]
	s_barrier
	s_setprio 2
	s_add_u32 s30, s30, 0x40180
	s_addc_u32 s31, s31, 0
	s_add_u32 s68, s22, 0x200
	s_addc_u32 s69, s23, 0
	s_mov_b32 s70, 0
.LBB0_287:
	ds_read_b128 v[134:137], v198
	ds_read_b128 v[138:141], v198 offset:1024
	ds_read_b128 v[142:145], v198 offset:2048
	ds_read_b128 v[146:149], v198 offset:3072
	ds_read_b128 v[150:153], v199
	ds_read_b128 v[154:157], v199 offset:1024
	ds_read_b128 v[158:161], v199 offset:2048
	ds_read_b128 v[178:181], v199 offset:3072
	s_add_u32 s14, s30, 0xfffc0080
	s_addc_u32 s22, s31, -1
	s_cmp_eq_u32 s70, 12
	s_cselect_b32 s37, s54, s22
	s_cselect_b32 s36, s55, s14
	s_cselect_b32 s23, s56, s69
	s_cselect_b32 s22, s57, s68
	s_mov_b32 m0, s58
	v_lshl_add_u64 v[162:163], s[30:31], 0, v[170:171]
	ds_read_b128 v[182:185], v197
	ds_read_b128 v[190:193], v197 offset:1024
	ds_read_b128 v[200:203], v197 offset:2048
	ds_read_b128 v[204:207], v197 offset:3072
	ds_read_b128 v[208:211], v197 offset:4096
	ds_read_b128 v[212:215], v197 offset:5120
	ds_read_b128 v[216:219], v197 offset:6144
	ds_read_b128 v[222:225], v197 offset:7168
	global_load_lds_dwordx4 v[162:163], off
	v_lshl_add_u64 v[162:163], s[30:31], 0, v[172:173]
	s_mov_b32 m0, s59
	s_nop 0
	global_load_lds_dwordx4 v[162:163], off
	s_waitcnt vmcnt(8)
	s_waitcnt lgkmcnt(0)
	s_barrier
	v_mfma_f32_16x16x32_bf16 v[128:131], v[134:137], v[182:185], v[128:131]
	s_setprio 1
	v_mfma_f32_16x16x32_bf16 v[124:127], v[142:145], v[182:185], v[124:127]
	v_mfma_f32_16x16x32_bf16 v[116:119], v[142:145], v[200:203], v[116:119]
	v_mfma_f32_16x16x32_bf16 v[120:123], v[134:137], v[200:203], v[120:123]
	v_mfma_f32_16x16x32_bf16 v[112:115], v[134:137], v[208:211], v[112:115]
	v_mfma_f32_16x16x32_bf16 v[108:111], v[142:145], v[208:211], v[108:111]
	v_mfma_f32_16x16x32_bf16 v[100:103], v[142:145], v[216:219], v[100:103]
	v_mfma_f32_16x16x32_bf16 v[104:107], v[134:137], v[216:219], v[104:107]
	v_mfma_f32_16x16x32_bf16 v[128:131], v[138:141], v[190:193], v[128:131]
	v_mfma_f32_16x16x32_bf16 v[124:127], v[146:149], v[190:193], v[124:127]
	v_mfma_f32_16x16x32_bf16 v[116:119], v[146:149], v[204:207], v[116:119]
	v_mfma_f32_16x16x32_bf16 v[120:123], v[138:141], v[204:207], v[120:123]
	v_mfma_f32_16x16x32_bf16 v[112:115], v[138:141], v[212:215], v[112:115]
	v_mfma_f32_16x16x32_bf16 v[108:111], v[146:149], v[212:215], v[108:111]
	v_mfma_f32_16x16x32_bf16 v[100:103], v[146:149], v[222:225], v[100:103]
	v_mfma_f32_16x16x32_bf16 v[104:107], v[138:141], v[222:225], v[104:107]
	s_setprio 2
	s_setprio 1
	v_mfma_f32_16x16x32_bf16 v[96:99], v[150:153], v[182:185], v[96:99]
	v_mfma_f32_16x16x32_bf16 v[92:95], v[158:161], v[182:185], v[92:95]
	v_mfma_f32_16x16x32_bf16 v[84:87], v[158:161], v[200:203], v[84:87]
	v_mfma_f32_16x16x32_bf16 v[88:91], v[150:153], v[200:203], v[88:91]
	v_mfma_f32_16x16x32_bf16 v[80:83], v[150:153], v[208:211], v[80:83]
	v_mfma_f32_16x16x32_bf16 v[76:79], v[158:161], v[208:211], v[76:79]
	v_mfma_f32_16x16x32_bf16 v[68:71], v[158:161], v[216:219], v[68:71]
	v_mfma_f32_16x16x32_bf16 v[72:75], v[150:153], v[216:219], v[72:75]
	v_mfma_f32_16x16x32_bf16 v[96:99], v[154:157], v[190:193], v[96:99]
	v_mfma_f32_16x16x32_bf16 v[92:95], v[178:181], v[190:193], v[92:95]
	v_mfma_f32_16x16x32_bf16 v[84:87], v[178:181], v[204:207], v[84:87]
	v_mfma_f32_16x16x32_bf16 v[88:91], v[154:157], v[204:207], v[88:91]
	v_mfma_f32_16x16x32_bf16 v[80:83], v[154:157], v[212:215], v[80:83]
	v_mfma_f32_16x16x32_bf16 v[76:79], v[178:181], v[212:215], v[76:79]
	v_mfma_f32_16x16x32_bf16 v[68:71], v[178:181], v[222:225], v[68:71]
	v_mfma_f32_16x16x32_bf16 v[72:75], v[154:157], v[222:225], v[72:75]
	s_barrier
	s_setprio 2
	s_mov_b32 m0, s60
	v_lshl_add_u64 v[162:163], s[22:23], 0, v[34:35]
	s_add_u32 s72, s22, 0x40000
	ds_read_b128 v[182:185], v197 offset:16384
	ds_read_b128 v[190:193], v197 offset:17408
	ds_read_b128 v[200:203], v197 offset:18432
	ds_read_b128 v[204:207], v197 offset:19456
	ds_read_b128 v[208:211], v197 offset:20480
	ds_read_b128 v[212:215], v197 offset:21504
	ds_read_b128 v[216:219], v197 offset:22528
	ds_read_b128 v[222:225], v197 offset:23552
	global_load_lds_dwordx4 v[162:163], off
	v_lshl_add_u64 v[174:175], s[22:23], 0, v[164:165]
	s_mov_b32 m0, s61
	s_addc_u32 s73, s23, 0
	global_load_lds_dwordx4 v[174:175], off
	v_lshl_add_u64 v[194:195], s[72:73], 0, v[34:35]
	s_mov_b32 m0, s62
	v_lshl_add_u64 v[226:227], s[36:37], 0, v[166:167]
	global_load_lds_dwordx4 v[194:195], off
	v_lshl_add_u64 v[194:195], s[72:73], 0, v[164:165]
	s_mov_b32 m0, s63
	s_nop 0
	global_load_lds_dwordx4 v[194:195], off
	v_lshl_add_u64 v[194:195], s[36:37], 0, v[168:169]
	s_mov_b32 m0, s41
	s_nop 0
	global_load_lds_dwordx4 v[194:195], off
	s_mov_b32 m0, s42
	s_nop 0
	global_load_lds_dwordx4 v[226:227], off
	s_waitcnt vmcnt(8)
	s_waitcnt lgkmcnt(0)
	s_barrier
	v_mfma_f32_16x16x32_bf16 v[64:67], v[134:137], v[182:185], v[64:67]
	s_setprio 1
	v_mfma_f32_16x16x32_bf16 v[60:63], v[142:145], v[182:185], v[60:63]
	v_mfma_f32_16x16x32_bf16 v[52:55], v[142:145], v[200:203], v[52:55]
	v_mfma_f32_16x16x32_bf16 v[56:59], v[134:137], v[200:203], v[56:59]
	v_mfma_f32_16x16x32_bf16 v[48:51], v[134:137], v[208:211], v[48:51]
	v_mfma_f32_16x16x32_bf16 v[44:47], v[142:145], v[208:211], v[44:47]
	v_mfma_f32_16x16x32_bf16 v[36:39], v[142:145], v[216:219], v[36:39]
	v_mfma_f32_16x16x32_bf16 v[40:43], v[134:137], v[216:219], v[40:43]
	v_mfma_f32_16x16x32_bf16 v[64:67], v[138:141], v[190:193], v[64:67]
	v_mfma_f32_16x16x32_bf16 v[60:63], v[146:149], v[190:193], v[60:63]
	v_mfma_f32_16x16x32_bf16 v[52:55], v[146:149], v[204:207], v[52:55]
	v_mfma_f32_16x16x32_bf16 v[56:59], v[138:141], v[204:207], v[56:59]
	v_mfma_f32_16x16x32_bf16 v[48:51], v[138:141], v[212:215], v[48:51]
	v_mfma_f32_16x16x32_bf16 v[44:47], v[146:149], v[212:215], v[44:47]
	v_mfma_f32_16x16x32_bf16 v[36:39], v[146:149], v[222:225], v[36:39]
	v_mfma_f32_16x16x32_bf16 v[40:43], v[138:141], v[222:225], v[40:43]
	s_setprio 2
	s_setprio 1
	v_mfma_f32_16x16x32_bf16 v[30:33], v[150:153], v[182:185], v[30:33]
	v_mfma_f32_16x16x32_bf16 v[26:29], v[158:161], v[182:185], v[26:29]
	v_mfma_f32_16x16x32_bf16 v[18:21], v[158:161], v[200:203], v[18:21]
	v_mfma_f32_16x16x32_bf16 v[22:25], v[150:153], v[200:203], v[22:25]
	v_mfma_f32_16x16x32_bf16 v[14:17], v[150:153], v[208:211], v[14:17]
	v_mfma_f32_16x16x32_bf16 v[10:13], v[158:161], v[208:211], v[10:13]
	v_mfma_f32_16x16x32_bf16 v[2:5], v[158:161], v[216:219], v[2:5]
	v_mfma_f32_16x16x32_bf16 v[6:9], v[150:153], v[216:219], v[6:9]
	v_mfma_f32_16x16x32_bf16 v[30:33], v[154:157], v[190:193], v[30:33]
	v_mfma_f32_16x16x32_bf16 v[26:29], v[178:181], v[190:193], v[26:29]
	v_mfma_f32_16x16x32_bf16 v[18:21], v[178:181], v[204:207], v[18:21]
	v_mfma_f32_16x16x32_bf16 v[22:25], v[154:157], v[204:207], v[22:25]
	v_mfma_f32_16x16x32_bf16 v[14:17], v[154:157], v[212:215], v[14:17]
	v_mfma_f32_16x16x32_bf16 v[10:13], v[178:181], v[212:215], v[10:13]
	v_mfma_f32_16x16x32_bf16 v[2:5], v[178:181], v[222:225], v[2:5]
	v_mfma_f32_16x16x32_bf16 v[6:9], v[154:157], v[222:225], v[6:9]
	s_barrier
	s_setprio 2
	ds_read_b128 v[134:137], v132
	ds_read_b128 v[138:141], v132 offset:1024
	ds_read_b128 v[142:145], v132 offset:2048
	ds_read_b128 v[146:149], v132 offset:3072
	ds_read_b128 v[150:153], v133
	ds_read_b128 v[154:157], v133 offset:1024
	ds_read_b128 v[158:161], v133 offset:2048
	ds_read_b128 v[178:181], v133 offset:3072
	s_add_u32 s36, s36, 0x40000
	s_addc_u32 s37, s37, 0
	s_mov_b32 m0, s43
	v_lshl_add_u64 v[228:229], s[36:37], 0, v[168:169]
	ds_read_b128 v[182:185], v197 offset:32768
	ds_read_b128 v[190:193], v197 offset:33792
	ds_read_b128 v[200:203], v197 offset:34816
	ds_read_b128 v[204:207], v197 offset:35840
	ds_read_b128 v[208:211], v197 offset:36864
	ds_read_b128 v[212:215], v197 offset:37888
	ds_read_b128 v[216:219], v197 offset:38912
	ds_read_b128 v[222:225], v197 offset:39936
	global_load_lds_dwordx4 v[228:229], off
	v_lshl_add_u64 v[228:229], s[36:37], 0, v[166:167]
	s_mov_b32 m0, s44
	s_nop 0
	global_load_lds_dwordx4 v[228:229], off
	s_waitcnt vmcnt(8)
	s_waitcnt lgkmcnt(0)
	s_barrier
	v_mfma_f32_16x16x32_bf16 v[128:131], v[134:137], v[182:185], v[128:131]
	s_setprio 1
	v_mfma_f32_16x16x32_bf16 v[124:127], v[142:145], v[182:185], v[124:127]
	v_mfma_f32_16x16x32_bf16 v[116:119], v[142:145], v[200:203], v[116:119]
	v_mfma_f32_16x16x32_bf16 v[120:123], v[134:137], v[200:203], v[120:123]
	v_mfma_f32_16x16x32_bf16 v[112:115], v[134:137], v[208:211], v[112:115]
	v_mfma_f32_16x16x32_bf16 v[108:111], v[142:145], v[208:211], v[108:111]
	v_mfma_f32_16x16x32_bf16 v[100:103], v[142:145], v[216:219], v[100:103]
	v_mfma_f32_16x16x32_bf16 v[104:107], v[134:137], v[216:219], v[104:107]
	v_mfma_f32_16x16x32_bf16 v[128:131], v[138:141], v[190:193], v[128:131]
	v_mfma_f32_16x16x32_bf16 v[124:127], v[146:149], v[190:193], v[124:127]
	v_mfma_f32_16x16x32_bf16 v[116:119], v[146:149], v[204:207], v[116:119]
	v_mfma_f32_16x16x32_bf16 v[120:123], v[138:141], v[204:207], v[120:123]
	v_mfma_f32_16x16x32_bf16 v[112:115], v[138:141], v[212:215], v[112:115]
	v_mfma_f32_16x16x32_bf16 v[108:111], v[146:149], v[212:215], v[108:111]
	v_mfma_f32_16x16x32_bf16 v[100:103], v[146:149], v[222:225], v[100:103]
	v_mfma_f32_16x16x32_bf16 v[104:107], v[138:141], v[222:225], v[104:107]
	s_setprio 2
	s_setprio 1
	v_mfma_f32_16x16x32_bf16 v[96:99], v[150:153], v[182:185], v[96:99]
	v_mfma_f32_16x16x32_bf16 v[92:95], v[158:161], v[182:185], v[92:95]
	v_mfma_f32_16x16x32_bf16 v[84:87], v[158:161], v[200:203], v[84:87]
	v_mfma_f32_16x16x32_bf16 v[88:91], v[150:153], v[200:203], v[88:91]
	v_mfma_f32_16x16x32_bf16 v[80:83], v[150:153], v[208:211], v[80:83]
	v_mfma_f32_16x16x32_bf16 v[76:79], v[158:161], v[208:211], v[76:79]
	v_mfma_f32_16x16x32_bf16 v[68:71], v[158:161], v[216:219], v[68:71]
	v_mfma_f32_16x16x32_bf16 v[72:75], v[150:153], v[216:219], v[72:75]
	v_mfma_f32_16x16x32_bf16 v[96:99], v[154:157], v[190:193], v[96:99]
	v_mfma_f32_16x16x32_bf16 v[92:95], v[178:181], v[190:193], v[92:95]
	v_mfma_f32_16x16x32_bf16 v[84:87], v[178:181], v[204:207], v[84:87]
	v_mfma_f32_16x16x32_bf16 v[88:91], v[154:157], v[204:207], v[88:91]
	v_mfma_f32_16x16x32_bf16 v[80:83], v[154:157], v[212:215], v[80:83]
	v_mfma_f32_16x16x32_bf16 v[76:79], v[178:181], v[212:215], v[76:79]
	v_mfma_f32_16x16x32_bf16 v[68:71], v[178:181], v[222:225], v[68:71]
	v_mfma_f32_16x16x32_bf16 v[72:75], v[154:157], v[222:225], v[72:75]
	s_barrier
	s_setprio 2
	s_mov_b32 m0, s64
	v_lshl_add_u64 v[162:163], v[162:163], 0, s[18:19]
	s_add_u32 s22, s22, 0x40080
	ds_read_b128 v[182:185], v197 offset:49152
	ds_read_b128 v[190:193], v197 offset:50176
	ds_read_b128 v[200:203], v197 offset:51200
	ds_read_b128 v[204:207], v197 offset:52224
	ds_read_b128 v[208:211], v197 offset:53248
	ds_read_b128 v[212:215], v197 offset:54272
	ds_read_b128 v[216:219], v197 offset:55296
	ds_read_b128 v[222:225], v197 offset:56320
	global_load_lds_dwordx4 v[162:163], off
	v_lshl_add_u64 v[162:163], v[174:175], 0, s[18:19]
	s_mov_b32 m0, s65
	s_addc_u32 s23, s23, 0
	global_load_lds_dwordx4 v[162:163], off
	v_lshl_add_u64 v[162:163], s[22:23], 0, v[34:35]
	s_mov_b32 m0, s66
	s_nop 0
	global_load_lds_dwordx4 v[162:163], off
	v_lshl_add_u64 v[162:163], s[22:23], 0, v[164:165]
	s_mov_b32 m0, s67
	s_nop 0
	global_load_lds_dwordx4 v[162:163], off
	v_lshl_add_u64 v[162:163], v[194:195], 0, s[18:19]
	s_mov_b32 m0, s47
	s_nop 0
	global_load_lds_dwordx4 v[162:163], off
	v_lshl_add_u64 v[162:163], v[226:227], 0, s[18:19]
	s_mov_b32 m0, s48
	s_nop 0
	global_load_lds_dwordx4 v[162:163], off
	s_waitcnt vmcnt(8)
	s_waitcnt lgkmcnt(0)
	s_barrier
	v_mfma_f32_16x16x32_bf16 v[64:67], v[134:137], v[182:185], v[64:67]
	s_setprio 1
	v_mfma_f32_16x16x32_bf16 v[60:63], v[142:145], v[182:185], v[60:63]
	v_mfma_f32_16x16x32_bf16 v[52:55], v[142:145], v[200:203], v[52:55]
	v_mfma_f32_16x16x32_bf16 v[56:59], v[134:137], v[200:203], v[56:59]
	v_mfma_f32_16x16x32_bf16 v[48:51], v[134:137], v[208:211], v[48:51]
	v_mfma_f32_16x16x32_bf16 v[44:47], v[142:145], v[208:211], v[44:47]
	v_mfma_f32_16x16x32_bf16 v[36:39], v[142:145], v[216:219], v[36:39]
	v_mfma_f32_16x16x32_bf16 v[40:43], v[134:137], v[216:219], v[40:43]
	v_mfma_f32_16x16x32_bf16 v[64:67], v[138:141], v[190:193], v[64:67]
	v_mfma_f32_16x16x32_bf16 v[60:63], v[146:149], v[190:193], v[60:63]
	v_mfma_f32_16x16x32_bf16 v[52:55], v[146:149], v[204:207], v[52:55]
	v_mfma_f32_16x16x32_bf16 v[56:59], v[138:141], v[204:207], v[56:59]
	v_mfma_f32_16x16x32_bf16 v[48:51], v[138:141], v[212:215], v[48:51]
	v_mfma_f32_16x16x32_bf16 v[44:47], v[146:149], v[212:215], v[44:47]
	v_mfma_f32_16x16x32_bf16 v[36:39], v[146:149], v[222:225], v[36:39]
	v_mfma_f32_16x16x32_bf16 v[40:43], v[138:141], v[222:225], v[40:43]
	s_setprio 2
	s_setprio 1
	v_mfma_f32_16x16x32_bf16 v[30:33], v[150:153], v[182:185], v[30:33]
	v_mfma_f32_16x16x32_bf16 v[26:29], v[158:161], v[182:185], v[26:29]
	v_mfma_f32_16x16x32_bf16 v[18:21], v[158:161], v[200:203], v[18:21]
	v_mfma_f32_16x16x32_bf16 v[22:25], v[150:153], v[200:203], v[22:25]
	v_mfma_f32_16x16x32_bf16 v[14:17], v[150:153], v[208:211], v[14:17]
	v_mfma_f32_16x16x32_bf16 v[10:13], v[158:161], v[208:211], v[10:13]
	v_mfma_f32_16x16x32_bf16 v[2:5], v[158:161], v[216:219], v[2:5]
	v_mfma_f32_16x16x32_bf16 v[6:9], v[150:153], v[216:219], v[6:9]
	v_mfma_f32_16x16x32_bf16 v[30:33], v[154:157], v[190:193], v[30:33]
	v_mfma_f32_16x16x32_bf16 v[26:29], v[178:181], v[190:193], v[26:29]
	v_mfma_f32_16x16x32_bf16 v[18:21], v[178:181], v[204:207], v[18:21]
	v_mfma_f32_16x16x32_bf16 v[22:25], v[154:157], v[204:207], v[22:25]
	v_mfma_f32_16x16x32_bf16 v[14:17], v[154:157], v[212:215], v[14:17]
	v_mfma_f32_16x16x32_bf16 v[10:13], v[178:181], v[212:215], v[10:13]
	v_mfma_f32_16x16x32_bf16 v[2:5], v[178:181], v[222:225], v[2:5]
	v_mfma_f32_16x16x32_bf16 v[6:9], v[154:157], v[222:225], v[6:9]
	s_barrier
	s_setprio 2
	s_add_i32 s70, s70, 2
	s_add_u32 s30, s30, 0x100
	s_addc_u32 s31, s31, 0
	s_add_u32 s68, s68, 0x100
	s_addc_u32 s69, s69, 0
	s_cmp_gt_u32 s70, 13
	s_cbranch_scc0 .LBB0_287
	s_and_b64 vcc, exec, s[8:9]
	s_cbranch_vccz .LBB0_290
	s_barrier

.LBB0_540:
	s_lshl_b32 s14, s55, 19
	v_readlane_b32 s16, v253, 53
	v_readlane_b32 s17, v253, 54
	s_add_u32 s16, s16, s14
	s_addc_u32 s17, s17, 0
	s_and_b64 s[22:23], s[4:5], exec
	s_cselect_b32 s58, s17, s37
	s_cselect_b32 s59, s16, s36
	s_lshl_b32 s14, s54, 19
	s_add_u32 s22, s15, s14
	s_addc_u32 s23, s26, 0
	s_and_b64 s[40:41], s[4:5], exec
	s_cselect_b32 s60, s23, s31
	s_cselect_b32 s61, s22, s30
	s_add_i32 s64, 0, 0x10000
	v_add_u32_e32 v172, s64, v222
	s_add_i32 s66, 0, 0x14000
	v_add_u32_e32 v173, s66, v222
	ds_read_b128 v[160:163], v172
	ds_read_b128 v[152:155], v172 offset:1024
	ds_read_b128 v[156:159], v172 offset:2048
	ds_read_b128 v[148:151], v172 offset:3072
	ds_read_b128 v[144:147], v173
	ds_read_b128 v[136:139], v173 offset:1024
	ds_read_b128 v[140:143], v173 offset:2048
	ds_read_b128 v[132:135], v173 offset:3072
	s_add_u32 s40, s36, 0x40080
	s_addc_u32 s41, s37, 0
	s_add_i32 s62, s43, 0xc000
	v_lshl_add_u64 v[174:175], s[40:41], 0, v[194:195]
	s_mov_b32 m0, s62
	s_add_i32 s63, s43, 0xe000
	ds_read_b128 v[164:167], v223
	ds_read_b128 v[168:171], v223 offset:1024
	ds_read_b128 v[178:181], v223 offset:2048
	ds_read_b128 v[182:185], v223 offset:3072
	ds_read_b128 v[200:203], v223 offset:4096
	ds_read_b128 v[204:207], v223 offset:5120
	ds_read_b128 v[208:211], v223 offset:6144
	ds_read_b128 v[212:215], v223 offset:7168
	global_load_lds_dwordx4 v[174:175], off
	v_lshl_add_u64 v[174:175], s[40:41], 0, v[192:193]
	s_mov_b32 m0, s63
	s_nop 0
	global_load_lds_dwordx4 v[174:175], off
	s_waitcnt vmcnt(8)
	s_waitcnt lgkmcnt(0)
	s_barrier
	v_mfma_f32_16x16x32_bf16 v[128:131], v[160:163], v[164:167], 0
	s_setprio 1
	v_mfma_f32_16x16x32_bf16 v[124:127], v[156:159], v[164:167], 0
	v_mfma_f32_16x16x32_bf16 v[116:119], v[156:159], v[178:181], 0
	v_mfma_f32_16x16x32_bf16 v[120:123], v[160:163], v[178:181], 0
	v_mfma_f32_16x16x32_bf16 v[112:115], v[160:163], v[200:203], 0
	v_mfma_f32_16x16x32_bf16 v[108:111], v[156:159], v[200:203], 0
	v_mfma_f32_16x16x32_bf16 v[100:103], v[156:159], v[208:211], 0
	v_mfma_f32_16x16x32_bf16 v[104:107], v[160:163], v[208:211], 0
	s_nop 0
	v_mfma_f32_16x16x32_bf16 v[128:131], v[152:155], v[168:171], v[128:131]
	v_mfma_f32_16x16x32_bf16 v[124:127], v[148:151], v[168:171], v[124:127]
	v_mfma_f32_16x16x32_bf16 v[116:119], v[148:151], v[182:185], v[116:119]
	v_mfma_f32_16x16x32_bf16 v[120:123], v[152:155], v[182:185], v[120:123]
	v_mfma_f32_16x16x32_bf16 v[112:115], v[152:155], v[204:207], v[112:115]
	v_mfma_f32_16x16x32_bf16 v[108:111], v[148:151], v[204:207], v[108:111]
	v_mfma_f32_16x16x32_bf16 v[100:103], v[148:151], v[212:215], v[100:103]
	v_mfma_f32_16x16x32_bf16 v[104:107], v[152:155], v[212:215], v[104:107]
	s_setprio 2
	s_setprio 1
	v_mfma_f32_16x16x32_bf16 v[96:99], v[144:147], v[164:167], 0
	v_mfma_f32_16x16x32_bf16 v[92:95], v[140:143], v[164:167], 0
	v_mfma_f32_16x16x32_bf16 v[84:87], v[140:143], v[178:181], 0
	v_mfma_f32_16x16x32_bf16 v[88:91], v[144:147], v[178:181], 0
	v_mfma_f32_16x16x32_bf16 v[80:83], v[144:147], v[200:203], 0
	v_mfma_f32_16x16x32_bf16 v[76:79], v[140:143], v[200:203], 0
	v_mfma_f32_16x16x32_bf16 v[68:71], v[140:143], v[208:211], 0
	v_mfma_f32_16x16x32_bf16 v[72:75], v[144:147], v[208:211], 0
	s_nop 0
	v_mfma_f32_16x16x32_bf16 v[96:99], v[136:139], v[168:171], v[96:99]
	v_mfma_f32_16x16x32_bf16 v[92:95], v[132:135], v[168:171], v[92:95]
	v_mfma_f32_16x16x32_bf16 v[84:87], v[132:135], v[182:185], v[84:87]
	v_mfma_f32_16x16x32_bf16 v[88:91], v[136:139], v[182:185], v[88:91]
	v_mfma_f32_16x16x32_bf16 v[80:83], v[136:139], v[204:207], v[80:83]
	v_mfma_f32_16x16x32_bf16 v[76:79], v[132:135], v[204:207], v[76:79]
	v_mfma_f32_16x16x32_bf16 v[68:71], v[132:135], v[212:215], v[68:71]
	v_mfma_f32_16x16x32_bf16 v[72:75], v[136:139], v[212:215], v[72:75]
	s_barrier
	s_setprio 2
	v_lshl_add_u64 v[164:165], s[30:31], 0, v[34:35]
	s_add_i32 s64, s64, s42
	v_lshl_add_u64 v[166:167], v[164:165], 0, s[28:29]
	s_mov_b32 m0, s64
	s_add_i32 s65, s64, 0x2000
	ds_read_b128 v[178:181], v223 offset:16384
	ds_read_b128 v[182:185], v223 offset:17408
	ds_read_b128 v[200:203], v223 offset:18432
	ds_read_b128 v[204:207], v223 offset:19456
	ds_read_b128 v[208:211], v223 offset:20480
	ds_read_b128 v[212:215], v223 offset:21504
	ds_read_b128 v[216:219], v223 offset:22528
	ds_read_b128 v[224:227], v223 offset:23552
	global_load_lds_dwordx4 v[166:167], off
	v_lshl_add_u64 v[166:167], s[30:31], 0, v[190:191]
	s_add_u32 s40, s30, 0x40100
	v_lshl_add_u64 v[168:169], v[166:167], 0, s[28:29]
	s_mov_b32 m0, s65
	s_addc_u32 s41, s31, 0
	s_add_i32 s66, s66, s42
	global_load_lds_dwordx4 v[168:169], off
	v_lshl_add_u64 v[168:169], s[40:41], 0, v[34:35]
	s_mov_b32 m0, s66
	s_add_i32 s67, s66, 0x2000
	global_load_lds_dwordx4 v[168:169], off
	v_lshl_add_u64 v[168:169], s[40:41], 0, v[190:191]
	s_mov_b32 m0, s67
	s_nop 0
	global_load_lds_dwordx4 v[168:169], off
	v_lshl_add_u64 v[168:169], s[36:37], 0, v[194:195]
	v_lshl_add_u64 v[170:171], v[168:169], 0, s[28:29]
	s_mov_b32 m0, s43
	s_nop 0
	global_load_lds_dwordx4 v[170:171], off
	v_lshl_add_u64 v[170:171], s[36:37], 0, v[192:193]
	v_lshl_add_u64 v[174:175], v[170:171], 0, s[28:29]
	s_mov_b32 m0, s44
	s_nop 0
	global_load_lds_dwordx4 v[174:175], off
	s_waitcnt vmcnt(8)
	s_waitcnt lgkmcnt(0)
	s_barrier
	v_mfma_f32_16x16x32_bf16 v[64:67], v[160:163], v[178:181], 0
	s_setprio 1
	v_mfma_f32_16x16x32_bf16 v[60:63], v[156:159], v[178:181], 0
	v_mfma_f32_16x16x32_bf16 v[52:55], v[156:159], v[200:203], 0
	v_mfma_f32_16x16x32_bf16 v[56:59], v[160:163], v[200:203], 0
	v_mfma_f32_16x16x32_bf16 v[48:51], v[160:163], v[208:211], 0
	v_mfma_f32_16x16x32_bf16 v[44:47], v[156:159], v[208:211], 0
	v_mfma_f32_16x16x32_bf16 v[36:39], v[156:159], v[216:219], 0
	v_mfma_f32_16x16x32_bf16 v[40:43], v[160:163], v[216:219], 0
	s_nop 0
	v_mfma_f32_16x16x32_bf16 v[64:67], v[152:155], v[182:185], v[64:67]
	v_mfma_f32_16x16x32_bf16 v[60:63], v[148:151], v[182:185], v[60:63]
	v_mfma_f32_16x16x32_bf16 v[52:55], v[148:151], v[204:207], v[52:55]
	v_mfma_f32_16x16x32_bf16 v[56:59], v[152:155], v[204:207], v[56:59]
	v_mfma_f32_16x16x32_bf16 v[48:51], v[152:155], v[212:215], v[48:51]
	v_mfma_f32_16x16x32_bf16 v[44:47], v[148:151], v[212:215], v[44:47]
	v_mfma_f32_16x16x32_bf16 v[36:39], v[148:151], v[224:227], v[36:39]
	v_mfma_f32_16x16x32_bf16 v[40:43], v[152:155], v[224:227], v[40:43]
	s_setprio 2
	s_setprio 1
	v_mfma_f32_16x16x32_bf16 v[30:33], v[144:147], v[178:181], 0
	v_mfma_f32_16x16x32_bf16 v[26:29], v[140:143], v[178:181], 0
	v_mfma_f32_16x16x32_bf16 v[18:21], v[140:143], v[200:203], 0
	v_mfma_f32_16x16x32_bf16 v[22:25], v[144:147], v[200:203], 0
	v_mfma_f32_16x16x32_bf16 v[14:17], v[144:147], v[208:211], 0
	v_mfma_f32_16x16x32_bf16 v[10:13], v[140:143], v[208:211], 0
	v_mfma_f32_16x16x32_bf16 v[2:5], v[140:143], v[216:219], 0
	v_mfma_f32_16x16x32_bf16 v[6:9], v[144:147], v[216:219], 0
	s_nop 0
	v_mfma_f32_16x16x32_bf16 v[30:33], v[136:139], v[182:185], v[30:33]
	v_mfma_f32_16x16x32_bf16 v[26:29], v[132:135], v[182:185], v[26:29]
	v_mfma_f32_16x16x32_bf16 v[18:21], v[132:135], v[204:207], v[18:21]
	v_mfma_f32_16x16x32_bf16 v[22:25], v[136:139], v[204:207], v[22:25]
	v_mfma_f32_16x16x32_bf16 v[14:17], v[136:139], v[212:215], v[14:17]
	v_mfma_f32_16x16x32_bf16 v[10:13], v[132:135], v[212:215], v[10:13]
	v_mfma_f32_16x16x32_bf16 v[2:5], v[132:135], v[224:227], v[2:5]
	v_mfma_f32_16x16x32_bf16 v[6:9], v[136:139], v[224:227], v[6:9]
	s_barrier
	s_setprio 2
	s_add_i32 s68, 0, 0x18000
	s_add_i32 s70, 0, 0x1c000
	v_add_u32_e32 v132, s68, v222
	v_add_u32_e32 v133, s70, v222
	ds_read_b128 v[134:137], v132
	ds_read_b128 v[138:141], v132 offset:1024
	ds_read_b128 v[142:145], v132 offset:2048
	ds_read_b128 v[146:149], v132 offset:3072
	ds_read_b128 v[150:153], v133
	ds_read_b128 v[154:157], v133 offset:1024
	ds_read_b128 v[158:161], v133 offset:2048
	ds_read_b128 v[178:181], v133 offset:3072
	s_add_u32 s40, s36, 0x40100
	s_addc_u32 s41, s37, 0
	s_mov_b32 m0, s45
	v_lshl_add_u64 v[162:163], s[40:41], 0, v[194:195]
	ds_read_b128 v[182:185], v223 offset:32768
	ds_read_b128 v[200:203], v223 offset:33792
	ds_read_b128 v[204:207], v223 offset:34816
	ds_read_b128 v[208:211], v223 offset:35840
	ds_read_b128 v[212:215], v223 offset:36864
	ds_read_b128 v[216:219], v223 offset:37888
	ds_read_b128 v[224:227], v223 offset:38912
	ds_read_b128 v[228:231], v223 offset:39936
	global_load_lds_dwordx4 v[162:163], off
	v_lshl_add_u64 v[162:163], s[40:41], 0, v[192:193]
	s_mov_b32 m0, s46
	s_nop 0
	global_load_lds_dwordx4 v[162:163], off
	s_waitcnt vmcnt(8)
	s_waitcnt lgkmcnt(0)
	s_barrier
	v_mfma_f32_16x16x32_bf16 v[128:131], v[134:137], v[182:185], v[128:131]
	s_setprio 1
	v_mfma_f32_16x16x32_bf16 v[124:127], v[142:145], v[182:185], v[124:127]
	v_mfma_f32_16x16x32_bf16 v[116:119], v[142:145], v[204:207], v[116:119]
	v_mfma_f32_16x16x32_bf16 v[120:123], v[134:137], v[204:207], v[120:123]
	v_mfma_f32_16x16x32_bf16 v[112:115], v[134:137], v[212:215], v[112:115]
	v_mfma_f32_16x16x32_bf16 v[108:111], v[142:145], v[212:215], v[108:111]
	v_mfma_f32_16x16x32_bf16 v[100:103], v[142:145], v[224:227], v[100:103]
	v_mfma_f32_16x16x32_bf16 v[104:107], v[134:137], v[224:227], v[104:107]
	v_mfma_f32_16x16x32_bf16 v[128:131], v[138:141], v[200:203], v[128:131]
	v_mfma_f32_16x16x32_bf16 v[124:127], v[146:149], v[200:203], v[124:127]
	v_mfma_f32_16x16x32_bf16 v[116:119], v[146:149], v[208:211], v[116:119]
	v_mfma_f32_16x16x32_bf16 v[120:123], v[138:141], v[208:211], v[120:123]
	v_mfma_f32_16x16x32_bf16 v[112:115], v[138:141], v[216:219], v[112:115]
	v_mfma_f32_16x16x32_bf16 v[108:111], v[146:149], v[216:219], v[108:111]
	v_mfma_f32_16x16x32_bf16 v[100:103], v[146:149], v[228:231], v[100:103]
	v_mfma_f32_16x16x32_bf16 v[104:107], v[138:141], v[228:231], v[104:107]
	s_setprio 2
	s_setprio 1
	v_mfma_f32_16x16x32_bf16 v[96:99], v[150:153], v[182:185], v[96:99]
	v_mfma_f32_16x16x32_bf16 v[92:95], v[158:161], v[182:185], v[92:95]
	v_mfma_f32_16x16x32_bf16 v[84:87], v[158:161], v[204:207], v[84:87]
	v_mfma_f32_16x16x32_bf16 v[88:91], v[150:153], v[204:207], v[88:91]
	v_mfma_f32_16x16x32_bf16 v[80:83], v[150:153], v[212:215], v[80:83]
	v_mfma_f32_16x16x32_bf16 v[76:79], v[158:161], v[212:215], v[76:79]
	v_mfma_f32_16x16x32_bf16 v[68:71], v[158:161], v[224:227], v[68:71]
	v_mfma_f32_16x16x32_bf16 v[72:75], v[150:153], v[224:227], v[72:75]
	v_mfma_f32_16x16x32_bf16 v[96:99], v[154:157], v[200:203], v[96:99]
	v_mfma_f32_16x16x32_bf16 v[92:95], v[178:181], v[200:203], v[92:95]
	v_mfma_f32_16x16x32_bf16 v[84:87], v[178:181], v[208:211], v[84:87]
	v_mfma_f32_16x16x32_bf16 v[88:91], v[154:157], v[208:211], v[88:91]
	v_mfma_f32_16x16x32_bf16 v[80:83], v[154:157], v[216:219], v[80:83]
	v_mfma_f32_16x16x32_bf16 v[76:79], v[178:181], v[216:219], v[76:79]
	v_mfma_f32_16x16x32_bf16 v[68:71], v[178:181], v[228:231], v[68:71]
	v_mfma_f32_16x16x32_bf16 v[72:75], v[154:157], v[228:231], v[72:75]
	s_barrier
	s_setprio 2
	s_add_i32 s68, s68, s42
	s_mov_b64 s[24:25], 0x180
	s_add_i32 s69, s68, 0x2000
	v_lshl_add_u64 v[162:163], v[164:165], 0, s[24:25]
	s_mov_b32 m0, s68
	s_add_u32 s40, s30, 0x40180
	ds_read_b128 v[182:185], v223 offset:49152
	ds_read_b128 v[200:203], v223 offset:50176
	ds_read_b128 v[204:207], v223 offset:51200
	ds_read_b128 v[208:211], v223 offset:52224
	ds_read_b128 v[212:215], v223 offset:53248
	ds_read_b128 v[216:219], v223 offset:54272
	ds_read_b128 v[224:227], v223 offset:55296
	ds_read_b128 v[228:231], v223 offset:56320
	global_load_lds_dwordx4 v[162:163], off
	v_lshl_add_u64 v[162:163], v[166:167], 0, s[24:25]
	s_mov_b32 m0, s69
	s_addc_u32 s41, s31, 0
	s_add_i32 s70, s70, s42
	global_load_lds_dwordx4 v[162:163], off
	v_lshl_add_u64 v[162:163], s[40:41], 0, v[34:35]
	s_mov_b32 m0, s70
	s_add_i32 s71, s70, 0x2000
	global_load_lds_dwordx4 v[162:163], off
	v_lshl_add_u64 v[162:163], s[40:41], 0, v[190:191]
	s_mov_b32 m0, s71
	s_nop 0
	global_load_lds_dwordx4 v[162:163], off
	v_lshl_add_u64 v[162:163], v[168:169], 0, s[24:25]
	s_mov_b32 m0, s51
	s_nop 0
	global_load_lds_dwordx4 v[162:163], off
	v_lshl_add_u64 v[162:163], v[170:171], 0, s[24:25]
	s_mov_b32 m0, s52
	s_nop 0
	global_load_lds_dwordx4 v[162:163], off
	s_waitcnt vmcnt(8)
	s_waitcnt lgkmcnt(0)
	s_barrier
	v_mfma_f32_16x16x32_bf16 v[64:67], v[134:137], v[182:185], v[64:67]
	s_setprio 1
	v_mfma_f32_16x16x32_bf16 v[60:63], v[142:145], v[182:185], v[60:63]
	v_mfma_f32_16x16x32_bf16 v[52:55], v[142:145], v[204:207], v[52:55]
	v_mfma_f32_16x16x32_bf16 v[56:59], v[134:137], v[204:207], v[56:59]
	v_mfma_f32_16x16x32_bf16 v[48:51], v[134:137], v[212:215], v[48:51]
	v_mfma_f32_16x16x32_bf16 v[44:47], v[142:145], v[212:215], v[44:47]
	v_mfma_f32_16x16x32_bf16 v[36:39], v[142:145], v[224:227], v[36:39]
	v_mfma_f32_16x16x32_bf16 v[40:43], v[134:137], v[224:227], v[40:43]
	v_mfma_f32_16x16x32_bf16 v[64:67], v[138:141], v[200:203], v[64:67]
	v_mfma_f32_16x16x32_bf16 v[60:63], v[146:149], v[200:203], v[60:63]
	v_mfma_f32_16x16x32_bf16 v[52:55], v[146:149], v[208:211], v[52:55]
	v_mfma_f32_16x16x32_bf16 v[56:59], v[138:141], v[208:211], v[56:59]
	v_mfma_f32_16x16x32_bf16 v[48:51], v[138:141], v[216:219], v[48:51]
	v_mfma_f32_16x16x32_bf16 v[44:47], v[146:149], v[216:219], v[44:47]
	v_mfma_f32_16x16x32_bf16 v[36:39], v[146:149], v[228:231], v[36:39]
	v_mfma_f32_16x16x32_bf16 v[40:43], v[138:141], v[228:231], v[40:43]
	s_setprio 2
	s_setprio 1
	v_mfma_f32_16x16x32_bf16 v[30:33], v[150:153], v[182:185], v[30:33]
	v_mfma_f32_16x16x32_bf16 v[26:29], v[158:161], v[182:185], v[26:29]
	v_mfma_f32_16x16x32_bf16 v[18:21], v[158:161], v[204:207], v[18:21]
	v_mfma_f32_16x16x32_bf16 v[22:25], v[150:153], v[204:207], v[22:25]
	v_mfma_f32_16x16x32_bf16 v[14:17], v[150:153], v[212:215], v[14:17]
	v_mfma_f32_16x16x32_bf16 v[10:13], v[158:161], v[212:215], v[10:13]
	v_mfma_f32_16x16x32_bf16 v[2:5], v[158:161], v[224:227], v[2:5]
	v_mfma_f32_16x16x32_bf16 v[6:9], v[150:153], v[224:227], v[6:9]
	v_mfma_f32_16x16x32_bf16 v[30:33], v[154:157], v[200:203], v[30:33]
	v_mfma_f32_16x16x32_bf16 v[26:29], v[178:181], v[200:203], v[26:29]
	v_mfma_f32_16x16x32_bf16 v[18:21], v[178:181], v[208:211], v[18:21]
	v_mfma_f32_16x16x32_bf16 v[22:25], v[154:157], v[208:211], v[22:25]
	v_mfma_f32_16x16x32_bf16 v[14:17], v[154:157], v[216:219], v[14:17]
	v_mfma_f32_16x16x32_bf16 v[10:13], v[178:181], v[216:219], v[10:13]
	v_mfma_f32_16x16x32_bf16 v[2:5], v[178:181], v[228:231], v[2:5]
	v_mfma_f32_16x16x32_bf16 v[6:9], v[154:157], v[228:231], v[6:9]
	s_barrier
	s_setprio 2
	s_add_u32 s36, s36, 0x40180
	s_addc_u32 s37, s37, 0
	s_add_u32 s72, s30, 0x200
	s_addc_u32 s73, s31, 0
	s_mov_b32 s74, 0
.LBB0_541:
	ds_read_b128 v[134:137], v172
	ds_read_b128 v[138:141], v172 offset:1024
	ds_read_b128 v[142:145], v172 offset:2048
	ds_read_b128 v[146:149], v172 offset:3072
	ds_read_b128 v[150:153], v173
	ds_read_b128 v[154:157], v173 offset:1024
	ds_read_b128 v[158:161], v173 offset:2048
	ds_read_b128 v[162:165], v173 offset:3072
	s_add_u32 s14, s36, 0xfffc0080
	s_addc_u32 s30, s37, -1
	s_cmp_eq_u32 s74, 12
	s_cselect_b32 s41, s58, s30
	s_cselect_b32 s40, s59, s14
	s_cselect_b32 s31, s60, s73
	s_cselect_b32 s30, s61, s72
	s_mov_b32 m0, s62
	v_lshl_add_u64 v[170:171], s[36:37], 0, v[196:197]
	ds_read_b128 v[166:169], v223
	ds_read_b128 v[178:181], v223 offset:1024
	ds_read_b128 v[182:185], v223 offset:2048
	ds_read_b128 v[200:203], v223 offset:3072
	ds_read_b128 v[204:207], v223 offset:4096
	ds_read_b128 v[208:211], v223 offset:5120
	ds_read_b128 v[212:215], v223 offset:6144
	ds_read_b128 v[216:219], v223 offset:7168
	global_load_lds_dwordx4 v[170:171], off
	v_lshl_add_u64 v[170:171], s[36:37], 0, v[198:199]
	s_mov_b32 m0, s63
	s_nop 0
	global_load_lds_dwordx4 v[170:171], off
	s_waitcnt vmcnt(8)
	s_waitcnt lgkmcnt(0)
	s_barrier
	v_mfma_f32_16x16x32_bf16 v[128:131], v[134:137], v[166:169], v[128:131]
	s_setprio 1
	v_mfma_f32_16x16x32_bf16 v[124:127], v[142:145], v[166:169], v[124:127]
	v_mfma_f32_16x16x32_bf16 v[116:119], v[142:145], v[182:185], v[116:119]
	v_mfma_f32_16x16x32_bf16 v[120:123], v[134:137], v[182:185], v[120:123]
	v_mfma_f32_16x16x32_bf16 v[112:115], v[134:137], v[204:207], v[112:115]
	v_mfma_f32_16x16x32_bf16 v[108:111], v[142:145], v[204:207], v[108:111]
	v_mfma_f32_16x16x32_bf16 v[100:103], v[142:145], v[212:215], v[100:103]
	v_mfma_f32_16x16x32_bf16 v[104:107], v[134:137], v[212:215], v[104:107]
	v_mfma_f32_16x16x32_bf16 v[128:131], v[138:141], v[178:181], v[128:131]
	v_mfma_f32_16x16x32_bf16 v[124:127], v[146:149], v[178:181], v[124:127]
	v_mfma_f32_16x16x32_bf16 v[116:119], v[146:149], v[200:203], v[116:119]
	v_mfma_f32_16x16x32_bf16 v[120:123], v[138:141], v[200:203], v[120:123]
	v_mfma_f32_16x16x32_bf16 v[112:115], v[138:141], v[208:211], v[112:115]
	v_mfma_f32_16x16x32_bf16 v[108:111], v[146:149], v[208:211], v[108:111]
	v_mfma_f32_16x16x32_bf16 v[100:103], v[146:149], v[216:219], v[100:103]
	v_mfma_f32_16x16x32_bf16 v[104:107], v[138:141], v[216:219], v[104:107]
	s_setprio 2
	s_setprio 1
	v_mfma_f32_16x16x32_bf16 v[96:99], v[150:153], v[166:169], v[96:99]
	v_mfma_f32_16x16x32_bf16 v[92:95], v[158:161], v[166:169], v[92:95]
	v_mfma_f32_16x16x32_bf16 v[84:87], v[158:161], v[182:185], v[84:87]
	v_mfma_f32_16x16x32_bf16 v[88:91], v[150:153], v[182:185], v[88:91]
	v_mfma_f32_16x16x32_bf16 v[80:83], v[150:153], v[204:207], v[80:83]
	v_mfma_f32_16x16x32_bf16 v[76:79], v[158:161], v[204:207], v[76:79]
	v_mfma_f32_16x16x32_bf16 v[68:71], v[158:161], v[212:215], v[68:71]
	v_mfma_f32_16x16x32_bf16 v[72:75], v[150:153], v[212:215], v[72:75]
	v_mfma_f32_16x16x32_bf16 v[96:99], v[154:157], v[178:181], v[96:99]
	v_mfma_f32_16x16x32_bf16 v[92:95], v[162:165], v[178:181], v[92:95]
	v_mfma_f32_16x16x32_bf16 v[84:87], v[162:165], v[200:203], v[84:87]
	v_mfma_f32_16x16x32_bf16 v[88:91], v[154:157], v[200:203], v[88:91]
	v_mfma_f32_16x16x32_bf16 v[80:83], v[154:157], v[208:211], v[80:83]
	v_mfma_f32_16x16x32_bf16 v[76:79], v[162:165], v[208:211], v[76:79]
	v_mfma_f32_16x16x32_bf16 v[68:71], v[162:165], v[216:219], v[68:71]
	v_mfma_f32_16x16x32_bf16 v[72:75], v[154:157], v[216:219], v[72:75]
	s_barrier
	s_setprio 2
	s_mov_b32 m0, s64
	v_lshl_add_u64 v[170:171], s[30:31], 0, v[34:35]
	s_add_u32 s76, s30, 0x40000
	ds_read_b128 v[166:169], v223 offset:16384
	ds_read_b128 v[178:181], v223 offset:17408
	ds_read_b128 v[182:185], v223 offset:18432
	ds_read_b128 v[200:203], v223 offset:19456
	ds_read_b128 v[204:207], v223 offset:20480
	ds_read_b128 v[208:211], v223 offset:21504
	ds_read_b128 v[212:215], v223 offset:22528
	ds_read_b128 v[216:219], v223 offset:23552
	global_load_lds_dwordx4 v[170:171], off
	v_lshl_add_u64 v[174:175], s[30:31], 0, v[190:191]
	s_mov_b32 m0, s65
	s_addc_u32 s77, s31, 0
	global_load_lds_dwordx4 v[174:175], off
	v_lshl_add_u64 v[224:225], s[76:77], 0, v[34:35]
	s_mov_b32 m0, s66
	v_lshl_add_u64 v[226:227], s[40:41], 0, v[192:193]
	global_load_lds_dwordx4 v[224:225], off
	v_lshl_add_u64 v[224:225], s[76:77], 0, v[190:191]
	s_mov_b32 m0, s67
	s_nop 0
	global_load_lds_dwordx4 v[224:225], off
	v_lshl_add_u64 v[224:225], s[40:41], 0, v[194:195]
	s_mov_b32 m0, s43
	s_nop 0
	global_load_lds_dwordx4 v[224:225], off
	s_mov_b32 m0, s44
	s_nop 0
	global_load_lds_dwordx4 v[226:227], off
	s_waitcnt vmcnt(8)
	s_waitcnt lgkmcnt(0)
	s_barrier
	v_mfma_f32_16x16x32_bf16 v[64:67], v[134:137], v[166:169], v[64:67]
	s_setprio 1
	v_mfma_f32_16x16x32_bf16 v[60:63], v[142:145], v[166:169], v[60:63]
	v_mfma_f32_16x16x32_bf16 v[52:55], v[142:145], v[182:185], v[52:55]
	v_mfma_f32_16x16x32_bf16 v[56:59], v[134:137], v[182:185], v[56:59]
	v_mfma_f32_16x16x32_bf16 v[48:51], v[134:137], v[204:207], v[48:51]
	v_mfma_f32_16x16x32_bf16 v[44:47], v[142:145], v[204:207], v[44:47]
	v_mfma_f32_16x16x32_bf16 v[36:39], v[142:145], v[212:215], v[36:39]
	v_mfma_f32_16x16x32_bf16 v[40:43], v[134:137], v[212:215], v[40:43]
	v_mfma_f32_16x16x32_bf16 v[64:67], v[138:141], v[178:181], v[64:67]
	v_mfma_f32_16x16x32_bf16 v[60:63], v[146:149], v[178:181], v[60:63]
	v_mfma_f32_16x16x32_bf16 v[52:55], v[146:149], v[200:203], v[52:55]
	v_mfma_f32_16x16x32_bf16 v[56:59], v[138:141], v[200:203], v[56:59]
	v_mfma_f32_16x16x32_bf16 v[48:51], v[138:141], v[208:211], v[48:51]
	v_mfma_f32_16x16x32_bf16 v[44:47], v[146:149], v[208:211], v[44:47]
	v_mfma_f32_16x16x32_bf16 v[36:39], v[146:149], v[216:219], v[36:39]
	v_mfma_f32_16x16x32_bf16 v[40:43], v[138:141], v[216:219], v[40:43]
	s_setprio 2
	s_setprio 1
	v_mfma_f32_16x16x32_bf16 v[30:33], v[150:153], v[166:169], v[30:33]
	v_mfma_f32_16x16x32_bf16 v[26:29], v[158:161], v[166:169], v[26:29]
	v_mfma_f32_16x16x32_bf16 v[18:21], v[158:161], v[182:185], v[18:21]
	v_mfma_f32_16x16x32_bf16 v[22:25], v[150:153], v[182:185], v[22:25]
	v_mfma_f32_16x16x32_bf16 v[14:17], v[150:153], v[204:207], v[14:17]
	v_mfma_f32_16x16x32_bf16 v[10:13], v[158:161], v[204:207], v[10:13]
	v_mfma_f32_16x16x32_bf16 v[2:5], v[158:161], v[212:215], v[2:5]
	v_mfma_f32_16x16x32_bf16 v[6:9], v[150:153], v[212:215], v[6:9]
	v_mfma_f32_16x16x32_bf16 v[30:33], v[154:157], v[178:181], v[30:33]
	v_mfma_f32_16x16x32_bf16 v[26:29], v[162:165], v[178:181], v[26:29]
	v_mfma_f32_16x16x32_bf16 v[18:21], v[162:165], v[200:203], v[18:21]
	v_mfma_f32_16x16x32_bf16 v[22:25], v[154:157], v[200:203], v[22:25]
	v_mfma_f32_16x16x32_bf16 v[14:17], v[154:157], v[208:211], v[14:17]
	v_mfma_f32_16x16x32_bf16 v[10:13], v[162:165], v[208:211], v[10:13]
	v_mfma_f32_16x16x32_bf16 v[2:5], v[162:165], v[216:219], v[2:5]
	v_mfma_f32_16x16x32_bf16 v[6:9], v[154:157], v[216:219], v[6:9]
	s_barrier
	s_setprio 2
	ds_read_b128 v[134:137], v132
	ds_read_b128 v[138:141], v132 offset:1024
	ds_read_b128 v[142:145], v132 offset:2048
	ds_read_b128 v[146:149], v132 offset:3072
	ds_read_b128 v[150:153], v133
	ds_read_b128 v[154:157], v133 offset:1024
	ds_read_b128 v[158:161], v133 offset:2048
	ds_read_b128 v[162:165], v133 offset:3072
	s_add_u32 s40, s40, 0x40000
	s_addc_u32 s41, s41, 0
	s_mov_b32 m0, s45
	v_lshl_add_u64 v[228:229], s[40:41], 0, v[194:195]
	ds_read_b128 v[166:169], v223 offset:32768
	ds_read_b128 v[178:181], v223 offset:33792
	ds_read_b128 v[182:185], v223 offset:34816
	ds_read_b128 v[200:203], v223 offset:35840
	ds_read_b128 v[204:207], v223 offset:36864
	ds_read_b128 v[208:211], v223 offset:37888
	ds_read_b128 v[212:215], v223 offset:38912
	ds_read_b128 v[216:219], v223 offset:39936
	global_load_lds_dwordx4 v[228:229], off
	v_lshl_add_u64 v[228:229], s[40:41], 0, v[192:193]
	s_mov_b32 m0, s46
	s_nop 0
	global_load_lds_dwordx4 v[228:229], off
	s_waitcnt vmcnt(8)
	s_waitcnt lgkmcnt(0)
	s_barrier
	v_mfma_f32_16x16x32_bf16 v[128:131], v[134:137], v[166:169], v[128:131]
	s_setprio 1
	v_mfma_f32_16x16x32_bf16 v[124:127], v[142:145], v[166:169], v[124:127]
	v_mfma_f32_16x16x32_bf16 v[116:119], v[142:145], v[182:185], v[116:119]
	v_mfma_f32_16x16x32_bf16 v[120:123], v[134:137], v[182:185], v[120:123]
	v_mfma_f32_16x16x32_bf16 v[112:115], v[134:137], v[204:207], v[112:115]
	v_mfma_f32_16x16x32_bf16 v[108:111], v[142:145], v[204:207], v[108:111]
	v_mfma_f32_16x16x32_bf16 v[100:103], v[142:145], v[212:215], v[100:103]
	v_mfma_f32_16x16x32_bf16 v[104:107], v[134:137], v[212:215], v[104:107]
	v_mfma_f32_16x16x32_bf16 v[128:131], v[138:141], v[178:181], v[128:131]
	v_mfma_f32_16x16x32_bf16 v[124:127], v[146:149], v[178:181], v[124:127]
	v_mfma_f32_16x16x32_bf16 v[116:119], v[146:149], v[200:203], v[116:119]
	v_mfma_f32_16x16x32_bf16 v[120:123], v[138:141], v[200:203], v[120:123]
	v_mfma_f32_16x16x32_bf16 v[112:115], v[138:141], v[208:211], v[112:115]
	v_mfma_f32_16x16x32_bf16 v[108:111], v[146:149], v[208:211], v[108:111]
	v_mfma_f32_16x16x32_bf16 v[100:103], v[146:149], v[216:219], v[100:103]
	v_mfma_f32_16x16x32_bf16 v[104:107], v[138:141], v[216:219], v[104:107]
	s_setprio 2
	s_setprio 1
	v_mfma_f32_16x16x32_bf16 v[96:99], v[150:153], v[166:169], v[96:99]
	v_mfma_f32_16x16x32_bf16 v[92:95], v[158:161], v[166:169], v[92:95]
	v_mfma_f32_16x16x32_bf16 v[84:87], v[158:161], v[182:185], v[84:87]
	v_mfma_f32_16x16x32_bf16 v[88:91], v[150:153], v[182:185], v[88:91]
	v_mfma_f32_16x16x32_bf16 v[80:83], v[150:153], v[204:207], v[80:83]
	v_mfma_f32_16x16x32_bf16 v[76:79], v[158:161], v[204:207], v[76:79]
	v_mfma_f32_16x16x32_bf16 v[68:71], v[158:161], v[212:215], v[68:71]
	v_mfma_f32_16x16x32_bf16 v[72:75], v[150:153], v[212:215], v[72:75]
	v_mfma_f32_16x16x32_bf16 v[96:99], v[154:157], v[178:181], v[96:99]
	v_mfma_f32_16x16x32_bf16 v[92:95], v[162:165], v[178:181], v[92:95]
	v_mfma_f32_16x16x32_bf16 v[84:87], v[162:165], v[200:203], v[84:87]
	v_mfma_f32_16x16x32_bf16 v[88:91], v[154:157], v[200:203], v[88:91]
	v_mfma_f32_16x16x32_bf16 v[80:83], v[154:157], v[208:211], v[80:83]
	v_mfma_f32_16x16x32_bf16 v[76:79], v[162:165], v[208:211], v[76:79]
	v_mfma_f32_16x16x32_bf16 v[68:71], v[162:165], v[216:219], v[68:71]
	v_mfma_f32_16x16x32_bf16 v[72:75], v[154:157], v[216:219], v[72:75]
	s_barrier
	s_setprio 2
	s_mov_b32 m0, s68
	v_lshl_add_u64 v[170:171], v[170:171], 0, s[18:19]
	s_add_u32 s30, s30, 0x40080
	ds_read_b128 v[166:169], v223 offset:49152
	ds_read_b128 v[178:181], v223 offset:50176
	ds_read_b128 v[182:185], v223 offset:51200
	ds_read_b128 v[200:203], v223 offset:52224
	ds_read_b128 v[204:207], v223 offset:53248
	ds_read_b128 v[208:211], v223 offset:54272
	ds_read_b128 v[212:215], v223 offset:55296
	ds_read_b128 v[216:219], v223 offset:56320
	global_load_lds_dwordx4 v[170:171], off
	v_lshl_add_u64 v[170:171], v[174:175], 0, s[18:19]
	s_mov_b32 m0, s69
	s_addc_u32 s31, s31, 0
	global_load_lds_dwordx4 v[170:171], off
	v_lshl_add_u64 v[170:171], s[30:31], 0, v[34:35]
	s_mov_b32 m0, s70
	s_nop 0
	global_load_lds_dwordx4 v[170:171], off
	v_lshl_add_u64 v[170:171], s[30:31], 0, v[190:191]
	s_mov_b32 m0, s71
	s_nop 0
	global_load_lds_dwordx4 v[170:171], off
	v_lshl_add_u64 v[170:171], v[224:225], 0, s[18:19]
	s_mov_b32 m0, s51
	s_nop 0
	global_load_lds_dwordx4 v[170:171], off
	v_lshl_add_u64 v[170:171], v[226:227], 0, s[18:19]
	s_mov_b32 m0, s52
	s_nop 0
	global_load_lds_dwordx4 v[170:171], off
	s_waitcnt vmcnt(8)
	s_waitcnt lgkmcnt(0)
	s_barrier
	v_mfma_f32_16x16x32_bf16 v[64:67], v[134:137], v[166:169], v[64:67]
	s_setprio 1
	v_mfma_f32_16x16x32_bf16 v[60:63], v[142:145], v[166:169], v[60:63]
	v_mfma_f32_16x16x32_bf16 v[52:55], v[142:145], v[182:185], v[52:55]
	v_mfma_f32_16x16x32_bf16 v[56:59], v[134:137], v[182:185], v[56:59]
	v_mfma_f32_16x16x32_bf16 v[48:51], v[134:137], v[204:207], v[48:51]
	v_mfma_f32_16x16x32_bf16 v[44:47], v[142:145], v[204:207], v[44:47]
	v_mfma_f32_16x16x32_bf16 v[36:39], v[142:145], v[212:215], v[36:39]
	v_mfma_f32_16x16x32_bf16 v[40:43], v[134:137], v[212:215], v[40:43]
	v_mfma_f32_16x16x32_bf16 v[64:67], v[138:141], v[178:181], v[64:67]
	v_mfma_f32_16x16x32_bf16 v[60:63], v[146:149], v[178:181], v[60:63]
	v_mfma_f32_16x16x32_bf16 v[52:55], v[146:149], v[200:203], v[52:55]
	v_mfma_f32_16x16x32_bf16 v[56:59], v[138:141], v[200:203], v[56:59]
	v_mfma_f32_16x16x32_bf16 v[48:51], v[138:141], v[208:211], v[48:51]
	v_mfma_f32_16x16x32_bf16 v[44:47], v[146:149], v[208:211], v[44:47]
	v_mfma_f32_16x16x32_bf16 v[36:39], v[146:149], v[216:219], v[36:39]
	v_mfma_f32_16x16x32_bf16 v[40:43], v[138:141], v[216:219], v[40:43]
	s_setprio 2
	s_setprio 1
	v_mfma_f32_16x16x32_bf16 v[30:33], v[150:153], v[166:169], v[30:33]
	v_mfma_f32_16x16x32_bf16 v[26:29], v[158:161], v[166:169], v[26:29]
	v_mfma_f32_16x16x32_bf16 v[18:21], v[158:161], v[182:185], v[18:21]
	v_mfma_f32_16x16x32_bf16 v[22:25], v[150:153], v[182:185], v[22:25]
	v_mfma_f32_16x16x32_bf16 v[14:17], v[150:153], v[204:207], v[14:17]
	v_mfma_f32_16x16x32_bf16 v[10:13], v[158:161], v[204:207], v[10:13]
	v_mfma_f32_16x16x32_bf16 v[2:5], v[158:161], v[212:215], v[2:5]
	v_mfma_f32_16x16x32_bf16 v[6:9], v[150:153], v[212:215], v[6:9]
	v_mfma_f32_16x16x32_bf16 v[30:33], v[154:157], v[178:181], v[30:33]
	v_mfma_f32_16x16x32_bf16 v[26:29], v[162:165], v[178:181], v[26:29]
	v_mfma_f32_16x16x32_bf16 v[18:21], v[162:165], v[200:203], v[18:21]
	v_mfma_f32_16x16x32_bf16 v[22:25], v[154:157], v[200:203], v[22:25]
	v_mfma_f32_16x16x32_bf16 v[14:17], v[154:157], v[208:211], v[14:17]
	v_mfma_f32_16x16x32_bf16 v[10:13], v[162:165], v[208:211], v[10:13]
	v_mfma_f32_16x16x32_bf16 v[2:5], v[162:165], v[216:219], v[2:5]
	v_mfma_f32_16x16x32_bf16 v[6:9], v[154:157], v[216:219], v[6:9]
	s_barrier
	s_setprio 2
	s_add_i32 s74, s74, 2
	s_add_u32 s36, s36, 0x100
	s_addc_u32 s37, s37, 0
	s_add_u32 s72, s72, 0x100
	s_addc_u32 s73, s73, 0
	s_cmp_gt_u32 s74, 13
	s_cbranch_scc0 .LBB0_541
	v_readlane_b32 s74, v255, 3
	s_and_b64 vcc, exec, s[10:11]
	v_readlane_b32 s75, v255, 4
	s_mov_b32 s58, 0x19b00000
	v_readlane_b32 s59, v255, 10
	s_mov_b32 s60, 0xff61b1e6
	s_mov_b64 s[62:63], 0x800
	s_mov_b32 s64, 0x3b000000
	s_cbranch_vccz .LBB0_544
	s_barrier

.LBB0_819:
	s_add_u32 s81, s30, 0x200
	s_addc_u32 s82, s31, 0
	s_add_i32 s55, 0, 0x14000
	s_add_i32 s52, 0, 0x10000
	v_add_u32_e32 v199, s55, v167
	v_add_u32_e32 v200, s52, v167
	ds_read_b128 v[10:13], v199
	ds_read_b128 v[14:17], v199 offset:1024
	ds_read_b128 v[2:5], v199 offset:2048
	ds_read_b128 v[6:9], v199 offset:3072
	ds_read_b128 v[22:25], v200 offset:3072
	ds_read_b128 v[18:21], v200 offset:2048
	ds_read_b128 v[30:33], v200 offset:1024
	ds_read_b128 v[26:29], v200
	s_lshl_b32 s14, s80, 10
	s_add_i32 s83, s14, 0
	s_add_i32 s83, s83, 0x20400
	v_mov_b32_e32 v191, v35
	v_mov_b32_e32 v175, v35
	s_add_i32 s84, s69, 0xc000
	v_readlane_b32 s26, v253, 28
	s_mov_b32 m0, s84
	v_readlane_b32 s27, v253, 29
	s_add_i32 s53, s69, 0xe000
	ds_read_b128 v[202:205], v169
	ds_read_b128 v[206:209], v169 offset:1024
	ds_read_b128 v[222:225], v169 offset:2048
	ds_read_b128 v[226:229], v169 offset:3072
	ds_read_b128 v[230:233], v169 offset:4096
	ds_read_b128 v[234:237], v169 offset:5120
	ds_read_b128 v[238:241], v169 offset:6144
	ds_read_b128 v[242:245], v169 offset:7168
	global_load_lds_dwordx4 v190, s[26:27]
	s_mov_b32 m0, s53
	s_nop 0
	global_load_lds_dwordx4 v174, s[26:27]
	s_waitcnt vmcnt(8)
	s_waitcnt lgkmcnt(0)
	s_barrier
	v_mfma_f32_16x16x128_f8f6f4 v[160:163], v[26:33], v[202:209], 0
	s_setprio 1
	v_mfma_f32_16x16x128_f8f6f4 v[156:159], v[18:25], v[202:209], 0
	v_mfma_f32_16x16x128_f8f6f4 v[148:151], v[18:25], v[222:229], 0
	v_mfma_f32_16x16x128_f8f6f4 v[152:155], v[26:33], v[222:229], 0
	v_mfma_f32_16x16x128_f8f6f4 v[144:147], v[26:33], v[230:237], 0
	v_mfma_f32_16x16x128_f8f6f4 v[140:143], v[18:25], v[230:237], 0
	v_mfma_f32_16x16x128_f8f6f4 v[132:135], v[18:25], v[238:245], 0
	v_mfma_f32_16x16x128_f8f6f4 v[136:139], v[26:33], v[238:245], 0
	s_setprio 2
	s_setprio 1
	v_mfma_f32_16x16x128_f8f6f4 v[128:131], v[10:17], v[202:209], 0
	v_mfma_f32_16x16x128_f8f6f4 v[124:127], v[2:9], v[202:209], 0
	v_mfma_f32_16x16x128_f8f6f4 v[116:119], v[2:9], v[222:229], 0
	v_mfma_f32_16x16x128_f8f6f4 v[120:123], v[10:17], v[222:229], 0
	v_mfma_f32_16x16x128_f8f6f4 v[112:115], v[10:17], v[230:237], 0
	v_mfma_f32_16x16x128_f8f6f4 v[108:111], v[2:9], v[230:237], 0
	v_mfma_f32_16x16x128_f8f6f4 v[100:103], v[2:9], v[238:245], 0
	v_mfma_f32_16x16x128_f8f6f4 v[104:107], v[10:17], v[238:245], 0
	s_barrier
	s_setprio 2
	s_add_i32 s52, s52, s68
	v_lshl_add_u64 v[194:195], s[30:31], 0, v[170:171]
	s_add_i32 s85, s52, 0x2000
	v_lshl_add_u64 v[178:179], v[194:195], 0, s[28:29]
	s_mov_b32 m0, s52
	v_lshl_add_u64 v[196:197], s[30:31], 0, v[172:173]
	s_add_u32 s36, s30, 0x20100
	ds_read_b128 v[202:205], v169 offset:16384
	ds_read_b128 v[206:209], v169 offset:17408
	ds_read_b128 v[222:225], v169 offset:18432
	ds_read_b128 v[226:229], v169 offset:19456
	ds_read_b128 v[230:233], v169 offset:20480
	ds_read_b128 v[234:237], v169 offset:21504
	ds_read_b128 v[238:241], v169 offset:22528
	ds_read_b128 v[242:245], v169 offset:23552
	global_load_lds_dwordx4 v[178:179], off
	v_lshl_add_u64 v[178:179], v[196:197], 0, s[28:29]
	s_mov_b32 m0, s85
	s_addc_u32 s37, s31, 0
	s_add_i32 s55, s55, s68
	global_load_lds_dwordx4 v[178:179], off
	v_lshl_add_u64 v[178:179], s[36:37], 0, v[170:171]
	s_mov_b32 m0, s55
	s_add_i32 s65, s55, 0x2000
	global_load_lds_dwordx4 v[178:179], off
	v_lshl_add_u64 v[178:179], s[36:37], 0, v[172:173]
	s_mov_b32 m0, s65
	v_readlane_b32 s26, v253, 37
	global_load_lds_dwordx4 v[178:179], off
	s_mov_b32 m0, s69
	v_readlane_b32 s27, v253, 38
	s_nop 4
	global_load_lds_dwordx4 v34, s[26:27]
	s_mov_b32 m0, s70
	s_nop 0
	global_load_lds_dwordx4 v192, s[26:27]
	s_waitcnt vmcnt(8)
	s_waitcnt lgkmcnt(0)
	s_barrier
	v_mfma_f32_16x16x128_f8f6f4 v[96:99], v[26:33], v[202:209], 0
	s_setprio 1
	v_mfma_f32_16x16x128_f8f6f4 v[92:95], v[18:25], v[202:209], 0
	v_mfma_f32_16x16x128_f8f6f4 v[84:87], v[18:25], v[222:229], 0
	v_mfma_f32_16x16x128_f8f6f4 v[88:91], v[26:33], v[222:229], 0
	v_mfma_f32_16x16x128_f8f6f4 v[80:83], v[26:33], v[230:237], 0
	v_mfma_f32_16x16x128_f8f6f4 v[76:79], v[18:25], v[230:237], 0
	v_mfma_f32_16x16x128_f8f6f4 v[68:71], v[18:25], v[238:245], 0
	v_mfma_f32_16x16x128_f8f6f4 v[72:75], v[26:33], v[238:245], 0
	s_setprio 2
	s_setprio 1
	v_mfma_f32_16x16x128_f8f6f4 v[64:67], v[10:17], v[202:209], 0
	v_mfma_f32_16x16x128_f8f6f4 v[60:63], v[2:9], v[202:209], 0
	v_mfma_f32_16x16x128_f8f6f4 v[52:55], v[2:9], v[222:229], 0
	v_mfma_f32_16x16x128_f8f6f4 v[56:59], v[10:17], v[222:229], 0
	v_mfma_f32_16x16x128_f8f6f4 v[48:51], v[10:17], v[230:237], 0
	v_mfma_f32_16x16x128_f8f6f4 v[44:47], v[2:9], v[230:237], 0
	v_mfma_f32_16x16x128_f8f6f4 v[36:39], v[2:9], v[238:245], 0
	v_mfma_f32_16x16x128_f8f6f4 v[40:43], v[10:17], v[238:245], 0
	s_barrier
	s_setprio 2
	s_add_i32 s54, 0, 0x18000
	s_add_i32 s51, 0, 0x1c000
	v_add_u32_e32 v201, s54, v167
	v_add_u32_e32 v202, s51, v167
	ds_read_b128 v[26:29], v201
	ds_read_b128 v[30:33], v201 offset:1024
	ds_read_b128 v[18:21], v201 offset:2048
	ds_read_b128 v[22:25], v201 offset:3072
	ds_read_b128 v[10:13], v202
	ds_read_b128 v[14:17], v202 offset:1024
	ds_read_b128 v[2:5], v202 offset:2048
	ds_read_b128 v[6:9], v202 offset:3072
	s_mov_b32 m0, s71
	ds_read_b128 v[204:207], v169 offset:32768
	ds_read_b128 v[208:211], v169 offset:33792
	ds_read_b128 v[222:225], v169 offset:34816
	ds_read_b128 v[226:229], v169 offset:35840
	ds_read_b128 v[230:233], v169 offset:36864
	ds_read_b128 v[234:237], v169 offset:37888
	ds_read_b128 v[238:241], v169 offset:38912
	ds_read_b128 v[242:245], v169 offset:39936
	global_load_lds_dwordx4 v189, s[26:27]
	s_mov_b32 m0, s72
	s_nop 0
	global_load_lds_dwordx4 v198, s[26:27]
	s_waitcnt vmcnt(8)
	s_waitcnt lgkmcnt(0)
	s_barrier
	v_mfma_f32_16x16x128_f8f6f4 v[160:163], v[26:33], v[204:211], v[160:163]
	s_setprio 1
	v_mfma_f32_16x16x128_f8f6f4 v[156:159], v[18:25], v[204:211], v[156:159]
	v_mfma_f32_16x16x128_f8f6f4 v[148:151], v[18:25], v[222:229], v[148:151]
	v_mfma_f32_16x16x128_f8f6f4 v[152:155], v[26:33], v[222:229], v[152:155]
	v_mfma_f32_16x16x128_f8f6f4 v[144:147], v[26:33], v[230:237], v[144:147]
	v_mfma_f32_16x16x128_f8f6f4 v[140:143], v[18:25], v[230:237], v[140:143]
	v_mfma_f32_16x16x128_f8f6f4 v[132:135], v[18:25], v[238:245], v[132:135]
	v_mfma_f32_16x16x128_f8f6f4 v[136:139], v[26:33], v[238:245], v[136:139]
	s_setprio 2
	s_setprio 1
	v_mfma_f32_16x16x128_f8f6f4 v[128:131], v[10:17], v[204:211], v[128:131]
	v_mfma_f32_16x16x128_f8f6f4 v[124:127], v[2:9], v[204:211], v[124:127]
	v_mfma_f32_16x16x128_f8f6f4 v[116:119], v[2:9], v[222:229], v[116:119]
	v_mfma_f32_16x16x128_f8f6f4 v[120:123], v[10:17], v[222:229], v[120:123]
	v_mfma_f32_16x16x128_f8f6f4 v[112:115], v[10:17], v[230:237], v[112:115]
	v_mfma_f32_16x16x128_f8f6f4 v[108:111], v[2:9], v[230:237], v[108:111]
	v_mfma_f32_16x16x128_f8f6f4 v[100:103], v[2:9], v[238:245], v[100:103]
	v_mfma_f32_16x16x128_f8f6f4 v[104:107], v[10:17], v[238:245], v[104:107]
	s_barrier
	s_setprio 2
	s_add_i32 s54, s54, s68
	s_mov_b64 s[26:27], 0x180
	s_add_i32 s50, s54, 0x2000
	v_lshl_add_u64 v[178:179], v[194:195], 0, s[26:27]
	s_mov_b32 m0, s54
	s_add_u32 s30, s30, 0x20180
	ds_read_b128 v[204:207], v169 offset:49152
	ds_read_b128 v[208:211], v169 offset:50176
	ds_read_b128 v[222:225], v169 offset:51200
	ds_read_b128 v[226:229], v169 offset:52224
	ds_read_b128 v[230:233], v169 offset:53248
	ds_read_b128 v[234:237], v169 offset:54272
	ds_read_b128 v[238:241], v169 offset:55296
	ds_read_b128 v[242:245], v169 offset:56320
	global_load_lds_dwordx4 v[178:179], off
	v_lshl_add_u64 v[178:179], v[196:197], 0, s[26:27]
	s_mov_b32 m0, s50
	s_addc_u32 s31, s31, 0
	s_add_i32 s51, s51, s68
	global_load_lds_dwordx4 v[178:179], off
	v_lshl_add_u64 v[178:179], s[30:31], 0, v[170:171]
	s_mov_b32 m0, s51
	s_add_i32 s64, s51, 0x2000
	global_load_lds_dwordx4 v[178:179], off
	v_lshl_add_u64 v[178:179], s[30:31], 0, v[172:173]
	s_mov_b32 m0, s64
	v_readlane_b32 s26, v253, 39
	global_load_lds_dwordx4 v[178:179], off
	s_mov_b32 m0, s75
	v_readlane_b32 s27, v253, 40
	s_nop 4
	global_load_lds_dwordx4 v34, s[26:27]
	s_mov_b32 m0, s76
	s_nop 0
	global_load_lds_dwordx4 v192, s[26:27]
	s_waitcnt vmcnt(8)
	s_waitcnt lgkmcnt(0)
	s_barrier
	v_mfma_f32_16x16x128_f8f6f4 v[96:99], v[26:33], v[204:211], v[96:99]
	s_setprio 1
	v_mfma_f32_16x16x128_f8f6f4 v[92:95], v[18:25], v[204:211], v[92:95]
	v_mfma_f32_16x16x128_f8f6f4 v[84:87], v[18:25], v[222:229], v[84:87]
	v_mfma_f32_16x16x128_f8f6f4 v[88:91], v[26:33], v[222:229], v[88:91]
	v_mfma_f32_16x16x128_f8f6f4 v[80:83], v[26:33], v[230:237], v[80:83]
	v_mfma_f32_16x16x128_f8f6f4 v[76:79], v[18:25], v[230:237], v[76:79]
	v_mfma_f32_16x16x128_f8f6f4 v[68:71], v[18:25], v[238:245], v[68:71]
	v_mfma_f32_16x16x128_f8f6f4 v[72:75], v[26:33], v[238:245], v[72:75]
	s_setprio 2
	s_setprio 1
	v_mfma_f32_16x16x128_f8f6f4 v[64:67], v[10:17], v[204:211], v[64:67]
	v_mfma_f32_16x16x128_f8f6f4 v[60:63], v[2:9], v[204:211], v[60:63]
	v_mfma_f32_16x16x128_f8f6f4 v[52:55], v[2:9], v[222:229], v[52:55]
	v_mfma_f32_16x16x128_f8f6f4 v[56:59], v[10:17], v[222:229], v[56:59]
	v_mfma_f32_16x16x128_f8f6f4 v[48:51], v[10:17], v[230:237], v[48:51]
	v_mfma_f32_16x16x128_f8f6f4 v[44:47], v[2:9], v[230:237], v[44:47]
	v_mfma_f32_16x16x128_f8f6f4 v[36:39], v[2:9], v[238:245], v[36:39]
	v_mfma_f32_16x16x128_f8f6f4 v[40:43], v[10:17], v[238:245], v[40:43]
	s_barrier
	s_setprio 2
	v_lshl_add_u64 v[18:19], s[26:27], 0, v[174:175]
	v_lshl_add_u64 v[20:21], s[26:27], 0, v[190:191]
	s_mov_b32 s63, 0
	s_mov_b64 s[30:31], 0
	s_branch .LBB0_821
.LBB0_820:
	ds_read_b128 v[204:207], v200
	ds_read_b128 v[208:211], v200 offset:1024
	ds_read_b128 v[222:225], v200 offset:2048
	ds_read_b128 v[226:229], v200 offset:3072
	ds_read_b128 v[10:13], v199
	ds_read_b128 v[14:17], v199 offset:1024
	ds_read_b128 v[2:5], v199 offset:2048
	ds_read_b128 v[6:9], v199 offset:3072
	s_add_u32 s14, s30, 0x200
	s_addc_u32 s86, s31, 0
	s_and_b64 s[40:41], s[36:37], exec
	s_cselect_b32 s14, 0, s14
	s_cselect_b32 s41, 0, s86
	s_add_u32 s40, s20, s14
	s_addc_u32 s41, s21, s41
	s_add_u32 s14, s81, s30
	s_addc_u32 s86, s82, s31
	s_and_b64 s[36:37], s[36:37], exec
	s_cselect_b32 s37, s23, s86
	s_cselect_b32 s36, s22, s14
	s_mov_b32 m0, s84
	v_lshl_add_u64 v[30:31], v[20:21], 0, s[30:31]
	ds_read_b128 v[22:25], v169
	ds_read_b128 v[26:29], v169 offset:1024
	ds_read_b128 v[230:233], v169 offset:2048
	ds_read_b128 v[234:237], v169 offset:3072
	ds_read_b128 v[238:241], v169 offset:4096
	ds_read_b128 v[242:245], v169 offset:5120
	ds_read_b128 v[178:181], v169 offset:6144
	ds_read_b128 v[182:185], v169 offset:7168
	global_load_lds_dwordx4 v[30:31], off
	v_lshl_add_u64 v[30:31], v[18:19], 0, s[30:31]
	s_mov_b32 m0, s53
	s_nop 0
	global_load_lds_dwordx4 v[30:31], off
	s_waitcnt vmcnt(8)
	s_waitcnt lgkmcnt(0)
	s_barrier
	v_mfma_f32_16x16x128_f8f6f4 v[160:163], v[204:211], v[22:29], v[160:163]
	s_setprio 1
	v_mfma_f32_16x16x128_f8f6f4 v[156:159], v[222:229], v[22:29], v[156:159]
	v_mfma_f32_16x16x128_f8f6f4 v[148:151], v[222:229], v[230:237], v[148:151]
	v_mfma_f32_16x16x128_f8f6f4 v[152:155], v[204:211], v[230:237], v[152:155]
	v_mfma_f32_16x16x128_f8f6f4 v[144:147], v[204:211], v[238:245], v[144:147]
	v_mfma_f32_16x16x128_f8f6f4 v[140:143], v[222:229], v[238:245], v[140:143]
	v_mfma_f32_16x16x128_f8f6f4 v[132:135], v[222:229], v[178:185], v[132:135]
	v_mfma_f32_16x16x128_f8f6f4 v[136:139], v[204:211], v[178:185], v[136:139]
	s_setprio 2
	s_setprio 1
	v_mfma_f32_16x16x128_f8f6f4 v[128:131], v[10:17], v[22:29], v[128:131]
	v_mfma_f32_16x16x128_f8f6f4 v[124:127], v[2:9], v[22:29], v[124:127]
	v_mfma_f32_16x16x128_f8f6f4 v[116:119], v[2:9], v[230:237], v[116:119]
	v_mfma_f32_16x16x128_f8f6f4 v[120:123], v[10:17], v[230:237], v[120:123]
	v_mfma_f32_16x16x128_f8f6f4 v[112:115], v[10:17], v[238:245], v[112:115]
	v_mfma_f32_16x16x128_f8f6f4 v[108:111], v[2:9], v[238:245], v[108:111]
	v_mfma_f32_16x16x128_f8f6f4 v[100:103], v[2:9], v[178:185], v[100:103]
	v_mfma_f32_16x16x128_f8f6f4 v[104:107], v[10:17], v[178:185], v[104:107]
	s_barrier
	s_setprio 2
	s_mov_b32 m0, s52
	v_lshl_add_u64 v[22:23], s[36:37], 0, v[170:171]
	s_add_u32 s86, s36, 0x20000
	ds_read_b128 v[178:181], v169 offset:16384
	ds_read_b128 v[182:185], v169 offset:17408
	ds_read_b128 v[230:233], v169 offset:18432
	ds_read_b128 v[234:237], v169 offset:19456
	ds_read_b128 v[238:241], v169 offset:20480
	ds_read_b128 v[242:245], v169 offset:21504
	ds_read_b128 v[212:215], v169 offset:22528
	ds_read_b128 v[216:219], v169 offset:23552
	global_load_lds_dwordx4 v[22:23], off
	v_lshl_add_u64 v[24:25], s[36:37], 0, v[172:173]
	s_mov_b32 m0, s85
	s_addc_u32 s87, s37, 0
	global_load_lds_dwordx4 v[24:25], off
	v_lshl_add_u64 v[26:27], s[86:87], 0, v[170:171]
	s_mov_b32 m0, s55
	v_mov_b32_e32 v193, v35
	global_load_lds_dwordx4 v[26:27], off
	v_lshl_add_u64 v[26:27], s[86:87], 0, v[172:173]
	s_mov_b32 m0, s65
	v_lshl_add_u64 v[28:29], s[40:41], 0, v[34:35]
	global_load_lds_dwordx4 v[26:27], off
	s_mov_b32 m0, s69
	v_lshl_add_u64 v[26:27], s[40:41], 0, v[192:193]
	global_load_lds_dwordx4 v34, s[40:41]
	s_mov_b32 m0, s70
	s_nop 0
	global_load_lds_dwordx4 v192, s[40:41]
	s_waitcnt vmcnt(8)
	s_waitcnt lgkmcnt(0)
	s_barrier
	v_mfma_f32_16x16x128_f8f6f4 v[96:99], v[204:211], v[178:185], v[96:99]
	s_setprio 1
	v_mfma_f32_16x16x128_f8f6f4 v[92:95], v[222:229], v[178:185], v[92:95]
	v_mfma_f32_16x16x128_f8f6f4 v[84:87], v[222:229], v[230:237], v[84:87]
	v_mfma_f32_16x16x128_f8f6f4 v[88:91], v[204:211], v[230:237], v[88:91]
	v_mfma_f32_16x16x128_f8f6f4 v[80:83], v[204:211], v[238:245], v[80:83]
	v_mfma_f32_16x16x128_f8f6f4 v[76:79], v[222:229], v[238:245], v[76:79]
	v_mfma_f32_16x16x128_f8f6f4 v[68:71], v[222:229], v[212:219], v[68:71]
	v_mfma_f32_16x16x128_f8f6f4 v[72:75], v[204:211], v[212:219], v[72:75]
	s_setprio 2
	s_setprio 1
	v_mfma_f32_16x16x128_f8f6f4 v[64:67], v[10:17], v[178:185], v[64:67]
	v_mfma_f32_16x16x128_f8f6f4 v[60:63], v[2:9], v[178:185], v[60:63]
	v_mfma_f32_16x16x128_f8f6f4 v[52:55], v[2:9], v[230:237], v[52:55]
	v_mfma_f32_16x16x128_f8f6f4 v[56:59], v[10:17], v[230:237], v[56:59]
	v_mfma_f32_16x16x128_f8f6f4 v[48:51], v[10:17], v[238:245], v[48:51]
	v_mfma_f32_16x16x128_f8f6f4 v[44:47], v[2:9], v[238:245], v[44:47]
	v_mfma_f32_16x16x128_f8f6f4 v[36:39], v[2:9], v[212:219], v[36:39]
	v_mfma_f32_16x16x128_f8f6f4 v[40:43], v[10:17], v[212:219], v[40:43]
	s_barrier
	s_setprio 2
	ds_read_b128 v[178:181], v201
	ds_read_b128 v[182:185], v201 offset:1024
	ds_read_b128 v[204:207], v201 offset:2048
	ds_read_b128 v[208:211], v201 offset:3072
	ds_read_b128 v[10:13], v202
	ds_read_b128 v[14:17], v202 offset:1024
	ds_read_b128 v[2:5], v202 offset:2048
	ds_read_b128 v[6:9], v202 offset:3072
	s_mov_b32 m0, s71
	ds_read_b128 v[212:215], v169 offset:32768
	ds_read_b128 v[216:219], v169 offset:33792
	ds_read_b128 v[222:225], v169 offset:34816
	ds_read_b128 v[226:229], v169 offset:35840
	ds_read_b128 v[230:233], v169 offset:36864
	ds_read_b128 v[234:237], v169 offset:37888
	ds_read_b128 v[238:241], v169 offset:38912
	ds_read_b128 v[242:245], v169 offset:39936
	global_load_lds_dwordx4 v189, s[40:41]
	s_mov_b32 m0, s72
	s_nop 0
	global_load_lds_dwordx4 v198, s[40:41]
	s_waitcnt vmcnt(8)
	s_waitcnt lgkmcnt(0)
	s_barrier
	v_mfma_f32_16x16x128_f8f6f4 v[160:163], v[178:185], v[212:219], v[160:163]
	s_setprio 1
	v_mfma_f32_16x16x128_f8f6f4 v[156:159], v[204:211], v[212:219], v[156:159]
	v_mfma_f32_16x16x128_f8f6f4 v[148:151], v[204:211], v[222:229], v[148:151]
	v_mfma_f32_16x16x128_f8f6f4 v[152:155], v[178:185], v[222:229], v[152:155]
	v_mfma_f32_16x16x128_f8f6f4 v[144:147], v[178:185], v[230:237], v[144:147]
	v_mfma_f32_16x16x128_f8f6f4 v[140:143], v[204:211], v[230:237], v[140:143]
	v_mfma_f32_16x16x128_f8f6f4 v[132:135], v[204:211], v[238:245], v[132:135]
	v_mfma_f32_16x16x128_f8f6f4 v[136:139], v[178:185], v[238:245], v[136:139]
	s_setprio 2
	s_setprio 1
	v_mfma_f32_16x16x128_f8f6f4 v[128:131], v[10:17], v[212:219], v[128:131]
	v_mfma_f32_16x16x128_f8f6f4 v[124:127], v[2:9], v[212:219], v[124:127]
	v_mfma_f32_16x16x128_f8f6f4 v[116:119], v[2:9], v[222:229], v[116:119]
	v_mfma_f32_16x16x128_f8f6f4 v[120:123], v[10:17], v[222:229], v[120:123]
	v_mfma_f32_16x16x128_f8f6f4 v[112:115], v[10:17], v[230:237], v[112:115]
	v_mfma_f32_16x16x128_f8f6f4 v[108:111], v[2:9], v[230:237], v[108:111]
	v_mfma_f32_16x16x128_f8f6f4 v[100:103], v[2:9], v[238:245], v[100:103]
	v_mfma_f32_16x16x128_f8f6f4 v[104:107], v[10:17], v[238:245], v[104:107]
	s_barrier
	s_setprio 2
	s_mov_b32 m0, s54
	v_lshl_add_u64 v[22:23], v[22:23], 0, s[18:19]
	s_add_u32 s36, s36, 0x20080
	ds_read_b128 v[212:215], v169 offset:49152
	ds_read_b128 v[216:219], v169 offset:50176
	ds_read_b128 v[222:225], v169 offset:51200
	ds_read_b128 v[226:229], v169 offset:52224
	ds_read_b128 v[230:233], v169 offset:53248
	ds_read_b128 v[234:237], v169 offset:54272
	ds_read_b128 v[238:241], v169 offset:55296
	ds_read_b128 v[242:245], v169 offset:56320
	global_load_lds_dwordx4 v[22:23], off
	v_lshl_add_u64 v[22:23], v[24:25], 0, s[18:19]
	s_mov_b32 m0, s50
	s_addc_u32 s37, s37, 0
	global_load_lds_dwordx4 v[22:23], off
	v_lshl_add_u64 v[22:23], s[36:37], 0, v[170:171]
	s_mov_b32 m0, s51
	s_nop 0
	global_load_lds_dwordx4 v[22:23], off
	v_lshl_add_u64 v[22:23], s[36:37], 0, v[172:173]
	s_mov_b32 m0, s64
	s_nop 0
	global_load_lds_dwordx4 v[22:23], off
	v_lshl_add_u64 v[22:23], v[28:29], 0, s[18:19]
	s_mov_b32 m0, s75
	s_nop 0
	global_load_lds_dwordx4 v[22:23], off
	v_lshl_add_u64 v[22:23], v[26:27], 0, s[18:19]
	s_mov_b32 m0, s76
	s_nop 0
	global_load_lds_dwordx4 v[22:23], off
	s_waitcnt vmcnt(8)
	s_waitcnt lgkmcnt(0)
	s_barrier
	v_mfma_f32_16x16x128_f8f6f4 v[96:99], v[178:185], v[212:219], v[96:99]
	s_setprio 1
	v_mfma_f32_16x16x128_f8f6f4 v[92:95], v[204:211], v[212:219], v[92:95]
	v_mfma_f32_16x16x128_f8f6f4 v[84:87], v[204:211], v[222:229], v[84:87]
	v_mfma_f32_16x16x128_f8f6f4 v[88:91], v[178:185], v[222:229], v[88:91]
	v_mfma_f32_16x16x128_f8f6f4 v[80:83], v[178:185], v[230:237], v[80:83]
	v_mfma_f32_16x16x128_f8f6f4 v[76:79], v[204:211], v[230:237], v[76:79]
	v_mfma_f32_16x16x128_f8f6f4 v[68:71], v[204:211], v[238:245], v[68:71]
	v_mfma_f32_16x16x128_f8f6f4 v[72:75], v[178:185], v[238:245], v[72:75]
	s_setprio 2
	s_setprio 1
	v_mfma_f32_16x16x128_f8f6f4 v[64:67], v[10:17], v[212:219], v[64:67]
	v_mfma_f32_16x16x128_f8f6f4 v[60:63], v[2:9], v[212:219], v[60:63]
	v_mfma_f32_16x16x128_f8f6f4 v[52:55], v[2:9], v[222:229], v[52:55]
	v_mfma_f32_16x16x128_f8f6f4 v[56:59], v[10:17], v[222:229], v[56:59]
	v_mfma_f32_16x16x128_f8f6f4 v[48:51], v[10:17], v[230:237], v[48:51]
	v_mfma_f32_16x16x128_f8f6f4 v[44:47], v[2:9], v[230:237], v[44:47]
	v_mfma_f32_16x16x128_f8f6f4 v[36:39], v[2:9], v[238:245], v[36:39]
	v_mfma_f32_16x16x128_f8f6f4 v[40:43], v[10:17], v[238:245], v[40:43]
	s_barrier
	s_setprio 2
	s_add_i32 s63, s63, 2
	s_add_u32 s30, s30, 0x100
	s_addc_u32 s31, s31, 0
	s_cmp_gt_u32 s63, 5
	s_cbranch_scc1 .LBB0_823

.LBB0_899:
	s_mul_i32 s14, s81, 0xe0000
	s_add_u32 s40, s44, s14
	s_addc_u32 s41, s45, 0
	s_and_b64 s[6:7], s[6:7], exec
	s_cselect_b32 s52, s41, s43
	s_cselect_b32 s53, s40, s42
	s_add_i32 s54, 0, 0x10000
	s_add_i32 s65, 0, 0x14000
	v_add_u32_e32 v34, s54, v167
	v_add_u32_e32 v206, s65, v167
	ds_read_b128 v[26:29], v34
	ds_read_b128 v[30:33], v34 offset:1024
	ds_read_b128 v[18:21], v34 offset:2048
	ds_read_b128 v[22:25], v34 offset:3072
	ds_read_b128 v[10:13], v206
	ds_read_b128 v[14:17], v206 offset:1024
	ds_read_b128 v[2:5], v206 offset:2048
	ds_read_b128 v[6:9], v206 offset:3072
	s_add_u32 s6, s42, 0x70080
	s_addc_u32 s7, s43, 0
	s_add_i32 s84, s72, 0xc000
	v_lshl_add_u64 v[216:217], s[6:7], 0, v[174:175]
	s_mov_b32 m0, s84
	s_add_i32 s85, s72, 0xe000
	ds_read_b128 v[178:181], v189
	ds_read_b128 v[182:185], v189 offset:1024
	ds_read_b128 v[198:201], v189 offset:2048
	ds_read_b128 v[202:205], v189 offset:3072
	ds_read_b128 v[208:211], v189 offset:4096
	ds_read_b128 v[212:215], v189 offset:5120
	ds_read_b128 v[222:225], v189 offset:6144
	ds_read_b128 v[226:229], v189 offset:7168
	global_load_lds_dwordx4 v[216:217], off
	v_lshl_add_u64 v[216:217], s[6:7], 0, v[170:171]
	s_mov_b32 m0, s85
	s_nop 0
	global_load_lds_dwordx4 v[216:217], off
	s_waitcnt vmcnt(8)
	s_waitcnt lgkmcnt(0)
	s_barrier
	v_mfma_f32_16x16x128_f8f6f4 v[160:163], v[26:33], v[178:185], 0
	s_setprio 1
	v_mfma_f32_16x16x128_f8f6f4 v[156:159], v[18:25], v[178:185], 0
	v_mfma_f32_16x16x128_f8f6f4 v[148:151], v[18:25], v[198:205], 0
	v_mfma_f32_16x16x128_f8f6f4 v[152:155], v[26:33], v[198:205], 0
	v_mfma_f32_16x16x128_f8f6f4 v[144:147], v[26:33], v[208:215], 0
	v_mfma_f32_16x16x128_f8f6f4 v[140:143], v[18:25], v[208:215], 0
	v_mfma_f32_16x16x128_f8f6f4 v[132:135], v[18:25], v[222:229], 0
	v_mfma_f32_16x16x128_f8f6f4 v[136:139], v[26:33], v[222:229], 0
	s_setprio 2
	s_setprio 1
	v_mfma_f32_16x16x128_f8f6f4 v[128:131], v[10:17], v[178:185], 0
	v_mfma_f32_16x16x128_f8f6f4 v[124:127], v[2:9], v[178:185], 0
	v_mfma_f32_16x16x128_f8f6f4 v[116:119], v[2:9], v[198:205], 0
	v_mfma_f32_16x16x128_f8f6f4 v[120:123], v[10:17], v[198:205], 0
	v_mfma_f32_16x16x128_f8f6f4 v[112:115], v[10:17], v[208:215], 0
	v_mfma_f32_16x16x128_f8f6f4 v[108:111], v[2:9], v[208:215], 0
	v_mfma_f32_16x16x128_f8f6f4 v[100:103], v[2:9], v[222:229], 0
	v_mfma_f32_16x16x128_f8f6f4 v[104:107], v[10:17], v[222:229], 0
	s_barrier
	s_setprio 2
	v_lshl_add_u64 v[198:199], v[196:197], 0, v[172:173]
	s_add_i32 s54, s54, s71
	v_lshl_add_u64 v[200:201], v[198:199], 0, s[28:29]
	s_mov_b32 m0, s54
	ds_read_b128 v[178:181], v189 offset:16384
	ds_read_b128 v[182:185], v189 offset:17408
	ds_read_b128 v[208:211], v189 offset:18432
	ds_read_b128 v[212:215], v189 offset:19456
	ds_read_b128 v[222:225], v189 offset:20480
	ds_read_b128 v[226:229], v189 offset:21504
	ds_read_b128 v[230:233], v189 offset:22528
	ds_read_b128 v[234:237], v189 offset:23552
	global_load_lds_dwordx4 v[200:201], off
	v_lshl_add_u64 v[200:201], v[196:197], 0, v[168:169]
	s_add_i32 s55, s54, 0x2000
	v_lshl_add_u64 v[202:203], v[200:201], 0, s[28:29]
	s_mov_b32 m0, s55
	s_mov_b64 s[6:7], 0x70100
	global_load_lds_dwordx4 v[202:203], off
	v_lshl_add_u64 v[202:203], v[196:197], 0, s[6:7]
	s_add_i32 s65, s65, s71
	v_lshl_add_u64 v[204:205], v[202:203], 0, v[172:173]
	s_mov_b32 m0, s65
	s_add_i32 s67, s65, 0x2000
	global_load_lds_dwordx4 v[204:205], off
	v_lshl_add_u64 v[202:203], v[202:203], 0, v[168:169]
	s_mov_b32 m0, s67
	s_nop 0
	global_load_lds_dwordx4 v[202:203], off
	v_lshl_add_u64 v[202:203], s[42:43], 0, v[174:175]
	v_lshl_add_u64 v[204:205], v[202:203], 0, s[28:29]
	s_mov_b32 m0, s72
	s_nop 0
	global_load_lds_dwordx4 v[204:205], off
	v_lshl_add_u64 v[204:205], s[42:43], 0, v[170:171]
	v_lshl_add_u64 v[216:217], v[204:205], 0, s[28:29]
	s_mov_b32 m0, s73
	s_nop 0
	global_load_lds_dwordx4 v[216:217], off
	s_waitcnt vmcnt(8)
	s_waitcnt lgkmcnt(0)
	s_barrier
	v_mfma_f32_16x16x128_f8f6f4 v[96:99], v[26:33], v[178:185], 0
	s_setprio 1
	v_mfma_f32_16x16x128_f8f6f4 v[92:95], v[18:25], v[178:185], 0
	v_mfma_f32_16x16x128_f8f6f4 v[84:87], v[18:25], v[208:215], 0
	v_mfma_f32_16x16x128_f8f6f4 v[88:91], v[26:33], v[208:215], 0
	v_mfma_f32_16x16x128_f8f6f4 v[80:83], v[26:33], v[222:229], 0
	v_mfma_f32_16x16x128_f8f6f4 v[76:79], v[18:25], v[222:229], 0
	v_mfma_f32_16x16x128_f8f6f4 v[68:71], v[18:25], v[230:237], 0
	v_mfma_f32_16x16x128_f8f6f4 v[72:75], v[26:33], v[230:237], 0
	s_setprio 2
	s_setprio 1
	v_mfma_f32_16x16x128_f8f6f4 v[64:67], v[10:17], v[178:185], 0
	v_mfma_f32_16x16x128_f8f6f4 v[60:63], v[2:9], v[178:185], 0
	v_mfma_f32_16x16x128_f8f6f4 v[52:55], v[2:9], v[208:215], 0
	v_mfma_f32_16x16x128_f8f6f4 v[56:59], v[10:17], v[208:215], 0
	v_mfma_f32_16x16x128_f8f6f4 v[48:51], v[10:17], v[222:229], 0
	v_mfma_f32_16x16x128_f8f6f4 v[44:47], v[2:9], v[222:229], 0
	v_mfma_f32_16x16x128_f8f6f4 v[36:39], v[2:9], v[230:237], 0
	v_mfma_f32_16x16x128_f8f6f4 v[40:43], v[10:17], v[230:237], 0
	s_barrier
	s_setprio 2
	s_add_i32 s50, 0, 0x18000
	s_add_i32 s63, 0, 0x1c000
	v_add_u32_e32 v207, s50, v167
	v_add_u32_e32 v208, s63, v167
	ds_read_b128 v[26:29], v207
	ds_read_b128 v[30:33], v207 offset:1024
	ds_read_b128 v[18:21], v207 offset:2048
	ds_read_b128 v[22:25], v207 offset:3072
	ds_read_b128 v[10:13], v208
	ds_read_b128 v[14:17], v208 offset:1024
	ds_read_b128 v[2:5], v208 offset:2048
	ds_read_b128 v[6:9], v208 offset:3072
	s_add_u32 s6, s42, 0x70100
	s_addc_u32 s7, s43, 0
	s_mov_b32 m0, s74
	v_lshl_add_u64 v[218:219], s[6:7], 0, v[174:175]
	ds_read_b128 v[178:181], v189 offset:32768
	ds_read_b128 v[182:185], v189 offset:33792
	ds_read_b128 v[210:213], v189 offset:34816
	ds_read_b128 v[214:217], v189 offset:35840
	ds_read_b128 v[222:225], v189 offset:36864
	ds_read_b128 v[226:229], v189 offset:37888
	ds_read_b128 v[230:233], v189 offset:38912
	ds_read_b128 v[234:237], v189 offset:39936
	global_load_lds_dwordx4 v[218:219], off
	v_lshl_add_u64 v[218:219], s[6:7], 0, v[170:171]
	s_mov_b32 m0, s75
	s_nop 0
	global_load_lds_dwordx4 v[218:219], off
	s_waitcnt vmcnt(8)
	s_waitcnt lgkmcnt(0)
	s_barrier
	v_mfma_f32_16x16x128_f8f6f4 v[160:163], v[26:33], v[178:185], v[160:163]
	s_setprio 1
	v_mfma_f32_16x16x128_f8f6f4 v[156:159], v[18:25], v[178:185], v[156:159]
	v_mfma_f32_16x16x128_f8f6f4 v[148:151], v[18:25], v[210:217], v[148:151]
	v_mfma_f32_16x16x128_f8f6f4 v[152:155], v[26:33], v[210:217], v[152:155]
	v_mfma_f32_16x16x128_f8f6f4 v[144:147], v[26:33], v[222:229], v[144:147]
	v_mfma_f32_16x16x128_f8f6f4 v[140:143], v[18:25], v[222:229], v[140:143]
	v_mfma_f32_16x16x128_f8f6f4 v[132:135], v[18:25], v[230:237], v[132:135]
	v_mfma_f32_16x16x128_f8f6f4 v[136:139], v[26:33], v[230:237], v[136:139]
	s_setprio 2
	s_setprio 1
	v_mfma_f32_16x16x128_f8f6f4 v[128:131], v[10:17], v[178:185], v[128:131]
	v_mfma_f32_16x16x128_f8f6f4 v[124:127], v[2:9], v[178:185], v[124:127]
	v_mfma_f32_16x16x128_f8f6f4 v[116:119], v[2:9], v[210:217], v[116:119]
	v_mfma_f32_16x16x128_f8f6f4 v[120:123], v[10:17], v[210:217], v[120:123]
	v_mfma_f32_16x16x128_f8f6f4 v[112:115], v[10:17], v[222:229], v[112:115]
	v_mfma_f32_16x16x128_f8f6f4 v[108:111], v[2:9], v[222:229], v[108:111]
	v_mfma_f32_16x16x128_f8f6f4 v[100:103], v[2:9], v[230:237], v[100:103]
	v_mfma_f32_16x16x128_f8f6f4 v[104:107], v[10:17], v[230:237], v[104:107]
	s_barrier
	s_setprio 2
	s_mov_b64 s[6:7], 0x180
	s_add_i32 s50, s50, s71
	v_lshl_add_u64 v[198:199], v[198:199], 0, s[6:7]
	s_mov_b32 m0, s50
	s_add_i32 s51, s50, 0x2000
	ds_read_b128 v[178:181], v189 offset:49152
	ds_read_b128 v[182:185], v189 offset:50176
	ds_read_b128 v[210:213], v189 offset:51200
	ds_read_b128 v[214:217], v189 offset:52224
	ds_read_b128 v[222:225], v189 offset:53248
	ds_read_b128 v[226:229], v189 offset:54272
	ds_read_b128 v[230:233], v189 offset:55296
	ds_read_b128 v[234:237], v189 offset:56320
	global_load_lds_dwordx4 v[198:199], off
	v_lshl_add_u64 v[198:199], v[200:201], 0, s[6:7]
	s_mov_b32 m0, s51
	s_add_i32 s63, s63, s71
	global_load_lds_dwordx4 v[198:199], off
	v_lshl_add_u64 v[198:199], v[196:197], 0, s[26:27]
	v_lshl_add_u64 v[200:201], v[198:199], 0, v[172:173]
	s_mov_b32 m0, s63
	s_add_i32 s64, s63, 0x2000
	global_load_lds_dwordx4 v[200:201], off
	v_lshl_add_u64 v[198:199], v[198:199], 0, v[168:169]
	s_mov_b32 m0, s64
	s_nop 0
	global_load_lds_dwordx4 v[198:199], off
	v_lshl_add_u64 v[198:199], v[202:203], 0, s[6:7]
	s_mov_b32 m0, s77
	s_nop 0
	global_load_lds_dwordx4 v[198:199], off
	v_lshl_add_u64 v[198:199], v[204:205], 0, s[6:7]
	s_mov_b32 m0, s78
	s_nop 0
	global_load_lds_dwordx4 v[198:199], off
	s_waitcnt vmcnt(8)
	s_waitcnt lgkmcnt(0)
	s_barrier
	v_mfma_f32_16x16x128_f8f6f4 v[96:99], v[26:33], v[178:185], v[96:99]
	s_setprio 1
	v_mfma_f32_16x16x128_f8f6f4 v[92:95], v[18:25], v[178:185], v[92:95]
	v_mfma_f32_16x16x128_f8f6f4 v[84:87], v[18:25], v[210:217], v[84:87]
	v_mfma_f32_16x16x128_f8f6f4 v[88:91], v[26:33], v[210:217], v[88:91]
	v_mfma_f32_16x16x128_f8f6f4 v[80:83], v[26:33], v[222:229], v[80:83]
	v_mfma_f32_16x16x128_f8f6f4 v[76:79], v[18:25], v[222:229], v[76:79]
	v_mfma_f32_16x16x128_f8f6f4 v[68:71], v[18:25], v[230:237], v[68:71]
	v_mfma_f32_16x16x128_f8f6f4 v[72:75], v[26:33], v[230:237], v[72:75]
	s_setprio 2
	s_setprio 1
	v_mfma_f32_16x16x128_f8f6f4 v[64:67], v[10:17], v[178:185], v[64:67]
	v_mfma_f32_16x16x128_f8f6f4 v[60:63], v[2:9], v[178:185], v[60:63]
	v_mfma_f32_16x16x128_f8f6f4 v[52:55], v[2:9], v[210:217], v[52:55]
	v_mfma_f32_16x16x128_f8f6f4 v[56:59], v[10:17], v[210:217], v[56:59]
	v_mfma_f32_16x16x128_f8f6f4 v[48:51], v[10:17], v[222:229], v[48:51]
	v_mfma_f32_16x16x128_f8f6f4 v[44:47], v[2:9], v[222:229], v[44:47]
	v_mfma_f32_16x16x128_f8f6f4 v[36:39], v[2:9], v[230:237], v[36:39]
	v_mfma_f32_16x16x128_f8f6f4 v[40:43], v[10:17], v[230:237], v[40:43]
	s_barrier
	s_setprio 2
	s_mov_b64 s[6:7], 0x200
	v_lshl_add_u64 v[18:19], v[196:197], 0, s[6:7]
	s_mov_b32 s86, 0
.LBB0_900:
	ds_read_b128 v[2:5], v34
	ds_read_b128 v[6:9], v34 offset:1024
	ds_read_b128 v[10:13], v34 offset:2048
	ds_read_b128 v[14:17], v34 offset:3072
	ds_read_b128 v[178:181], v206
	ds_read_b128 v[182:185], v206 offset:1024
	ds_read_b128 v[196:199], v206 offset:2048
	ds_read_b128 v[200:203], v206 offset:3072
	s_add_u32 s6, s42, 0x200
	s_addc_u32 s7, s43, 0
	s_cmp_eq_u32 s86, 24
	s_cselect_b64 vcc, -1, 0
	s_cselect_b32 s7, s52, s7
	s_cselect_b32 s6, s53, s6
	v_cndmask_b32_e32 v21, v19, v195, vcc
	v_cndmask_b32_e32 v20, v18, v194, vcc
	s_mov_b32 m0, s84
	v_lshl_add_u64 v[30:31], s[42:43], 0, v[190:191]
	ds_read_b128 v[22:25], v189
	ds_read_b128 v[26:29], v189 offset:1024
	ds_read_b128 v[210:213], v189 offset:2048
	ds_read_b128 v[214:217], v189 offset:3072
	ds_read_b128 v[222:225], v189 offset:4096
	ds_read_b128 v[226:229], v189 offset:5120
	ds_read_b128 v[230:233], v189 offset:6144
	ds_read_b128 v[234:237], v189 offset:7168
	global_load_lds_dwordx4 v[30:31], off
	v_lshl_add_u64 v[30:31], s[42:43], 0, v[192:193]
	s_mov_b32 m0, s85
	s_nop 0
	global_load_lds_dwordx4 v[30:31], off
	s_waitcnt vmcnt(8)
	s_waitcnt lgkmcnt(0)
	s_barrier
	v_mfma_f32_16x16x128_f8f6f4 v[160:163], v[2:9], v[22:29], v[160:163]
	s_setprio 1
	v_mfma_f32_16x16x128_f8f6f4 v[156:159], v[10:17], v[22:29], v[156:159]
	v_mfma_f32_16x16x128_f8f6f4 v[148:151], v[10:17], v[210:217], v[148:151]
	v_mfma_f32_16x16x128_f8f6f4 v[152:155], v[2:9], v[210:217], v[152:155]
	v_mfma_f32_16x16x128_f8f6f4 v[144:147], v[2:9], v[222:229], v[144:147]
	v_mfma_f32_16x16x128_f8f6f4 v[140:143], v[10:17], v[222:229], v[140:143]
	v_mfma_f32_16x16x128_f8f6f4 v[132:135], v[10:17], v[230:237], v[132:135]
	v_mfma_f32_16x16x128_f8f6f4 v[136:139], v[2:9], v[230:237], v[136:139]
	s_setprio 2
	s_setprio 1
	v_mfma_f32_16x16x128_f8f6f4 v[128:131], v[178:185], v[22:29], v[128:131]
	v_mfma_f32_16x16x128_f8f6f4 v[124:127], v[196:203], v[22:29], v[124:127]
	v_mfma_f32_16x16x128_f8f6f4 v[116:119], v[196:203], v[210:217], v[116:119]
	v_mfma_f32_16x16x128_f8f6f4 v[120:123], v[178:185], v[210:217], v[120:123]
	v_mfma_f32_16x16x128_f8f6f4 v[112:115], v[178:185], v[222:229], v[112:115]
	v_mfma_f32_16x16x128_f8f6f4 v[108:111], v[196:203], v[222:229], v[108:111]
	v_mfma_f32_16x16x128_f8f6f4 v[100:103], v[196:203], v[230:237], v[100:103]
	v_mfma_f32_16x16x128_f8f6f4 v[104:107], v[178:185], v[230:237], v[104:107]
	s_barrier
	s_setprio 2
	s_mov_b32 m0, s54
	v_lshl_add_u64 v[22:23], v[20:21], 0, v[172:173]
	ds_read_b128 v[210:213], v189 offset:16384
	ds_read_b128 v[214:217], v189 offset:17408
	ds_read_b128 v[222:225], v189 offset:18432
	ds_read_b128 v[226:229], v189 offset:19456
	ds_read_b128 v[230:233], v189 offset:20480
	ds_read_b128 v[234:237], v189 offset:21504
	ds_read_b128 v[238:241], v189 offset:22528
	ds_read_b128 v[242:245], v189 offset:23552
	global_load_lds_dwordx4 v[22:23], off
	v_lshl_add_u64 v[24:25], v[20:21], 0, v[168:169]
	s_mov_b32 m0, s55
	v_lshl_add_u64 v[26:27], v[20:21], 0, s[2:3]
	global_load_lds_dwordx4 v[24:25], off
	v_lshl_add_u64 v[28:29], v[26:27], 0, v[172:173]
	s_mov_b32 m0, s65
	v_lshl_add_u64 v[26:27], v[26:27], 0, v[168:169]
	global_load_lds_dwordx4 v[28:29], off
	s_mov_b32 m0, s67
	v_lshl_add_u64 v[28:29], s[6:7], 0, v[170:171]
	global_load_lds_dwordx4 v[26:27], off
	v_lshl_add_u64 v[26:27], s[6:7], 0, v[174:175]
	s_mov_b32 m0, s72
	s_nop 0
	global_load_lds_dwordx4 v[26:27], off
	s_mov_b32 m0, s73
	s_nop 0
	global_load_lds_dwordx4 v[28:29], off
	s_waitcnt vmcnt(8)
	s_waitcnt lgkmcnt(0)
	s_barrier
	v_mfma_f32_16x16x128_f8f6f4 v[96:99], v[2:9], v[210:217], v[96:99]
	s_setprio 1
	v_mfma_f32_16x16x128_f8f6f4 v[92:95], v[10:17], v[210:217], v[92:95]
	v_mfma_f32_16x16x128_f8f6f4 v[84:87], v[10:17], v[222:229], v[84:87]
	v_mfma_f32_16x16x128_f8f6f4 v[88:91], v[2:9], v[222:229], v[88:91]
	v_mfma_f32_16x16x128_f8f6f4 v[80:83], v[2:9], v[230:237], v[80:83]
	v_mfma_f32_16x16x128_f8f6f4 v[76:79], v[10:17], v[230:237], v[76:79]
	v_mfma_f32_16x16x128_f8f6f4 v[68:71], v[10:17], v[238:245], v[68:71]
	v_mfma_f32_16x16x128_f8f6f4 v[72:75], v[2:9], v[238:245], v[72:75]
	s_setprio 2
	s_setprio 1
	v_mfma_f32_16x16x128_f8f6f4 v[64:67], v[178:185], v[210:217], v[64:67]
	v_mfma_f32_16x16x128_f8f6f4 v[60:63], v[196:203], v[210:217], v[60:63]
	v_mfma_f32_16x16x128_f8f6f4 v[52:55], v[196:203], v[222:229], v[52:55]
	v_mfma_f32_16x16x128_f8f6f4 v[56:59], v[178:185], v[222:229], v[56:59]
	v_mfma_f32_16x16x128_f8f6f4 v[48:51], v[178:185], v[230:237], v[48:51]
	v_mfma_f32_16x16x128_f8f6f4 v[44:47], v[196:203], v[230:237], v[44:47]
	v_mfma_f32_16x16x128_f8f6f4 v[36:39], v[196:203], v[238:245], v[36:39]
	v_mfma_f32_16x16x128_f8f6f4 v[40:43], v[178:185], v[238:245], v[40:43]
	s_barrier
	s_setprio 2
	ds_read_b128 v[178:181], v207
	ds_read_b128 v[182:185], v207 offset:1024
	ds_read_b128 v[196:199], v207 offset:2048
	ds_read_b128 v[200:203], v207 offset:3072
	ds_read_b128 v[10:13], v208
	ds_read_b128 v[14:17], v208 offset:1024
	ds_read_b128 v[2:5], v208 offset:2048
	ds_read_b128 v[6:9], v208 offset:3072
	s_add_u32 s6, s6, 0x70000
	s_addc_u32 s7, s7, 0
	s_mov_b32 m0, s74
	v_lshl_add_u64 v[30:31], s[6:7], 0, v[174:175]
	ds_read_b128 v[210:213], v189 offset:32768
	ds_read_b128 v[214:217], v189 offset:33792
	ds_read_b128 v[222:225], v189 offset:34816
	ds_read_b128 v[226:229], v189 offset:35840
	ds_read_b128 v[230:233], v189 offset:36864
	ds_read_b128 v[234:237], v189 offset:37888
	ds_read_b128 v[238:241], v189 offset:38912
	ds_read_b128 v[242:245], v189 offset:39936
	global_load_lds_dwordx4 v[30:31], off
	v_lshl_add_u64 v[30:31], s[6:7], 0, v[170:171]
	s_mov_b32 m0, s75
	s_nop 0
	global_load_lds_dwordx4 v[30:31], off
	s_waitcnt vmcnt(8)
	s_waitcnt lgkmcnt(0)
	s_barrier
	v_mfma_f32_16x16x128_f8f6f4 v[160:163], v[178:185], v[210:217], v[160:163]
	s_setprio 1
	v_mfma_f32_16x16x128_f8f6f4 v[156:159], v[196:203], v[210:217], v[156:159]
	v_mfma_f32_16x16x128_f8f6f4 v[148:151], v[196:203], v[222:229], v[148:151]
	v_mfma_f32_16x16x128_f8f6f4 v[152:155], v[178:185], v[222:229], v[152:155]
	v_mfma_f32_16x16x128_f8f6f4 v[144:147], v[178:185], v[230:237], v[144:147]
	v_mfma_f32_16x16x128_f8f6f4 v[140:143], v[196:203], v[230:237], v[140:143]
	v_mfma_f32_16x16x128_f8f6f4 v[132:135], v[196:203], v[238:245], v[132:135]
	v_mfma_f32_16x16x128_f8f6f4 v[136:139], v[178:185], v[238:245], v[136:139]
	s_setprio 2
	s_setprio 1
	v_mfma_f32_16x16x128_f8f6f4 v[128:131], v[10:17], v[210:217], v[128:131]
	v_mfma_f32_16x16x128_f8f6f4 v[124:127], v[2:9], v[210:217], v[124:127]
	v_mfma_f32_16x16x128_f8f6f4 v[116:119], v[2:9], v[222:229], v[116:119]
	v_mfma_f32_16x16x128_f8f6f4 v[120:123], v[10:17], v[222:229], v[120:123]
	v_mfma_f32_16x16x128_f8f6f4 v[112:115], v[10:17], v[230:237], v[112:115]
	v_mfma_f32_16x16x128_f8f6f4 v[108:111], v[2:9], v[230:237], v[108:111]
	v_mfma_f32_16x16x128_f8f6f4 v[100:103], v[2:9], v[238:245], v[100:103]
	v_mfma_f32_16x16x128_f8f6f4 v[104:107], v[10:17], v[238:245], v[104:107]
	s_barrier
	s_setprio 2
	s_mov_b32 m0, s50
	v_lshl_add_u64 v[22:23], v[22:23], 0, s[18:19]
	ds_read_b128 v[210:213], v189 offset:49152
	ds_read_b128 v[214:217], v189 offset:50176
	ds_read_b128 v[222:225], v189 offset:51200
	ds_read_b128 v[226:229], v189 offset:52224
	ds_read_b128 v[230:233], v189 offset:53248
	ds_read_b128 v[234:237], v189 offset:54272
	ds_read_b128 v[238:241], v189 offset:55296
	ds_read_b128 v[242:245], v189 offset:56320
	global_load_lds_dwordx4 v[22:23], off
	v_lshl_add_u64 v[22:23], v[24:25], 0, s[18:19]
	s_mov_b32 m0, s51
	v_lshl_add_u64 v[20:21], v[20:21], 0, s[34:35]
	global_load_lds_dwordx4 v[22:23], off
	v_lshl_add_u64 v[22:23], v[20:21], 0, v[172:173]
	s_mov_b32 m0, s63
	v_lshl_add_u64 v[20:21], v[20:21], 0, v[168:169]
	global_load_lds_dwordx4 v[22:23], off
	s_mov_b32 m0, s64
	s_nop 0
	global_load_lds_dwordx4 v[20:21], off
	v_lshl_add_u64 v[20:21], v[26:27], 0, s[18:19]
	s_mov_b32 m0, s77
	s_nop 0
	global_load_lds_dwordx4 v[20:21], off
	v_lshl_add_u64 v[20:21], v[28:29], 0, s[18:19]
	s_mov_b32 m0, s78
	s_nop 0
	global_load_lds_dwordx4 v[20:21], off
	s_waitcnt vmcnt(8)
	s_waitcnt lgkmcnt(0)
	s_barrier
	v_mfma_f32_16x16x128_f8f6f4 v[96:99], v[178:185], v[210:217], v[96:99]
	s_setprio 1
	v_mfma_f32_16x16x128_f8f6f4 v[92:95], v[196:203], v[210:217], v[92:95]
	v_mfma_f32_16x16x128_f8f6f4 v[84:87], v[196:203], v[222:229], v[84:87]
	v_mfma_f32_16x16x128_f8f6f4 v[88:91], v[178:185], v[222:229], v[88:91]
	v_mfma_f32_16x16x128_f8f6f4 v[80:83], v[178:185], v[230:237], v[80:83]
	v_mfma_f32_16x16x128_f8f6f4 v[76:79], v[196:203], v[230:237], v[76:79]
	v_mfma_f32_16x16x128_f8f6f4 v[68:71], v[196:203], v[238:245], v[68:71]
	v_mfma_f32_16x16x128_f8f6f4 v[72:75], v[178:185], v[238:245], v[72:75]
	s_setprio 2
	s_setprio 1
	v_mfma_f32_16x16x128_f8f6f4 v[64:67], v[10:17], v[210:217], v[64:67]
	v_mfma_f32_16x16x128_f8f6f4 v[60:63], v[2:9], v[210:217], v[60:63]
	v_mfma_f32_16x16x128_f8f6f4 v[52:55], v[2:9], v[222:229], v[52:55]
	v_mfma_f32_16x16x128_f8f6f4 v[56:59], v[10:17], v[222:229], v[56:59]
	v_mfma_f32_16x16x128_f8f6f4 v[48:51], v[10:17], v[230:237], v[48:51]
	v_mfma_f32_16x16x128_f8f6f4 v[44:47], v[2:9], v[230:237], v[44:47]
	v_mfma_f32_16x16x128_f8f6f4 v[36:39], v[2:9], v[238:245], v[36:39]
	v_mfma_f32_16x16x128_f8f6f4 v[40:43], v[10:17], v[238:245], v[40:43]
	s_barrier
	s_setprio 2
	s_add_i32 s86, s86, 2
	s_add_u32 s42, s42, 0x100
	s_addc_u32 s43, s43, 0
	s_cmp_gt_u32 s86, 25
	v_lshl_add_u64 v[18:19], v[18:19], 0, s[28:29]
	s_cbranch_scc0 .LBB0_900
	s_and_b64 vcc, exec, s[36:37]
	s_mov_b64 s[84:85], s[24:25]
	s_cbranch_vccz .LBB0_903
	s_barrier

.LBB0_953:
	s_add_u32 s95, s30, 0x200
	s_addc_u32 s96, s31, 0
	s_add_i32 s65, 0, 0x14000
	s_add_i32 s67, 0, 0x10000
	v_add_u32_e32 v199, s65, v167
	v_add_u32_e32 v200, s67, v167
	ds_read_b128 v[10:13], v199
	ds_read_b128 v[14:17], v199 offset:1024
	ds_read_b128 v[2:5], v199 offset:2048
	ds_read_b128 v[6:9], v199 offset:3072
	ds_read_b128 v[22:25], v200 offset:3072
	ds_read_b128 v[18:21], v200 offset:2048
	ds_read_b128 v[30:33], v200 offset:1024
	ds_read_b128 v[26:29], v200
	s_lshl_b32 s14, s94, 10
	s_add_i32 s97, s14, 0
	s_add_i32 s97, s97, 0x20400
	v_mov_b32_e32 v191, v35
	v_mov_b32_e32 v175, v35
	s_add_i32 s83, s52, 0xc000
	v_readlane_b32 s26, v253, 28
	s_mov_b32 m0, s83
	v_readlane_b32 s27, v253, 29
	s_add_i32 s53, s52, 0xe000
	ds_read_b128 v[178:181], v169
	ds_read_b128 v[182:185], v169 offset:1024
	ds_read_b128 v[202:205], v169 offset:2048
	ds_read_b128 v[206:209], v169 offset:3072
	ds_read_b128 v[210:213], v169 offset:4096
	ds_read_b128 v[214:217], v169 offset:5120
	ds_read_b128 v[222:225], v169 offset:6144
	ds_read_b128 v[226:229], v169 offset:7168
	global_load_lds_dwordx4 v190, s[26:27]
	s_mov_b32 m0, s53
	s_nop 0
	global_load_lds_dwordx4 v174, s[26:27]
	s_waitcnt vmcnt(8)
	s_waitcnt lgkmcnt(0)
	s_barrier
	v_mfma_f32_16x16x128_f8f6f4 v[160:163], v[26:33], v[178:185], 0
	s_setprio 1
	v_mfma_f32_16x16x128_f8f6f4 v[156:159], v[18:25], v[178:185], 0
	v_mfma_f32_16x16x128_f8f6f4 v[148:151], v[18:25], v[202:209], 0
	v_mfma_f32_16x16x128_f8f6f4 v[152:155], v[26:33], v[202:209], 0
	v_mfma_f32_16x16x128_f8f6f4 v[144:147], v[26:33], v[210:217], 0
	v_mfma_f32_16x16x128_f8f6f4 v[140:143], v[18:25], v[210:217], 0
	v_mfma_f32_16x16x128_f8f6f4 v[132:135], v[18:25], v[222:229], 0
	v_mfma_f32_16x16x128_f8f6f4 v[136:139], v[26:33], v[222:229], 0
	s_setprio 2
	s_setprio 1
	v_mfma_f32_16x16x128_f8f6f4 v[128:131], v[10:17], v[178:185], 0
	v_mfma_f32_16x16x128_f8f6f4 v[124:127], v[2:9], v[178:185], 0
	v_mfma_f32_16x16x128_f8f6f4 v[116:119], v[2:9], v[202:209], 0
	v_mfma_f32_16x16x128_f8f6f4 v[120:123], v[10:17], v[202:209], 0
	v_mfma_f32_16x16x128_f8f6f4 v[112:115], v[10:17], v[210:217], 0
	v_mfma_f32_16x16x128_f8f6f4 v[108:111], v[2:9], v[210:217], 0
	v_mfma_f32_16x16x128_f8f6f4 v[100:103], v[2:9], v[222:229], 0
	v_mfma_f32_16x16x128_f8f6f4 v[104:107], v[10:17], v[222:229], 0
	s_barrier
	s_setprio 2
	v_lshl_add_u64 v[194:195], s[30:31], 0, v[170:171]
	s_add_i32 s67, s67, s82
	v_lshl_add_u64 v[196:197], v[194:195], 0, s[28:29]
	s_mov_b32 m0, s67
	s_add_i32 s55, s67, 0x2000
	ds_read_b128 v[178:181], v169 offset:16384
	ds_read_b128 v[182:185], v169 offset:17408
	ds_read_b128 v[202:205], v169 offset:18432
	ds_read_b128 v[206:209], v169 offset:19456
	ds_read_b128 v[210:213], v169 offset:20480
	ds_read_b128 v[214:217], v169 offset:21504
	ds_read_b128 v[222:225], v169 offset:22528
	ds_read_b128 v[226:229], v169 offset:23552
	global_load_lds_dwordx4 v[196:197], off
	v_lshl_add_u64 v[196:197], s[30:31], 0, v[172:173]
	s_add_u32 s46, s30, 0x20100
	v_lshl_add_u64 v[218:219], v[196:197], 0, s[28:29]
	s_mov_b32 m0, s55
	s_addc_u32 s47, s31, 0
	s_add_i32 s65, s65, s82
	global_load_lds_dwordx4 v[218:219], off
	v_lshl_add_u64 v[218:219], s[46:47], 0, v[170:171]
	s_mov_b32 m0, s65
	s_add_i32 s54, s65, 0x2000
	global_load_lds_dwordx4 v[218:219], off
	v_lshl_add_u64 v[218:219], s[46:47], 0, v[172:173]
	s_mov_b32 m0, s54
	v_readlane_b32 s26, v253, 37
	global_load_lds_dwordx4 v[218:219], off
	s_mov_b32 m0, s52
	v_readlane_b32 s27, v253, 38
	s_nop 4
	global_load_lds_dwordx4 v34, s[26:27]
	s_mov_b32 m0, s84
	s_nop 0
	global_load_lds_dwordx4 v192, s[26:27]
	s_waitcnt vmcnt(8)
	s_waitcnt lgkmcnt(0)
	s_barrier
	v_mfma_f32_16x16x128_f8f6f4 v[96:99], v[26:33], v[178:185], 0
	s_setprio 1
	v_mfma_f32_16x16x128_f8f6f4 v[92:95], v[18:25], v[178:185], 0
	v_mfma_f32_16x16x128_f8f6f4 v[84:87], v[18:25], v[202:209], 0
	v_mfma_f32_16x16x128_f8f6f4 v[88:91], v[26:33], v[202:209], 0
	v_mfma_f32_16x16x128_f8f6f4 v[80:83], v[26:33], v[210:217], 0
	v_mfma_f32_16x16x128_f8f6f4 v[76:79], v[18:25], v[210:217], 0
	v_mfma_f32_16x16x128_f8f6f4 v[68:71], v[18:25], v[222:229], 0
	v_mfma_f32_16x16x128_f8f6f4 v[72:75], v[26:33], v[222:229], 0
	s_setprio 2
	s_setprio 1
	v_mfma_f32_16x16x128_f8f6f4 v[64:67], v[10:17], v[178:185], 0
	v_mfma_f32_16x16x128_f8f6f4 v[60:63], v[2:9], v[178:185], 0
	v_mfma_f32_16x16x128_f8f6f4 v[52:55], v[2:9], v[202:209], 0
	v_mfma_f32_16x16x128_f8f6f4 v[56:59], v[10:17], v[202:209], 0
	v_mfma_f32_16x16x128_f8f6f4 v[48:51], v[10:17], v[210:217], 0
	v_mfma_f32_16x16x128_f8f6f4 v[44:47], v[2:9], v[210:217], 0
	v_mfma_f32_16x16x128_f8f6f4 v[36:39], v[2:9], v[222:229], 0
	v_mfma_f32_16x16x128_f8f6f4 v[40:43], v[10:17], v[222:229], 0
	s_barrier
	s_setprio 2
	s_add_i32 s50, 0, 0x18000
	s_add_i32 s64, 0, 0x1c000
	v_add_u32_e32 v201, s50, v167
	v_add_u32_e32 v202, s64, v167
	ds_read_b128 v[26:29], v201
	ds_read_b128 v[30:33], v201 offset:1024
	ds_read_b128 v[18:21], v201 offset:2048
	ds_read_b128 v[22:25], v201 offset:3072
	ds_read_b128 v[10:13], v202
	ds_read_b128 v[14:17], v202 offset:1024
	ds_read_b128 v[2:5], v202 offset:2048
	ds_read_b128 v[6:9], v202 offset:3072
	s_mov_b32 m0, s85
	ds_read_b128 v[178:181], v169 offset:32768
	ds_read_b128 v[182:185], v169 offset:33792
	ds_read_b128 v[204:207], v169 offset:34816
	ds_read_b128 v[208:211], v169 offset:35840
	ds_read_b128 v[212:215], v169 offset:36864
	ds_read_b128 v[216:219], v169 offset:37888
	ds_read_b128 v[222:225], v169 offset:38912
	ds_read_b128 v[226:229], v169 offset:39936
	global_load_lds_dwordx4 v189, s[26:27]
	s_mov_b32 m0, s86
	s_nop 0
	global_load_lds_dwordx4 v198, s[26:27]
	s_waitcnt vmcnt(8)
	s_waitcnt lgkmcnt(0)
	s_barrier
	v_mfma_f32_16x16x128_f8f6f4 v[160:163], v[26:33], v[178:185], v[160:163]
	s_setprio 1
	v_mfma_f32_16x16x128_f8f6f4 v[156:159], v[18:25], v[178:185], v[156:159]
	v_mfma_f32_16x16x128_f8f6f4 v[148:151], v[18:25], v[204:211], v[148:151]
	v_mfma_f32_16x16x128_f8f6f4 v[152:155], v[26:33], v[204:211], v[152:155]
	v_mfma_f32_16x16x128_f8f6f4 v[144:147], v[26:33], v[212:219], v[144:147]
	v_mfma_f32_16x16x128_f8f6f4 v[140:143], v[18:25], v[212:219], v[140:143]
	v_mfma_f32_16x16x128_f8f6f4 v[132:135], v[18:25], v[222:229], v[132:135]
	v_mfma_f32_16x16x128_f8f6f4 v[136:139], v[26:33], v[222:229], v[136:139]
	s_setprio 2
	s_setprio 1
	v_mfma_f32_16x16x128_f8f6f4 v[128:131], v[10:17], v[178:185], v[128:131]
	v_mfma_f32_16x16x128_f8f6f4 v[124:127], v[2:9], v[178:185], v[124:127]
	v_mfma_f32_16x16x128_f8f6f4 v[116:119], v[2:9], v[204:211], v[116:119]
	v_mfma_f32_16x16x128_f8f6f4 v[120:123], v[10:17], v[204:211], v[120:123]
	v_mfma_f32_16x16x128_f8f6f4 v[112:115], v[10:17], v[212:219], v[112:115]
	v_mfma_f32_16x16x128_f8f6f4 v[108:111], v[2:9], v[212:219], v[108:111]
	v_mfma_f32_16x16x128_f8f6f4 v[100:103], v[2:9], v[222:229], v[100:103]
	v_mfma_f32_16x16x128_f8f6f4 v[104:107], v[10:17], v[222:229], v[104:107]
	s_barrier
	s_setprio 2
	s_add_i32 s50, s50, s82
	s_mov_b64 s[26:27], 0x180
	s_add_i32 s51, s50, 0x2000
	v_lshl_add_u64 v[194:195], v[194:195], 0, s[26:27]
	s_mov_b32 m0, s50
	s_add_u32 s30, s30, 0x20180
	ds_read_b128 v[178:181], v169 offset:49152
	ds_read_b128 v[182:185], v169 offset:50176
	ds_read_b128 v[204:207], v169 offset:51200
	ds_read_b128 v[208:211], v169 offset:52224
	ds_read_b128 v[212:215], v169 offset:53248
	ds_read_b128 v[216:219], v169 offset:54272
	ds_read_b128 v[222:225], v169 offset:55296
	ds_read_b128 v[226:229], v169 offset:56320
	global_load_lds_dwordx4 v[194:195], off
	v_lshl_add_u64 v[194:195], v[196:197], 0, s[26:27]
	s_mov_b32 m0, s51
	s_addc_u32 s31, s31, 0
	s_add_i32 s64, s64, s82
	global_load_lds_dwordx4 v[194:195], off
	v_lshl_add_u64 v[194:195], s[30:31], 0, v[170:171]
	s_mov_b32 m0, s64
	s_add_i32 s63, s64, 0x2000
	global_load_lds_dwordx4 v[194:195], off
	v_lshl_add_u64 v[194:195], s[30:31], 0, v[172:173]
	s_mov_b32 m0, s63
	v_readlane_b32 s26, v253, 39
	global_load_lds_dwordx4 v[194:195], off
	s_mov_b32 m0, s90
	v_readlane_b32 s27, v253, 40
	s_nop 4
	global_load_lds_dwordx4 v34, s[26:27]
	s_mov_b32 m0, s91
	s_nop 0
	global_load_lds_dwordx4 v192, s[26:27]
	s_waitcnt vmcnt(8)
	s_waitcnt lgkmcnt(0)
	s_barrier
	v_mfma_f32_16x16x128_f8f6f4 v[96:99], v[26:33], v[178:185], v[96:99]
	s_setprio 1
	v_mfma_f32_16x16x128_f8f6f4 v[92:95], v[18:25], v[178:185], v[92:95]
	v_mfma_f32_16x16x128_f8f6f4 v[84:87], v[18:25], v[204:211], v[84:87]
	v_mfma_f32_16x16x128_f8f6f4 v[88:91], v[26:33], v[204:211], v[88:91]
	v_mfma_f32_16x16x128_f8f6f4 v[80:83], v[26:33], v[212:219], v[80:83]
	v_mfma_f32_16x16x128_f8f6f4 v[76:79], v[18:25], v[212:219], v[76:79]
	v_mfma_f32_16x16x128_f8f6f4 v[68:71], v[18:25], v[222:229], v[68:71]
	v_mfma_f32_16x16x128_f8f6f4 v[72:75], v[26:33], v[222:229], v[72:75]
	s_setprio 2
	s_setprio 1
	v_mfma_f32_16x16x128_f8f6f4 v[64:67], v[10:17], v[178:185], v[64:67]
	v_mfma_f32_16x16x128_f8f6f4 v[60:63], v[2:9], v[178:185], v[60:63]
	v_mfma_f32_16x16x128_f8f6f4 v[52:55], v[2:9], v[204:211], v[52:55]
	v_mfma_f32_16x16x128_f8f6f4 v[56:59], v[10:17], v[204:211], v[56:59]
	v_mfma_f32_16x16x128_f8f6f4 v[48:51], v[10:17], v[212:219], v[48:51]
	v_mfma_f32_16x16x128_f8f6f4 v[44:47], v[2:9], v[212:219], v[44:47]
	v_mfma_f32_16x16x128_f8f6f4 v[36:39], v[2:9], v[222:229], v[36:39]
	v_mfma_f32_16x16x128_f8f6f4 v[40:43], v[10:17], v[222:229], v[40:43]
	s_barrier
	s_setprio 2
	v_lshl_add_u64 v[18:19], s[26:27], 0, v[174:175]
	v_lshl_add_u64 v[20:21], s[26:27], 0, v[190:191]
	s_mov_b32 s75, 0
	s_mov_b64 s[30:31], 0
	s_branch .LBB0_955
.LBB0_954:
	ds_read_b128 v[178:181], v200
	ds_read_b128 v[182:185], v200 offset:1024
	ds_read_b128 v[204:207], v200 offset:2048
	ds_read_b128 v[208:211], v200 offset:3072
	ds_read_b128 v[10:13], v199
	ds_read_b128 v[14:17], v199 offset:1024
	ds_read_b128 v[2:5], v199 offset:2048
	ds_read_b128 v[6:9], v199 offset:3072
	s_add_u32 s14, s30, 0x200
	s_addc_u32 vcc_lo, s31, 0
	s_and_b64 s[48:49], s[46:47], exec
	s_cselect_b32 s14, 0, s14
	s_cselect_b32 s49, 0, vcc_lo
	s_add_u32 s48, s20, s14
	s_addc_u32 s49, s21, s49
	s_add_u32 s14, s95, s30
	s_addc_u32 vcc_lo, s96, s31
	s_and_b64 s[46:47], s[46:47], exec
	s_cselect_b32 s47, s43, vcc_lo
	s_cselect_b32 s46, s42, s14
	s_mov_b32 m0, s83
	v_lshl_add_u64 v[30:31], v[20:21], 0, s[30:31]
	ds_read_b128 v[22:25], v169
	ds_read_b128 v[26:29], v169 offset:1024
	ds_read_b128 v[212:215], v169 offset:2048
	ds_read_b128 v[216:219], v169 offset:3072
	ds_read_b128 v[222:225], v169 offset:4096
	ds_read_b128 v[226:229], v169 offset:5120
	ds_read_b128 v[230:233], v169 offset:6144
	ds_read_b128 v[234:237], v169 offset:7168
	global_load_lds_dwordx4 v[30:31], off
	v_lshl_add_u64 v[30:31], v[18:19], 0, s[30:31]
	s_mov_b32 m0, s53
	s_nop 0
	global_load_lds_dwordx4 v[30:31], off
	s_waitcnt vmcnt(8)
	s_waitcnt lgkmcnt(0)
	s_barrier
	v_mfma_f32_16x16x128_f8f6f4 v[160:163], v[178:185], v[22:29], v[160:163]
	s_setprio 1
	v_mfma_f32_16x16x128_f8f6f4 v[156:159], v[204:211], v[22:29], v[156:159]
	v_mfma_f32_16x16x128_f8f6f4 v[148:151], v[204:211], v[212:219], v[148:151]
	v_mfma_f32_16x16x128_f8f6f4 v[152:155], v[178:185], v[212:219], v[152:155]
	v_mfma_f32_16x16x128_f8f6f4 v[144:147], v[178:185], v[222:229], v[144:147]
	v_mfma_f32_16x16x128_f8f6f4 v[140:143], v[204:211], v[222:229], v[140:143]
	v_mfma_f32_16x16x128_f8f6f4 v[132:135], v[204:211], v[230:237], v[132:135]
	v_mfma_f32_16x16x128_f8f6f4 v[136:139], v[178:185], v[230:237], v[136:139]
	s_setprio 2
	s_setprio 1
	v_mfma_f32_16x16x128_f8f6f4 v[128:131], v[10:17], v[22:29], v[128:131]
	v_mfma_f32_16x16x128_f8f6f4 v[124:127], v[2:9], v[22:29], v[124:127]
	v_mfma_f32_16x16x128_f8f6f4 v[116:119], v[2:9], v[212:219], v[116:119]
	v_mfma_f32_16x16x128_f8f6f4 v[120:123], v[10:17], v[212:219], v[120:123]
	v_mfma_f32_16x16x128_f8f6f4 v[112:115], v[10:17], v[222:229], v[112:115]
	v_mfma_f32_16x16x128_f8f6f4 v[108:111], v[2:9], v[222:229], v[108:111]
	v_mfma_f32_16x16x128_f8f6f4 v[100:103], v[2:9], v[230:237], v[100:103]
	v_mfma_f32_16x16x128_f8f6f4 v[104:107], v[10:17], v[230:237], v[104:107]
	s_barrier
	s_setprio 2
	s_mov_b32 m0, s67
	v_lshl_add_u64 v[22:23], s[46:47], 0, v[170:171]
	s_add_u32 vcc_lo, s46, 0x20000
	ds_read_b128 v[212:215], v169 offset:16384
	ds_read_b128 v[216:219], v169 offset:17408
	ds_read_b128 v[222:225], v169 offset:18432
	ds_read_b128 v[226:229], v169 offset:19456
	ds_read_b128 v[230:233], v169 offset:20480
	ds_read_b128 v[234:237], v169 offset:21504
	ds_read_b128 v[238:241], v169 offset:22528
	ds_read_b128 v[242:245], v169 offset:23552
	global_load_lds_dwordx4 v[22:23], off
	v_lshl_add_u64 v[24:25], s[46:47], 0, v[172:173]
	s_mov_b32 m0, s55
	s_addc_u32 vcc_hi, s47, 0
	global_load_lds_dwordx4 v[24:25], off
	v_lshl_add_u64 v[26:27], vcc, 0, v[170:171]
	s_mov_b32 m0, s65
	v_mov_b32_e32 v193, v35
	global_load_lds_dwordx4 v[26:27], off
	v_lshl_add_u64 v[26:27], vcc, 0, v[172:173]
	s_mov_b32 m0, s54
	v_lshl_add_u64 v[28:29], s[48:49], 0, v[34:35]
	global_load_lds_dwordx4 v[26:27], off
	s_mov_b32 m0, s52
	v_lshl_add_u64 v[26:27], s[48:49], 0, v[192:193]
	global_load_lds_dwordx4 v34, s[48:49]
	s_mov_b32 m0, s84
	s_nop 0
	global_load_lds_dwordx4 v192, s[48:49]
	s_waitcnt vmcnt(8)
	s_waitcnt lgkmcnt(0)
	s_barrier
	v_mfma_f32_16x16x128_f8f6f4 v[96:99], v[178:185], v[212:219], v[96:99]
	s_setprio 1
	v_mfma_f32_16x16x128_f8f6f4 v[92:95], v[204:211], v[212:219], v[92:95]
	v_mfma_f32_16x16x128_f8f6f4 v[84:87], v[204:211], v[222:229], v[84:87]
	v_mfma_f32_16x16x128_f8f6f4 v[88:91], v[178:185], v[222:229], v[88:91]
	v_mfma_f32_16x16x128_f8f6f4 v[80:83], v[178:185], v[230:237], v[80:83]
	v_mfma_f32_16x16x128_f8f6f4 v[76:79], v[204:211], v[230:237], v[76:79]
	v_mfma_f32_16x16x128_f8f6f4 v[68:71], v[204:211], v[238:245], v[68:71]
	v_mfma_f32_16x16x128_f8f6f4 v[72:75], v[178:185], v[238:245], v[72:75]
	s_setprio 2
	s_setprio 1
	v_mfma_f32_16x16x128_f8f6f4 v[64:67], v[10:17], v[212:219], v[64:67]
	v_mfma_f32_16x16x128_f8f6f4 v[60:63], v[2:9], v[212:219], v[60:63]
	v_mfma_f32_16x16x128_f8f6f4 v[52:55], v[2:9], v[222:229], v[52:55]
	v_mfma_f32_16x16x128_f8f6f4 v[56:59], v[10:17], v[222:229], v[56:59]
	v_mfma_f32_16x16x128_f8f6f4 v[48:51], v[10:17], v[230:237], v[48:51]
	v_mfma_f32_16x16x128_f8f6f4 v[44:47], v[2:9], v[230:237], v[44:47]
	v_mfma_f32_16x16x128_f8f6f4 v[36:39], v[2:9], v[238:245], v[36:39]
	v_mfma_f32_16x16x128_f8f6f4 v[40:43], v[10:17], v[238:245], v[40:43]
	s_barrier
	s_setprio 2
	ds_read_b128 v[178:181], v201
	ds_read_b128 v[182:185], v201 offset:1024
	ds_read_b128 v[204:207], v201 offset:2048
	ds_read_b128 v[208:211], v201 offset:3072
	ds_read_b128 v[10:13], v202
	ds_read_b128 v[14:17], v202 offset:1024
	ds_read_b128 v[2:5], v202 offset:2048
	ds_read_b128 v[6:9], v202 offset:3072
	s_mov_b32 m0, s85
	ds_read_b128 v[212:215], v169 offset:32768
	ds_read_b128 v[216:219], v169 offset:33792
	ds_read_b128 v[222:225], v169 offset:34816
	ds_read_b128 v[226:229], v169 offset:35840
	ds_read_b128 v[230:233], v169 offset:36864
	ds_read_b128 v[234:237], v169 offset:37888
	ds_read_b128 v[238:241], v169 offset:38912
	ds_read_b128 v[242:245], v169 offset:39936
	global_load_lds_dwordx4 v189, s[48:49]
	s_mov_b32 m0, s86
	s_nop 0
	global_load_lds_dwordx4 v198, s[48:49]
	s_waitcnt vmcnt(8)
	s_waitcnt lgkmcnt(0)
	s_barrier
	v_mfma_f32_16x16x128_f8f6f4 v[160:163], v[178:185], v[212:219], v[160:163]
	s_setprio 1
	v_mfma_f32_16x16x128_f8f6f4 v[156:159], v[204:211], v[212:219], v[156:159]
	v_mfma_f32_16x16x128_f8f6f4 v[148:151], v[204:211], v[222:229], v[148:151]
	v_mfma_f32_16x16x128_f8f6f4 v[152:155], v[178:185], v[222:229], v[152:155]
	v_mfma_f32_16x16x128_f8f6f4 v[144:147], v[178:185], v[230:237], v[144:147]
	v_mfma_f32_16x16x128_f8f6f4 v[140:143], v[204:211], v[230:237], v[140:143]
	v_mfma_f32_16x16x128_f8f6f4 v[132:135], v[204:211], v[238:245], v[132:135]
	v_mfma_f32_16x16x128_f8f6f4 v[136:139], v[178:185], v[238:245], v[136:139]
	s_setprio 2
	s_setprio 1
	v_mfma_f32_16x16x128_f8f6f4 v[128:131], v[10:17], v[212:219], v[128:131]
	v_mfma_f32_16x16x128_f8f6f4 v[124:127], v[2:9], v[212:219], v[124:127]
	v_mfma_f32_16x16x128_f8f6f4 v[116:119], v[2:9], v[222:229], v[116:119]
	v_mfma_f32_16x16x128_f8f6f4 v[120:123], v[10:17], v[222:229], v[120:123]
	v_mfma_f32_16x16x128_f8f6f4 v[112:115], v[10:17], v[230:237], v[112:115]
	v_mfma_f32_16x16x128_f8f6f4 v[108:111], v[2:9], v[230:237], v[108:111]
	v_mfma_f32_16x16x128_f8f6f4 v[100:103], v[2:9], v[238:245], v[100:103]
	v_mfma_f32_16x16x128_f8f6f4 v[104:107], v[10:17], v[238:245], v[104:107]
	s_barrier
	s_setprio 2
	s_mov_b32 m0, s50
	v_lshl_add_u64 v[22:23], v[22:23], 0, s[18:19]
	s_add_u32 s46, s46, 0x20080
	ds_read_b128 v[212:215], v169 offset:49152
	ds_read_b128 v[216:219], v169 offset:50176
	ds_read_b128 v[222:225], v169 offset:51200
	ds_read_b128 v[226:229], v169 offset:52224
	ds_read_b128 v[230:233], v169 offset:53248
	ds_read_b128 v[234:237], v169 offset:54272
	ds_read_b128 v[238:241], v169 offset:55296
	ds_read_b128 v[242:245], v169 offset:56320
	global_load_lds_dwordx4 v[22:23], off
	v_lshl_add_u64 v[22:23], v[24:25], 0, s[18:19]
	s_mov_b32 m0, s51
	s_addc_u32 s47, s47, 0
	global_load_lds_dwordx4 v[22:23], off
	v_lshl_add_u64 v[22:23], s[46:47], 0, v[170:171]
	s_mov_b32 m0, s64
	s_nop 0
	global_load_lds_dwordx4 v[22:23], off
	v_lshl_add_u64 v[22:23], s[46:47], 0, v[172:173]
	s_mov_b32 m0, s63
	s_nop 0
	global_load_lds_dwordx4 v[22:23], off
	v_lshl_add_u64 v[22:23], v[28:29], 0, s[18:19]
	s_mov_b32 m0, s90
	s_nop 0
	global_load_lds_dwordx4 v[22:23], off
	v_lshl_add_u64 v[22:23], v[26:27], 0, s[18:19]
	s_mov_b32 m0, s91
	s_nop 0
	global_load_lds_dwordx4 v[22:23], off
	s_waitcnt vmcnt(8)
	s_waitcnt lgkmcnt(0)
	s_barrier
	v_mfma_f32_16x16x128_f8f6f4 v[96:99], v[178:185], v[212:219], v[96:99]
	s_setprio 1
	v_mfma_f32_16x16x128_f8f6f4 v[92:95], v[204:211], v[212:219], v[92:95]
	v_mfma_f32_16x16x128_f8f6f4 v[84:87], v[204:211], v[222:229], v[84:87]
	v_mfma_f32_16x16x128_f8f6f4 v[88:91], v[178:185], v[222:229], v[88:91]
	v_mfma_f32_16x16x128_f8f6f4 v[80:83], v[178:185], v[230:237], v[80:83]
	v_mfma_f32_16x16x128_f8f6f4 v[76:79], v[204:211], v[230:237], v[76:79]
	v_mfma_f32_16x16x128_f8f6f4 v[68:71], v[204:211], v[238:245], v[68:71]
	v_mfma_f32_16x16x128_f8f6f4 v[72:75], v[178:185], v[238:245], v[72:75]
	s_setprio 2
	s_setprio 1
	v_mfma_f32_16x16x128_f8f6f4 v[64:67], v[10:17], v[212:219], v[64:67]
	v_mfma_f32_16x16x128_f8f6f4 v[60:63], v[2:9], v[212:219], v[60:63]
	v_mfma_f32_16x16x128_f8f6f4 v[52:55], v[2:9], v[222:229], v[52:55]
	v_mfma_f32_16x16x128_f8f6f4 v[56:59], v[10:17], v[222:229], v[56:59]
	v_mfma_f32_16x16x128_f8f6f4 v[48:51], v[10:17], v[230:237], v[48:51]
	v_mfma_f32_16x16x128_f8f6f4 v[44:47], v[2:9], v[230:237], v[44:47]
	v_mfma_f32_16x16x128_f8f6f4 v[36:39], v[2:9], v[238:245], v[36:39]
	v_mfma_f32_16x16x128_f8f6f4 v[40:43], v[10:17], v[238:245], v[40:43]
	s_barrier
	s_setprio 2
	s_add_i32 s75, s75, 2
	s_add_u32 s30, s30, 0x100
	s_addc_u32 s31, s31, 0
	s_cmp_gt_u32 s75, 5
	s_cbranch_scc1 .LBB0_957

.LBB0_1086:
	s_lshl_b32 s10, s51, 18
	s_add_u32 s10, s20, s10
	s_addc_u32 s11, s21, 0
	s_and_b64 s[16:17], s[4:5], exec
	s_cselect_b32 s54, s11, s31
	s_cselect_b32 s55, s10, s30
	s_lshl_b32 s14, s50, 18
	s_add_u32 s16, s15, s14
	s_addc_u32 s17, s26, 0
	s_and_b64 s[36:37], s[4:5], exec
	s_cselect_b32 s56, s17, s23
	s_cselect_b32 s57, s16, s22
	s_add_i32 s60, 0, 0x10000
	s_add_i32 s62, 0, 0x14000
	v_add_u32_e32 v198, s60, v196
	v_add_u32_e32 v199, s62, v196
	ds_read_b128 v[26:29], v198
	ds_read_b128 v[30:33], v198 offset:1024
	ds_read_b128 v[18:21], v198 offset:2048
	ds_read_b128 v[22:25], v198 offset:3072
	ds_read_b128 v[10:13], v199
	ds_read_b128 v[14:17], v199 offset:1024
	ds_read_b128 v[2:5], v199 offset:2048
	ds_read_b128 v[6:9], v199 offset:3072
	s_add_u32 s36, s30, 0x20080
	s_addc_u32 s37, s31, 0
	s_add_i32 s58, s41, 0xc000
	v_lshl_add_u64 v[174:175], s[36:37], 0, v[168:169]
	s_mov_b32 m0, s58
	s_add_i32 s59, s41, 0xe000
	ds_read_b128 v[200:203], v197
	ds_read_b128 v[204:207], v197 offset:1024
	ds_read_b128 v[222:225], v197 offset:2048
	ds_read_b128 v[226:229], v197 offset:3072
	ds_read_b128 v[230:233], v197 offset:4096
	ds_read_b128 v[234:237], v197 offset:5120
	ds_read_b128 v[238:241], v197 offset:6144
	ds_read_b128 v[242:245], v197 offset:7168
	global_load_lds_dwordx4 v[174:175], off
	v_lshl_add_u64 v[174:175], s[36:37], 0, v[166:167]
	s_mov_b32 m0, s59
	s_nop 0
	global_load_lds_dwordx4 v[174:175], off
	s_waitcnt vmcnt(8)
	s_waitcnt lgkmcnt(0)
	s_barrier
	v_mfma_f32_16x16x128_f8f6f4 v[160:163], v[26:33], v[200:207], 0
	s_setprio 1
	v_mfma_f32_16x16x128_f8f6f4 v[156:159], v[18:25], v[200:207], 0
	v_mfma_f32_16x16x128_f8f6f4 v[148:151], v[18:25], v[222:229], 0
	v_mfma_f32_16x16x128_f8f6f4 v[152:155], v[26:33], v[222:229], 0
	v_mfma_f32_16x16x128_f8f6f4 v[144:147], v[26:33], v[230:237], 0
	v_mfma_f32_16x16x128_f8f6f4 v[140:143], v[18:25], v[230:237], 0
	v_mfma_f32_16x16x128_f8f6f4 v[132:135], v[18:25], v[238:245], 0
	v_mfma_f32_16x16x128_f8f6f4 v[136:139], v[26:33], v[238:245], 0
	s_setprio 2
	s_setprio 1
	v_mfma_f32_16x16x128_f8f6f4 v[128:131], v[10:17], v[200:207], 0
	v_mfma_f32_16x16x128_f8f6f4 v[124:127], v[2:9], v[200:207], 0
	v_mfma_f32_16x16x128_f8f6f4 v[116:119], v[2:9], v[222:229], 0
	v_mfma_f32_16x16x128_f8f6f4 v[120:123], v[10:17], v[222:229], 0
	v_mfma_f32_16x16x128_f8f6f4 v[112:115], v[10:17], v[230:237], 0
	v_mfma_f32_16x16x128_f8f6f4 v[108:111], v[2:9], v[230:237], 0
	v_mfma_f32_16x16x128_f8f6f4 v[100:103], v[2:9], v[238:245], 0
	v_mfma_f32_16x16x128_f8f6f4 v[104:107], v[10:17], v[238:245], 0
	s_barrier
	s_setprio 2
	s_add_i32 s60, s60, s40
	v_lshl_add_u64 v[174:175], s[22:23], 0, v[34:35]
	s_add_i32 s61, s60, 0x2000
	v_lshl_add_u64 v[178:179], v[174:175], 0, s[28:29]
	s_mov_b32 m0, s60
	v_lshl_add_u64 v[190:191], s[22:23], 0, v[164:165]
	s_add_u32 s36, s22, 0x20100
	ds_read_b128 v[200:203], v197 offset:16384
	ds_read_b128 v[204:207], v197 offset:17408
	ds_read_b128 v[222:225], v197 offset:18432
	ds_read_b128 v[226:229], v197 offset:19456
	ds_read_b128 v[230:233], v197 offset:20480
	ds_read_b128 v[234:237], v197 offset:21504
	ds_read_b128 v[238:241], v197 offset:22528
	ds_read_b128 v[242:245], v197 offset:23552
	global_load_lds_dwordx4 v[178:179], off
	v_lshl_add_u64 v[178:179], v[190:191], 0, s[28:29]
	s_mov_b32 m0, s61
	s_addc_u32 s37, s23, 0
	s_add_i32 s62, s62, s40
	global_load_lds_dwordx4 v[178:179], off
	v_lshl_add_u64 v[178:179], s[36:37], 0, v[34:35]
	s_mov_b32 m0, s62
	s_add_i32 s63, s62, 0x2000
	global_load_lds_dwordx4 v[178:179], off
	v_lshl_add_u64 v[178:179], s[36:37], 0, v[164:165]
	s_mov_b32 m0, s63
	v_lshl_add_u64 v[192:193], s[30:31], 0, v[168:169]
	global_load_lds_dwordx4 v[178:179], off
	v_lshl_add_u64 v[178:179], v[192:193], 0, s[28:29]
	s_mov_b32 m0, s41
	v_lshl_add_u64 v[194:195], s[30:31], 0, v[166:167]
	global_load_lds_dwordx4 v[178:179], off
	v_lshl_add_u64 v[178:179], v[194:195], 0, s[28:29]
	s_mov_b32 m0, s42
	s_nop 0
	global_load_lds_dwordx4 v[178:179], off
	s_waitcnt vmcnt(8)
	s_waitcnt lgkmcnt(0)
	s_barrier
	v_mfma_f32_16x16x128_f8f6f4 v[96:99], v[26:33], v[200:207], 0
	s_setprio 1
	v_mfma_f32_16x16x128_f8f6f4 v[92:95], v[18:25], v[200:207], 0
	v_mfma_f32_16x16x128_f8f6f4 v[84:87], v[18:25], v[222:229], 0
	v_mfma_f32_16x16x128_f8f6f4 v[88:91], v[26:33], v[222:229], 0
	v_mfma_f32_16x16x128_f8f6f4 v[80:83], v[26:33], v[230:237], 0
	v_mfma_f32_16x16x128_f8f6f4 v[76:79], v[18:25], v[230:237], 0
	v_mfma_f32_16x16x128_f8f6f4 v[68:71], v[18:25], v[238:245], 0
	v_mfma_f32_16x16x128_f8f6f4 v[72:75], v[26:33], v[238:245], 0
	s_setprio 2
	s_setprio 1
	v_mfma_f32_16x16x128_f8f6f4 v[64:67], v[10:17], v[200:207], 0
	v_mfma_f32_16x16x128_f8f6f4 v[60:63], v[2:9], v[200:207], 0
	v_mfma_f32_16x16x128_f8f6f4 v[52:55], v[2:9], v[222:229], 0
	v_mfma_f32_16x16x128_f8f6f4 v[56:59], v[10:17], v[222:229], 0
	v_mfma_f32_16x16x128_f8f6f4 v[48:51], v[10:17], v[230:237], 0
	v_mfma_f32_16x16x128_f8f6f4 v[44:47], v[2:9], v[230:237], 0
	v_mfma_f32_16x16x128_f8f6f4 v[36:39], v[2:9], v[238:245], 0
	v_mfma_f32_16x16x128_f8f6f4 v[40:43], v[10:17], v[238:245], 0
	s_barrier
	s_setprio 2
	s_add_i32 s64, 0, 0x18000
	s_add_i32 s66, 0, 0x1c000
	v_add_u32_e32 v200, s64, v196
	v_add_u32_e32 v201, s66, v196
	ds_read_b128 v[26:29], v200
	ds_read_b128 v[30:33], v200 offset:1024
	ds_read_b128 v[18:21], v200 offset:2048
	ds_read_b128 v[22:25], v200 offset:3072
	ds_read_b128 v[10:13], v201
	ds_read_b128 v[14:17], v201 offset:1024
	ds_read_b128 v[2:5], v201 offset:2048
	ds_read_b128 v[6:9], v201 offset:3072
	s_add_u32 s36, s30, 0x20100
	s_addc_u32 s37, s31, 0
	s_mov_b32 m0, s43
	v_lshl_add_u64 v[178:179], s[36:37], 0, v[168:169]
	ds_read_b128 v[202:205], v197 offset:32768
	ds_read_b128 v[206:209], v197 offset:33792
	ds_read_b128 v[222:225], v197 offset:34816
	ds_read_b128 v[226:229], v197 offset:35840
	ds_read_b128 v[230:233], v197 offset:36864
	ds_read_b128 v[234:237], v197 offset:37888
	ds_read_b128 v[238:241], v197 offset:38912
	ds_read_b128 v[242:245], v197 offset:39936
	global_load_lds_dwordx4 v[178:179], off
	v_lshl_add_u64 v[178:179], s[36:37], 0, v[166:167]
	s_mov_b32 m0, s44
	s_nop 0
	global_load_lds_dwordx4 v[178:179], off
	s_waitcnt vmcnt(8)
	s_waitcnt lgkmcnt(0)
	s_barrier
	v_mfma_f32_16x16x128_f8f6f4 v[160:163], v[26:33], v[202:209], v[160:163]
	s_setprio 1
	v_mfma_f32_16x16x128_f8f6f4 v[156:159], v[18:25], v[202:209], v[156:159]
	v_mfma_f32_16x16x128_f8f6f4 v[148:151], v[18:25], v[222:229], v[148:151]
	v_mfma_f32_16x16x128_f8f6f4 v[152:155], v[26:33], v[222:229], v[152:155]
	v_mfma_f32_16x16x128_f8f6f4 v[144:147], v[26:33], v[230:237], v[144:147]
	v_mfma_f32_16x16x128_f8f6f4 v[140:143], v[18:25], v[230:237], v[140:143]
	v_mfma_f32_16x16x128_f8f6f4 v[132:135], v[18:25], v[238:245], v[132:135]
	v_mfma_f32_16x16x128_f8f6f4 v[136:139], v[26:33], v[238:245], v[136:139]
	s_setprio 2
	s_setprio 1
	v_mfma_f32_16x16x128_f8f6f4 v[128:131], v[10:17], v[202:209], v[128:131]
	v_mfma_f32_16x16x128_f8f6f4 v[124:127], v[2:9], v[202:209], v[124:127]
	v_mfma_f32_16x16x128_f8f6f4 v[116:119], v[2:9], v[222:229], v[116:119]
	v_mfma_f32_16x16x128_f8f6f4 v[120:123], v[10:17], v[222:229], v[120:123]
	v_mfma_f32_16x16x128_f8f6f4 v[112:115], v[10:17], v[230:237], v[112:115]
	v_mfma_f32_16x16x128_f8f6f4 v[108:111], v[2:9], v[230:237], v[108:111]
	v_mfma_f32_16x16x128_f8f6f4 v[100:103], v[2:9], v[238:245], v[100:103]
	v_mfma_f32_16x16x128_f8f6f4 v[104:107], v[10:17], v[238:245], v[104:107]
	s_barrier
	s_setprio 2
	s_add_i32 s64, s64, s40
	s_mov_b64 s[24:25], 0x180
	s_add_i32 s65, s64, 0x2000
	v_lshl_add_u64 v[174:175], v[174:175], 0, s[24:25]
	s_mov_b32 m0, s64
	s_add_u32 s36, s22, 0x20180
	ds_read_b128 v[202:205], v197 offset:49152
	ds_read_b128 v[206:209], v197 offset:50176
	ds_read_b128 v[222:225], v197 offset:51200
	ds_read_b128 v[226:229], v197 offset:52224
	ds_read_b128 v[230:233], v197 offset:53248
	ds_read_b128 v[234:237], v197 offset:54272
	ds_read_b128 v[238:241], v197 offset:55296
	ds_read_b128 v[242:245], v197 offset:56320
	global_load_lds_dwordx4 v[174:175], off
	v_lshl_add_u64 v[174:175], v[190:191], 0, s[24:25]
	s_mov_b32 m0, s65
	s_addc_u32 s37, s23, 0
	s_add_i32 s66, s66, s40
	global_load_lds_dwordx4 v[174:175], off
	v_lshl_add_u64 v[174:175], s[36:37], 0, v[34:35]
	s_mov_b32 m0, s66
	s_add_i32 s67, s66, 0x2000
	global_load_lds_dwordx4 v[174:175], off
	v_lshl_add_u64 v[174:175], s[36:37], 0, v[164:165]
	s_mov_b32 m0, s67
	s_nop 0
	global_load_lds_dwordx4 v[174:175], off
	v_lshl_add_u64 v[174:175], v[192:193], 0, s[24:25]
	s_mov_b32 m0, s47
	s_nop 0
	global_load_lds_dwordx4 v[174:175], off
	v_lshl_add_u64 v[174:175], v[194:195], 0, s[24:25]
	s_mov_b32 m0, s48
	s_nop 0
	global_load_lds_dwordx4 v[174:175], off
	s_waitcnt vmcnt(8)
	s_waitcnt lgkmcnt(0)
	s_barrier
	v_mfma_f32_16x16x128_f8f6f4 v[96:99], v[26:33], v[202:209], v[96:99]
	s_setprio 1
	v_mfma_f32_16x16x128_f8f6f4 v[92:95], v[18:25], v[202:209], v[92:95]
	v_mfma_f32_16x16x128_f8f6f4 v[84:87], v[18:25], v[222:229], v[84:87]
	v_mfma_f32_16x16x128_f8f6f4 v[88:91], v[26:33], v[222:229], v[88:91]
	v_mfma_f32_16x16x128_f8f6f4 v[80:83], v[26:33], v[230:237], v[80:83]
	v_mfma_f32_16x16x128_f8f6f4 v[76:79], v[18:25], v[230:237], v[76:79]
	v_mfma_f32_16x16x128_f8f6f4 v[68:71], v[18:25], v[238:245], v[68:71]
	v_mfma_f32_16x16x128_f8f6f4 v[72:75], v[26:33], v[238:245], v[72:75]
	s_setprio 2
	s_setprio 1
	v_mfma_f32_16x16x128_f8f6f4 v[64:67], v[10:17], v[202:209], v[64:67]
	v_mfma_f32_16x16x128_f8f6f4 v[60:63], v[2:9], v[202:209], v[60:63]
	v_mfma_f32_16x16x128_f8f6f4 v[52:55], v[2:9], v[222:229], v[52:55]
	v_mfma_f32_16x16x128_f8f6f4 v[56:59], v[10:17], v[222:229], v[56:59]
	v_mfma_f32_16x16x128_f8f6f4 v[48:51], v[10:17], v[230:237], v[48:51]
	v_mfma_f32_16x16x128_f8f6f4 v[44:47], v[2:9], v[230:237], v[44:47]
	v_mfma_f32_16x16x128_f8f6f4 v[36:39], v[2:9], v[238:245], v[36:39]
	v_mfma_f32_16x16x128_f8f6f4 v[40:43], v[10:17], v[238:245], v[40:43]
	s_barrier
	s_setprio 2
	s_add_u32 s30, s30, 0x20180
	s_addc_u32 s31, s31, 0
	s_add_u32 s68, s22, 0x200
	s_addc_u32 s69, s23, 0
	s_mov_b32 s70, 0
.LBB0_1087:
	ds_read_b128 v[2:5], v198
	ds_read_b128 v[6:9], v198 offset:1024
	ds_read_b128 v[10:13], v198 offset:2048
	ds_read_b128 v[14:17], v198 offset:3072
	ds_read_b128 v[18:21], v199
	ds_read_b128 v[22:25], v199 offset:1024
	ds_read_b128 v[26:29], v199 offset:2048
	ds_read_b128 v[30:33], v199 offset:3072
	s_add_u32 s14, s30, 0xfffe0080
	s_addc_u32 s22, s31, -1
	s_cmp_eq_u32 s70, 4
	s_cselect_b32 s37, s54, s22
	s_cselect_b32 s36, s55, s14
	s_cselect_b32 s23, s56, s69
	s_cselect_b32 s22, s57, s68
	s_mov_b32 m0, s58
	v_lshl_add_u64 v[174:175], s[30:31], 0, v[170:171]
	ds_read_b128 v[202:205], v197
	ds_read_b128 v[206:209], v197 offset:1024
	ds_read_b128 v[222:225], v197 offset:2048
	ds_read_b128 v[226:229], v197 offset:3072
	ds_read_b128 v[230:233], v197 offset:4096
	ds_read_b128 v[234:237], v197 offset:5120
	ds_read_b128 v[238:241], v197 offset:6144
	ds_read_b128 v[242:245], v197 offset:7168
	global_load_lds_dwordx4 v[174:175], off
	v_lshl_add_u64 v[174:175], s[30:31], 0, v[172:173]
	s_mov_b32 m0, s59
	s_nop 0
	global_load_lds_dwordx4 v[174:175], off
	s_waitcnt vmcnt(8)
	s_waitcnt lgkmcnt(0)
	s_barrier
	v_mfma_f32_16x16x128_f8f6f4 v[160:163], v[2:9], v[202:209], v[160:163]
	s_setprio 1
	v_mfma_f32_16x16x128_f8f6f4 v[156:159], v[10:17], v[202:209], v[156:159]
	v_mfma_f32_16x16x128_f8f6f4 v[148:151], v[10:17], v[222:229], v[148:151]
	v_mfma_f32_16x16x128_f8f6f4 v[152:155], v[2:9], v[222:229], v[152:155]
	v_mfma_f32_16x16x128_f8f6f4 v[144:147], v[2:9], v[230:237], v[144:147]
	v_mfma_f32_16x16x128_f8f6f4 v[140:143], v[10:17], v[230:237], v[140:143]
	v_mfma_f32_16x16x128_f8f6f4 v[132:135], v[10:17], v[238:245], v[132:135]
	v_mfma_f32_16x16x128_f8f6f4 v[136:139], v[2:9], v[238:245], v[136:139]
	s_setprio 2
	s_setprio 1
	v_mfma_f32_16x16x128_f8f6f4 v[128:131], v[18:25], v[202:209], v[128:131]
	v_mfma_f32_16x16x128_f8f6f4 v[124:127], v[26:33], v[202:209], v[124:127]
	v_mfma_f32_16x16x128_f8f6f4 v[116:119], v[26:33], v[222:229], v[116:119]
	v_mfma_f32_16x16x128_f8f6f4 v[120:123], v[18:25], v[222:229], v[120:123]
	v_mfma_f32_16x16x128_f8f6f4 v[112:115], v[18:25], v[230:237], v[112:115]
	v_mfma_f32_16x16x128_f8f6f4 v[108:111], v[26:33], v[230:237], v[108:111]
	v_mfma_f32_16x16x128_f8f6f4 v[100:103], v[26:33], v[238:245], v[100:103]
	v_mfma_f32_16x16x128_f8f6f4 v[104:107], v[18:25], v[238:245], v[104:107]
	s_barrier
	s_setprio 2
	s_mov_b32 m0, s60
	v_lshl_add_u64 v[174:175], s[22:23], 0, v[34:35]
	s_add_u32 s72, s22, 0x20000
	ds_read_b128 v[202:205], v197 offset:16384
	ds_read_b128 v[206:209], v197 offset:17408
	ds_read_b128 v[222:225], v197 offset:18432
	ds_read_b128 v[226:229], v197 offset:19456
	ds_read_b128 v[230:233], v197 offset:20480
	ds_read_b128 v[234:237], v197 offset:21504
	ds_read_b128 v[238:241], v197 offset:22528
	ds_read_b128 v[242:245], v197 offset:23552
	global_load_lds_dwordx4 v[174:175], off
	v_lshl_add_u64 v[190:191], s[22:23], 0, v[164:165]
	s_mov_b32 m0, s61
	s_addc_u32 s73, s23, 0
	global_load_lds_dwordx4 v[190:191], off
	v_lshl_add_u64 v[178:179], s[72:73], 0, v[34:35]
	s_mov_b32 m0, s62
	v_lshl_add_u64 v[192:193], s[36:37], 0, v[168:169]
	global_load_lds_dwordx4 v[178:179], off
	v_lshl_add_u64 v[178:179], s[72:73], 0, v[164:165]
	s_mov_b32 m0, s63
	v_lshl_add_u64 v[194:195], s[36:37], 0, v[166:167]
	global_load_lds_dwordx4 v[178:179], off
	s_mov_b32 m0, s41
	s_nop 0
	global_load_lds_dwordx4 v[192:193], off
	s_mov_b32 m0, s42
	s_nop 0
	global_load_lds_dwordx4 v[194:195], off
	s_waitcnt vmcnt(8)
	s_waitcnt lgkmcnt(0)
	s_barrier
	v_mfma_f32_16x16x128_f8f6f4 v[96:99], v[2:9], v[202:209], v[96:99]
	s_setprio 1
	v_mfma_f32_16x16x128_f8f6f4 v[92:95], v[10:17], v[202:209], v[92:95]
	v_mfma_f32_16x16x128_f8f6f4 v[84:87], v[10:17], v[222:229], v[84:87]
	v_mfma_f32_16x16x128_f8f6f4 v[88:91], v[2:9], v[222:229], v[88:91]
	v_mfma_f32_16x16x128_f8f6f4 v[80:83], v[2:9], v[230:237], v[80:83]
	v_mfma_f32_16x16x128_f8f6f4 v[76:79], v[10:17], v[230:237], v[76:79]
	v_mfma_f32_16x16x128_f8f6f4 v[68:71], v[10:17], v[238:245], v[68:71]
	v_mfma_f32_16x16x128_f8f6f4 v[72:75], v[2:9], v[238:245], v[72:75]
	s_setprio 2
	s_setprio 1
	v_mfma_f32_16x16x128_f8f6f4 v[64:67], v[18:25], v[202:209], v[64:67]
	v_mfma_f32_16x16x128_f8f6f4 v[60:63], v[26:33], v[202:209], v[60:63]
	v_mfma_f32_16x16x128_f8f6f4 v[52:55], v[26:33], v[222:229], v[52:55]
	v_mfma_f32_16x16x128_f8f6f4 v[56:59], v[18:25], v[222:229], v[56:59]
	v_mfma_f32_16x16x128_f8f6f4 v[48:51], v[18:25], v[230:237], v[48:51]
	v_mfma_f32_16x16x128_f8f6f4 v[44:47], v[26:33], v[230:237], v[44:47]
	v_mfma_f32_16x16x128_f8f6f4 v[36:39], v[26:33], v[238:245], v[36:39]
	v_mfma_f32_16x16x128_f8f6f4 v[40:43], v[18:25], v[238:245], v[40:43]
	s_barrier
	s_setprio 2
	ds_read_b128 v[26:29], v200
	ds_read_b128 v[30:33], v200 offset:1024
	ds_read_b128 v[18:21], v200 offset:2048
	ds_read_b128 v[22:25], v200 offset:3072
	ds_read_b128 v[10:13], v201
	ds_read_b128 v[14:17], v201 offset:1024
	ds_read_b128 v[2:5], v201 offset:2048
	ds_read_b128 v[6:9], v201 offset:3072
	s_add_u32 s36, s36, 0x20000
	s_addc_u32 s37, s37, 0
	s_mov_b32 m0, s43
	v_lshl_add_u64 v[178:179], s[36:37], 0, v[168:169]
	ds_read_b128 v[202:205], v197 offset:32768
	ds_read_b128 v[206:209], v197 offset:33792
	ds_read_b128 v[222:225], v197 offset:34816
	ds_read_b128 v[226:229], v197 offset:35840
	ds_read_b128 v[230:233], v197 offset:36864
	ds_read_b128 v[234:237], v197 offset:37888
	ds_read_b128 v[238:241], v197 offset:38912
	ds_read_b128 v[242:245], v197 offset:39936
	global_load_lds_dwordx4 v[178:179], off
	v_lshl_add_u64 v[178:179], s[36:37], 0, v[166:167]
	s_mov_b32 m0, s44
	s_nop 0
	global_load_lds_dwordx4 v[178:179], off
	s_waitcnt vmcnt(8)
	s_waitcnt lgkmcnt(0)
	s_barrier
	v_mfma_f32_16x16x128_f8f6f4 v[160:163], v[26:33], v[202:209], v[160:163]
	s_setprio 1
	v_mfma_f32_16x16x128_f8f6f4 v[156:159], v[18:25], v[202:209], v[156:159]
	v_mfma_f32_16x16x128_f8f6f4 v[148:151], v[18:25], v[222:229], v[148:151]
	v_mfma_f32_16x16x128_f8f6f4 v[152:155], v[26:33], v[222:229], v[152:155]
	v_mfma_f32_16x16x128_f8f6f4 v[144:147], v[26:33], v[230:237], v[144:147]
	v_mfma_f32_16x16x128_f8f6f4 v[140:143], v[18:25], v[230:237], v[140:143]
	v_mfma_f32_16x16x128_f8f6f4 v[132:135], v[18:25], v[238:245], v[132:135]
	v_mfma_f32_16x16x128_f8f6f4 v[136:139], v[26:33], v[238:245], v[136:139]
	s_setprio 2
	s_setprio 1
	v_mfma_f32_16x16x128_f8f6f4 v[128:131], v[10:17], v[202:209], v[128:131]
	v_mfma_f32_16x16x128_f8f6f4 v[124:127], v[2:9], v[202:209], v[124:127]
	v_mfma_f32_16x16x128_f8f6f4 v[116:119], v[2:9], v[222:229], v[116:119]
	v_mfma_f32_16x16x128_f8f6f4 v[120:123], v[10:17], v[222:229], v[120:123]
	v_mfma_f32_16x16x128_f8f6f4 v[112:115], v[10:17], v[230:237], v[112:115]
	v_mfma_f32_16x16x128_f8f6f4 v[108:111], v[2:9], v[230:237], v[108:111]
	v_mfma_f32_16x16x128_f8f6f4 v[100:103], v[2:9], v[238:245], v[100:103]
	v_mfma_f32_16x16x128_f8f6f4 v[104:107], v[10:17], v[238:245], v[104:107]
	s_barrier
	s_setprio 2
	s_mov_b32 m0, s64
	v_lshl_add_u64 v[174:175], v[174:175], 0, s[18:19]
	s_add_u32 s22, s22, 0x20080
	ds_read_b128 v[202:205], v197 offset:49152
	ds_read_b128 v[206:209], v197 offset:50176
	ds_read_b128 v[222:225], v197 offset:51200
	ds_read_b128 v[226:229], v197 offset:52224
	ds_read_b128 v[230:233], v197 offset:53248
	ds_read_b128 v[234:237], v197 offset:54272
	ds_read_b128 v[238:241], v197 offset:55296
	ds_read_b128 v[242:245], v197 offset:56320
	global_load_lds_dwordx4 v[174:175], off
	v_lshl_add_u64 v[174:175], v[190:191], 0, s[18:19]
	s_mov_b32 m0, s65
	s_addc_u32 s23, s23, 0
	global_load_lds_dwordx4 v[174:175], off
	v_lshl_add_u64 v[174:175], s[22:23], 0, v[34:35]
	s_mov_b32 m0, s66
	s_nop 0
	global_load_lds_dwordx4 v[174:175], off
	v_lshl_add_u64 v[174:175], s[22:23], 0, v[164:165]
	s_mov_b32 m0, s67
	s_nop 0
	global_load_lds_dwordx4 v[174:175], off
	v_lshl_add_u64 v[174:175], v[192:193], 0, s[18:19]
	s_mov_b32 m0, s47
	s_nop 0
	global_load_lds_dwordx4 v[174:175], off
	v_lshl_add_u64 v[174:175], v[194:195], 0, s[18:19]
	s_mov_b32 m0, s48
	s_nop 0
	global_load_lds_dwordx4 v[174:175], off
	s_waitcnt vmcnt(8)
	s_waitcnt lgkmcnt(0)
	s_barrier
	v_mfma_f32_16x16x128_f8f6f4 v[96:99], v[26:33], v[202:209], v[96:99]
	s_setprio 1
	v_mfma_f32_16x16x128_f8f6f4 v[92:95], v[18:25], v[202:209], v[92:95]
	v_mfma_f32_16x16x128_f8f6f4 v[84:87], v[18:25], v[222:229], v[84:87]
	v_mfma_f32_16x16x128_f8f6f4 v[88:91], v[26:33], v[222:229], v[88:91]
	v_mfma_f32_16x16x128_f8f6f4 v[80:83], v[26:33], v[230:237], v[80:83]
	v_mfma_f32_16x16x128_f8f6f4 v[76:79], v[18:25], v[230:237], v[76:79]
	v_mfma_f32_16x16x128_f8f6f4 v[68:71], v[18:25], v[238:245], v[68:71]
	v_mfma_f32_16x16x128_f8f6f4 v[72:75], v[26:33], v[238:245], v[72:75]
	s_setprio 2
	s_setprio 1
	v_mfma_f32_16x16x128_f8f6f4 v[64:67], v[10:17], v[202:209], v[64:67]
	v_mfma_f32_16x16x128_f8f6f4 v[60:63], v[2:9], v[202:209], v[60:63]
	v_mfma_f32_16x16x128_f8f6f4 v[52:55], v[2:9], v[222:229], v[52:55]
	v_mfma_f32_16x16x128_f8f6f4 v[56:59], v[10:17], v[222:229], v[56:59]
	v_mfma_f32_16x16x128_f8f6f4 v[48:51], v[10:17], v[230:237], v[48:51]
	v_mfma_f32_16x16x128_f8f6f4 v[44:47], v[2:9], v[230:237], v[44:47]
	v_mfma_f32_16x16x128_f8f6f4 v[36:39], v[2:9], v[238:245], v[36:39]
	v_mfma_f32_16x16x128_f8f6f4 v[40:43], v[10:17], v[238:245], v[40:43]
	s_barrier
	s_setprio 2
	s_add_i32 s70, s70, 2
	s_add_u32 s30, s30, 0x100
	s_addc_u32 s31, s31, 0
	s_add_u32 s68, s68, 0x100
	s_addc_u32 s69, s69, 0
	s_cmp_gt_u32 s70, 5
	s_cbranch_scc0 .LBB0_1087

.LBB0_1160:
	s_add_u32 s22, s30, 0x100
	s_addc_u32 s23, s31, 0
	s_add_i32 s65, 0, 0x10000
	s_cmp_eq_u32 s64, 18
	s_cselect_b32 s41, s58, s23
	s_cselect_b32 s40, s59, s22
	s_cselect_b32 s37, s60, s63
	s_cselect_b32 s36, s61, s62
	s_add_i32 s66, 0, 0x14000
	v_add_u32_e32 v2, s65, v222
	v_add_u32_e32 v6, s66, v222
	ds_read_b128 v[26:29], v2
	ds_read_b128 v[30:33], v2 offset:1024
	ds_read_b128 v[18:21], v2 offset:2048
	ds_read_b128 v[22:25], v2 offset:3072
	ds_read_b128 v[10:13], v6
	ds_read_b128 v[14:17], v6 offset:1024
	ds_read_b128 v[2:5], v6 offset:2048
	ds_read_b128 v[6:9], v6 offset:3072
	v_lshl_add_u64 v[174:175], s[30:31], 0, v[170:171]
	s_add_i32 m0, s43, 0xc000
	ds_read_b128 v[190:193], v223
	ds_read_b128 v[194:197], v223 offset:1024
	ds_read_b128 v[198:201], v223 offset:2048
	ds_read_b128 v[202:205], v223 offset:3072
	ds_read_b128 v[224:227], v223 offset:4096
	ds_read_b128 v[228:231], v223 offset:5120
	ds_read_b128 v[232:235], v223 offset:6144
	ds_read_b128 v[236:239], v223 offset:7168
	global_load_lds_dwordx4 v[174:175], off
	v_lshl_add_u64 v[174:175], s[30:31], 0, v[172:173]
	s_add_i32 m0, s43, 0xe000
	s_nop 0
	global_load_lds_dwordx4 v[174:175], off
	s_waitcnt vmcnt(8)
	s_waitcnt lgkmcnt(0)
	s_barrier
	v_mfma_f32_16x16x128_f8f6f4 v[160:163], v[26:33], v[190:197], v[160:163]
	s_setprio 1
	v_mfma_f32_16x16x128_f8f6f4 v[156:159], v[18:25], v[190:197], v[156:159]
	v_mfma_f32_16x16x128_f8f6f4 v[140:143], v[18:25], v[198:205], v[140:143]
	v_mfma_f32_16x16x128_f8f6f4 v[144:147], v[26:33], v[198:205], v[144:147]
	v_mfma_f32_16x16x128_f8f6f4 v[132:135], v[26:33], v[224:231], v[132:135]
	v_mfma_f32_16x16x128_f8f6f4 v[124:127], v[18:25], v[224:231], v[124:127]
	v_mfma_f32_16x16x128_f8f6f4 v[108:111], v[18:25], v[232:239], v[108:111]
	v_mfma_f32_16x16x128_f8f6f4 v[116:119], v[26:33], v[232:239], v[116:119]
	s_setprio 2
	s_setprio 1
	v_mfma_f32_16x16x128_f8f6f4 v[152:155], v[10:17], v[190:197], v[152:155]
	v_mfma_f32_16x16x128_f8f6f4 v[148:151], v[2:9], v[190:197], v[148:151]
	v_mfma_f32_16x16x128_f8f6f4 v[128:131], v[2:9], v[198:205], v[128:131]
	v_mfma_f32_16x16x128_f8f6f4 v[136:139], v[10:17], v[198:205], v[136:139]
	v_mfma_f32_16x16x128_f8f6f4 v[120:123], v[10:17], v[224:231], v[120:123]
	v_mfma_f32_16x16x128_f8f6f4 v[112:115], v[2:9], v[224:231], v[112:115]
	v_mfma_f32_16x16x128_f8f6f4 v[100:103], v[2:9], v[232:239], v[100:103]
	v_mfma_f32_16x16x128_f8f6f4 v[104:107], v[10:17], v[232:239], v[104:107]
	s_barrier
	s_setprio 2
	s_add_i32 s14, s65, s42
	v_lshl_add_u64 v[174:175], s[36:37], 0, v[34:35]
	s_mov_b32 m0, s14
	ds_read_b128 v[196:199], v223 offset:16384
	ds_read_b128 v[200:203], v223 offset:17408
	ds_read_b128 v[204:207], v223 offset:18432
	ds_read_b128 v[208:211], v223 offset:19456
	ds_read_b128 v[224:227], v223 offset:20480
	ds_read_b128 v[228:231], v223 offset:21504
	ds_read_b128 v[232:235], v223 offset:22528
	ds_read_b128 v[236:239], v223 offset:23552
	global_load_lds_dwordx4 v[174:175], off
	s_add_i32 m0, s14, 0x2000
	s_add_u32 s30, s36, 0x58000
	v_lshl_add_u64 v[190:191], s[36:37], 0, v[164:165]
	s_addc_u32 s31, s37, 0
	s_add_i32 s14, s66, s42
	global_load_lds_dwordx4 v[190:191], off
	v_lshl_add_u64 v[178:179], s[30:31], 0, v[34:35]
	s_mov_b32 m0, s14
	v_lshl_add_u64 v[192:193], s[40:41], 0, v[168:169]
	global_load_lds_dwordx4 v[178:179], off
	v_lshl_add_u64 v[178:179], s[30:31], 0, v[164:165]
	s_add_i32 m0, s14, 0x2000
	v_lshl_add_u64 v[194:195], s[40:41], 0, v[166:167]
	global_load_lds_dwordx4 v[178:179], off
	s_mov_b32 m0, s43
	s_nop 0
	global_load_lds_dwordx4 v[192:193], off
	s_mov_b32 m0, s44
	s_nop 0
	global_load_lds_dwordx4 v[194:195], off
	s_waitcnt vmcnt(8)
	s_waitcnt lgkmcnt(0)
	s_barrier
	v_mfma_f32_16x16x128_f8f6f4 v[96:99], v[26:33], v[196:203], v[96:99]
	s_setprio 1
	v_mfma_f32_16x16x128_f8f6f4 v[92:95], v[18:25], v[196:203], v[92:95]
	v_mfma_f32_16x16x128_f8f6f4 v[76:79], v[18:25], v[204:211], v[76:79]
	v_mfma_f32_16x16x128_f8f6f4 v[84:87], v[26:33], v[204:211], v[84:87]
	v_mfma_f32_16x16x128_f8f6f4 v[68:71], v[26:33], v[224:231], v[68:71]
	v_mfma_f32_16x16x128_f8f6f4 v[60:63], v[18:25], v[224:231], v[60:63]
	v_mfma_f32_16x16x128_f8f6f4 v[44:47], v[18:25], v[232:239], v[44:47]
	v_mfma_f32_16x16x128_f8f6f4 v[52:55], v[26:33], v[232:239], v[52:55]
	s_setprio 2
	s_setprio 1
	v_mfma_f32_16x16x128_f8f6f4 v[88:91], v[10:17], v[196:203], v[88:91]
	v_mfma_f32_16x16x128_f8f6f4 v[80:83], v[2:9], v[196:203], v[80:83]
	v_mfma_f32_16x16x128_f8f6f4 v[64:67], v[2:9], v[204:211], v[64:67]
	v_mfma_f32_16x16x128_f8f6f4 v[72:75], v[10:17], v[204:211], v[72:75]
	v_mfma_f32_16x16x128_f8f6f4 v[56:59], v[10:17], v[224:231], v[56:59]
	v_mfma_f32_16x16x128_f8f6f4 v[48:51], v[2:9], v[224:231], v[48:51]
	v_mfma_f32_16x16x128_f8f6f4 v[36:39], v[2:9], v[232:239], v[36:39]
	v_mfma_f32_16x16x128_f8f6f4 v[40:43], v[10:17], v[232:239], v[40:43]
	s_barrier
	s_setprio 2
	s_add_i32 s14, 0, 0x18000
	s_add_i32 s65, 0, 0x1c000
	v_add_u32_e32 v14, s14, v222
	v_add_u32_e32 v30, s65, v222
	ds_read_b128 v[2:5], v14
	ds_read_b128 v[6:9], v14 offset:1024
	ds_read_b128 v[10:13], v14 offset:2048
	ds_read_b128 v[14:17], v14 offset:3072
	ds_read_b128 v[18:21], v30
	ds_read_b128 v[22:25], v30 offset:1024
	ds_read_b128 v[26:29], v30 offset:2048
	ds_read_b128 v[30:33], v30 offset:3072
	s_add_u32 s30, s40, 0x58000
	s_addc_u32 s31, s41, 0
	s_mov_b32 m0, s45
	v_lshl_add_u64 v[178:179], s[30:31], 0, v[168:169]
	ds_read_b128 v[196:199], v223 offset:32768
	ds_read_b128 v[200:203], v223 offset:33792
	ds_read_b128 v[204:207], v223 offset:34816
	ds_read_b128 v[208:211], v223 offset:35840
	ds_read_b128 v[224:227], v223 offset:36864
	ds_read_b128 v[228:231], v223 offset:37888
	ds_read_b128 v[232:235], v223 offset:38912
	ds_read_b128 v[236:239], v223 offset:39936
	global_load_lds_dwordx4 v[178:179], off
	v_lshl_add_u64 v[178:179], s[30:31], 0, v[166:167]
	s_mov_b32 m0, s46
	s_nop 0
	global_load_lds_dwordx4 v[178:179], off
	s_waitcnt vmcnt(8)
	s_waitcnt lgkmcnt(0)
	s_barrier
	v_mfma_f32_16x16x128_f8f6f4 v[160:163], v[2:9], v[196:203], v[160:163]
	s_setprio 1
	v_mfma_f32_16x16x128_f8f6f4 v[156:159], v[10:17], v[196:203], v[156:159]
	v_mfma_f32_16x16x128_f8f6f4 v[140:143], v[10:17], v[204:211], v[140:143]
	v_mfma_f32_16x16x128_f8f6f4 v[144:147], v[2:9], v[204:211], v[144:147]
	v_mfma_f32_16x16x128_f8f6f4 v[132:135], v[2:9], v[224:231], v[132:135]
	v_mfma_f32_16x16x128_f8f6f4 v[124:127], v[10:17], v[224:231], v[124:127]
	v_mfma_f32_16x16x128_f8f6f4 v[108:111], v[10:17], v[232:239], v[108:111]
	v_mfma_f32_16x16x128_f8f6f4 v[116:119], v[2:9], v[232:239], v[116:119]
	s_setprio 2
	s_setprio 1
	v_mfma_f32_16x16x128_f8f6f4 v[152:155], v[18:25], v[196:203], v[152:155]
	v_mfma_f32_16x16x128_f8f6f4 v[148:151], v[26:33], v[196:203], v[148:151]
	v_mfma_f32_16x16x128_f8f6f4 v[128:131], v[26:33], v[204:211], v[128:131]
	v_mfma_f32_16x16x128_f8f6f4 v[136:139], v[18:25], v[204:211], v[136:139]
	v_mfma_f32_16x16x128_f8f6f4 v[120:123], v[18:25], v[224:231], v[120:123]
	v_mfma_f32_16x16x128_f8f6f4 v[112:115], v[26:33], v[224:231], v[112:115]
	v_mfma_f32_16x16x128_f8f6f4 v[100:103], v[26:33], v[232:239], v[100:103]
	v_mfma_f32_16x16x128_f8f6f4 v[104:107], v[18:25], v[232:239], v[104:107]
	s_barrier
	s_setprio 2
	s_add_i32 s14, s14, s42
	v_lshl_add_u64 v[174:175], v[174:175], 0, s[18:19]
	s_mov_b32 m0, s14
	ds_read_b128 v[196:199], v223 offset:49152
	ds_read_b128 v[200:203], v223 offset:50176
	ds_read_b128 v[204:207], v223 offset:51200
	ds_read_b128 v[208:211], v223 offset:52224
	ds_read_b128 v[224:227], v223 offset:53248
	ds_read_b128 v[228:231], v223 offset:54272
	ds_read_b128 v[232:235], v223 offset:55296
	ds_read_b128 v[236:239], v223 offset:56320
	global_load_lds_dwordx4 v[174:175], off
	s_add_i32 m0, s14, 0x2000
	s_add_u32 s30, s36, 0x58080
	v_lshl_add_u64 v[174:175], v[190:191], 0, s[18:19]
	s_addc_u32 s31, s37, 0
	s_add_i32 s14, s65, s42
	global_load_lds_dwordx4 v[174:175], off
	v_lshl_add_u64 v[174:175], s[30:31], 0, v[34:35]
	s_mov_b32 m0, s14
	s_nop 0
	global_load_lds_dwordx4 v[174:175], off
	v_lshl_add_u64 v[174:175], s[30:31], 0, v[164:165]
	s_add_i32 m0, s14, 0x2000
	s_nop 0
	global_load_lds_dwordx4 v[174:175], off
	v_lshl_add_u64 v[174:175], v[192:193], 0, s[18:19]
	s_mov_b32 m0, s51
	s_nop 0
	global_load_lds_dwordx4 v[174:175], off
	v_lshl_add_u64 v[174:175], v[194:195], 0, s[18:19]
	s_mov_b32 m0, s52
	s_nop 0
	global_load_lds_dwordx4 v[174:175], off
	s_waitcnt vmcnt(8)
	s_waitcnt lgkmcnt(0)
	s_barrier
	v_mfma_f32_16x16x128_f8f6f4 v[96:99], v[2:9], v[196:203], v[96:99]
	s_setprio 1
	v_mfma_f32_16x16x128_f8f6f4 v[92:95], v[10:17], v[196:203], v[92:95]
	v_mfma_f32_16x16x128_f8f6f4 v[76:79], v[10:17], v[204:211], v[76:79]
	v_mfma_f32_16x16x128_f8f6f4 v[84:87], v[2:9], v[204:211], v[84:87]
	v_mfma_f32_16x16x128_f8f6f4 v[68:71], v[2:9], v[224:231], v[68:71]
	v_mfma_f32_16x16x128_f8f6f4 v[60:63], v[10:17], v[224:231], v[60:63]
	v_mfma_f32_16x16x128_f8f6f4 v[44:47], v[10:17], v[232:239], v[44:47]
	v_mfma_f32_16x16x128_f8f6f4 v[52:55], v[2:9], v[232:239], v[52:55]
	s_setprio 2
	s_setprio 1
	v_mfma_f32_16x16x128_f8f6f4 v[88:91], v[18:25], v[196:203], v[88:91]
	v_mfma_f32_16x16x128_f8f6f4 v[80:83], v[26:33], v[196:203], v[80:83]
	v_mfma_f32_16x16x128_f8f6f4 v[64:67], v[26:33], v[204:211], v[64:67]
	v_mfma_f32_16x16x128_f8f6f4 v[72:75], v[18:25], v[204:211], v[72:75]
	v_mfma_f32_16x16x128_f8f6f4 v[56:59], v[18:25], v[224:231], v[56:59]
	v_mfma_f32_16x16x128_f8f6f4 v[48:51], v[26:33], v[224:231], v[48:51]
	v_mfma_f32_16x16x128_f8f6f4 v[36:39], v[26:33], v[232:239], v[36:39]
	v_mfma_f32_16x16x128_f8f6f4 v[40:43], v[18:25], v[232:239], v[40:43]
	s_barrier
	s_setprio 2
	s_add_i32 s64, s64, 2
	s_add_u32 s62, s62, 0x100
	s_addc_u32 s63, s63, 0
	s_cmp_gt_u32 s64, 19
	s_mov_b64 s[30:31], s[22:23]
	s_cbranch_scc0 .LBB0_1160
	s_and_b64 vcc, exec, s[8:9]
	s_mov_b32 s58, 0x19b00000
	v_readlane_b32 s59, v255, 10
	s_mov_b32 s60, 0xff61b1e6
	s_mov_b64 s[62:63], 0x800
	s_cbranch_vccz .LBB0_1163
	s_barrier
